# s18p + cross-row reductions via v_permlane16/32_swap instead of ds_swizzle(SWAP,16)/ds_bpermute(lane^32): norm1 L0 gate keep/send steps, wave sums, attention softmax row max (L0+L1), GEMM row-ss parti
# baseline (speedup 1.0000x reference)
; DI float wave_sum(float v) { v += shx<1>(v); v += shx<2>(v); v += shx<4>(v); v += shx<8>(v); v += shx<16>(v); v += shx<32>(v); return v; }
; template <int MODE, bool SB  > DI void norm_phase(const Params& P, const Frame& F, int L, const void* src_, const float* gain, bool combine) {
;     ...
;         { const int rnx = (row + NWAVES < r_hi) ? row + NWAVES : row;
; #pragma unroll
;           for (int j = 0; j < 8; ++j) { if constexpr (SB) vb[j] = *(const u32x2*)(srcb + (size_t)rnx * D + 4 * F.lane + 256 * j); else vn[j] = *(const f32x4*)(src + (size_t)rnx * D + 4 * F.lane + 256 * j); } }
;     ...
;         float ss = 0.f;
; #pragma unroll
;         for (int j = 0; j < 8; ++j) ss += (v[j][0] * v[j][0] + v[j][1] * v[j][1]) + (v[j][2] * v[j][2] + v[j][3] * v[j][3]);
;         const float rstd = 1.0f / sqrtf(wave_sum(ss) * (1.0f / D) + EPS);
.LBB0_83:
	s_waitcnt vmcnt(1)
	v_mov_b64_e32 v[90:91], v[38:39]
	s_waitcnt vmcnt(0)
	v_mov_b64_e32 v[94:95], v[34:35]
	v_mov_b64_e32 v[88:89], v[36:37]
	v_mov_b64_e32 v[92:93], v[32:33]
	v_mov_b32_e32 v114, v93
	v_mov_b32_e32 v115, v89
	v_mov_b32_e32 v112, v92
	v_mov_b32_e32 v113, v88
	v_pk_mul_f32 v[114:115], v[114:115], v[114:115]
	v_mov_b32_e32 v188, v95
	v_mov_b32_e32 v189, v91
	v_mov_b64_e32 v[86:87], v[42:43]
	v_pk_fma_f32 v[112:113], v[112:113], v[112:113], v[114:115]
	v_mov_b32_e32 v114, v94
	v_mov_b32_e32 v115, v90
	v_pk_mul_f32 v[188:189], v[188:189], v[188:189]
	v_mov_b64_e32 v[84:85], v[40:41]
	v_pk_fma_f32 v[114:115], v[114:115], v[114:115], v[188:189]
	v_pk_mul_f32 v[188:189], v[84:85], v[84:85]
	v_pk_add_f32 v[112:113], v[112:113], v[114:115]
	v_pk_mul_f32 v[114:115], v[86:87], v[86:87]
	v_mov_b64_e32 v[78:79], v[50:51]
	v_pk_mov_b32 v[190:191], v[188:189], v[114:115] op_sel:[1,0]
	v_mov_b32_e32 v189, v115
	v_mov_b64_e32 v[76:77], v[48:49]
	v_pk_add_f32 v[114:115], v[190:191], v[188:189]
	v_mov_b64_e32 v[82:83], v[46:47]
	v_mul_f32_e32 v111, v76, v76
	v_mul_f32_e32 v188, v77, v77
	v_pk_add_f32 v[112:113], v[112:113], v[112:113] op_sel:[0,1] op_sel_hi:[1,0]
	v_pk_add_f32 v[114:115], v[114:115], v[114:115] op_sel:[0,1] op_sel_hi:[1,0]
	v_mov_b64_e32 v[80:81], v[44:45]
	v_mov_b32_e32 v113, v111
	v_mov_b32_e32 v115, v188
	v_pk_add_f32 v[112:113], v[112:113], v[114:115]
	v_mul_f32_e32 v114, v81, v81
	v_mul_f32_e32 v189, v78, v78
	v_pk_fma_f32 v[114:115], v[80:81], v[80:81], v[114:115] op_sel_hi:[1,1,0]
	v_mul_f32_e32 v188, v83, v83
	v_mul_f32_e32 v190, v79, v79
	v_mov_b32_e32 v115, v189
	v_pk_fma_f32 v[188:189], v[82:83], v[82:83], v[188:189] op_sel_hi:[1,1,0]
	v_mov_b64_e32 v[74:75], v[54:55]
	v_mov_b32_e32 v189, v190
	v_mov_b64_e32 v[72:73], v[52:53]
	v_pk_add_f32 v[114:115], v[114:115], v[188:189]
	v_pk_mul_f32 v[188:189], v[72:73], v[72:73]
	v_pk_add_f32 v[112:113], v[112:113], v[114:115]
	v_pk_mul_f32 v[114:115], v[74:75], v[74:75]
	v_mov_b64_e32 v[66:67], v[62:63]
	v_pk_mov_b32 v[190:191], v[188:189], v[114:115] op_sel:[1,0]
	v_mov_b32_e32 v189, v115
	v_mov_b64_e32 v[64:65], v[60:61]
	v_pk_add_f32 v[114:115], v[190:191], v[188:189]
	v_mov_b64_e32 v[70:71], v[58:59]
	v_mul_f32_e32 v111, v64, v64
	v_mul_f32_e32 v188, v65, v65
	v_pk_add_f32 v[112:113], v[112:113], v[112:113] op_sel:[0,1] op_sel_hi:[1,0]
	v_pk_add_f32 v[114:115], v[114:115], v[114:115] op_sel:[0,1] op_sel_hi:[1,0]
	v_mov_b64_e32 v[68:69], v[56:57]
	v_mov_b32_e32 v113, v111
	v_mov_b32_e32 v115, v188
	v_pk_add_f32 v[112:113], v[112:113], v[114:115]
	v_mul_f32_e32 v114, v69, v69
	v_mul_f32_e32 v189, v66, v66
	v_pk_fma_f32 v[114:115], v[68:69], v[68:69], v[114:115] op_sel_hi:[1,1,0]
	v_mul_f32_e32 v188, v71, v71
	v_mul_f32_e32 v190, v67, v67
	v_mov_b32_e32 v115, v189
	v_pk_fma_f32 v[188:189], v[70:71], v[70:71], v[188:189] op_sel_hi:[1,1,0]
	s_mov_b32 s20, s0
	v_mov_b32_e32 v189, v190
	v_pk_add_f32 v[114:115], v[114:115], v[188:189]
	s_add_i32 s0, s0, 8
	v_pk_add_f32 v[112:113], v[112:113], v[114:115]
	s_cmp_ge_i32 s0, s3
	v_add_f32_e32 v111, v112, v113
	s_cselect_b64 s[22:23], -1, 0
	s_cmp_lt_i32 s0, s3
	v_add_f32_dpp v111, v111, v111 quad_perm:[1,0,3,2] row_mask:0xf bank_mask:0xf bound_ctrl:1
	s_cselect_b32 s20, s0, s20
	s_ashr_i32 s21, s20, 31
	v_add_f32_dpp v111, v111, v111 quad_perm:[2,3,0,1] row_mask:0xf bank_mask:0xf bound_ctrl:1
	ds_swizzle_b32 v112, v111 offset:swizzle(SWAP,4)
	s_lshl_b64 s[20:21], s[20:21], 13
	v_lshl_add_u64 v[48:49], v[96:97], 0, s[20:21]
	v_add_co_u32_e32 v60, vcc, s30, v48
	s_waitcnt lgkmcnt(0)
	v_add_f32_e32 v111, v111, v112
	ds_swizzle_b32 v112, v111 offset:swizzle(SWAP,8)
	v_addc_co_u32_e32 v61, vcc, 0, v49, vcc
	s_mov_b32 s20, 0xf800000
	global_load_dwordx4 v[32:35], v[48:49], off
	global_load_dwordx4 v[36:39], v[48:49], off offset:1024
	global_load_dwordx4 v[40:43], v[48:49], off offset:2048
	global_load_dwordx4 v[44:47], v[48:49], off offset:3072
	s_waitcnt lgkmcnt(0)
	v_add_f32_e32 v111, v111, v112
	v_mov_b32_e32 v112, v111
	global_load_dwordx4 v[48:51], v[60:61], off
	global_load_dwordx4 v[52:55], v[60:61], off offset:1024
	global_load_dwordx4 v[56:59], v[60:61], off offset:2048
	s_nop 0
	global_load_dwordx4 v[60:63], v[60:61], off offset:3072
	s_waitcnt lgkmcnt(0)
	s_nop 1
	v_permlane16_swap_b32_e32 v111, v112
	v_add_f32_e32 v111, v111, v112
	v_mov_b32_e32 v112, v111
	s_waitcnt lgkmcnt(0)
; #define LAS __attribute__((address_space(3)))
; DI unsigned pk2(float lo, float hi) { const f32x2 v = {lo, hi}; return __builtin_bit_cast(unsigned, __builtin_convertvector(v, bf16x2_t)); }
; DI unsigned pk4_fp8(float a, float b, float c, float d) { unsigned w = 0u; w = __builtin_amdgcn_cvt_pk_fp8_f32(a, b, w, false); w = __builtin_amdgcn_cvt_pk_fp8_f32(c, d, w, true); return w; }
; DI float wave_sum(float v) { v += shx<1>(v); v += shx<2>(v); v += shx<4>(v); v += shx<8>(v); v += shx<16>(v); v += shx<32>(v); return v; }
; template <int MODE, bool SB  > DI void norm_phase(const Params& P, const Frame& F, int L, const void* src_, const float* gain, bool combine) {
;     ...
;         const float rstd = 1.0f / sqrtf(wave_sum(ss) * (1.0f / D) + EPS);
; #pragma unroll
;         for (int j = 0; j < 8; ++j) v[j] = v[j] * rstd * g[j];
;         if (MODE == 4) {
; #pragma unroll
;             for (int j = 0; j < 8; ++j) *(f32x4*)(P.out + (size_t)row * D + 4 * F.lane + 256 * j) = v[j];
;         } else if (MODE == 0 || MODE == 2 || (MODE == 3 && L == 1)) {
;             unsigned* o4 = (unsigned*)((unsigned char*)HN + (size_t)row * D) + F.lane; const float hs = (float)(1 << LS_HN);
; #pragma unroll
;             for (int j = 0; j < 8; ++j) o4[64 * j] = pk4_fp8(v[j][0] * hs, v[j][1] * hs, v[j][2] * hs, v[j][3] * hs);
;         } else {
;             unsigned long long* o8 = (unsigned long long*)(HN + (size_t)row * D) + F.lane;
; #pragma unroll
;             for (int j = 0; j < 8; ++j) o8[64 * j] = (unsigned long long)pk2(v[j][0], v[j][1]) | ((unsigned long long)pk2(v[j][2], v[j][3]) << 32);
;         }
;         if (MODE == 1) {
;             float s[16];
; #pragma unroll
;             for (int q = 0; q < 16; ++q) { float t = 0.f;
; #pragma unroll
;                 for (int j = 0; j < 8; ++j) { const f32x4 w = *(const LAS f32x4*)(F.lds + (size_t)(q * D + 256 * j + 4 * F.lane) * 4); t += (v[j][0] * w[0] + v[j][1] * w[1]) + (v[j][2] * w[2] + v[j][3] * w[3]); }
;                 s[q] = t; if ((q & 3) == 3) asm volatile("" ::: "memory"); }
	s_nop 1
	v_permlane32_swap_b32_e32 v111, v112
	v_add_f32_e32 v111, v111, v112
	v_fmamk_f32 v111, v111, 0x3a000000, v182
	v_cmp_gt_f32_e32 vcc, s20, v111
	v_mul_f32_e32 v112, 0x4f800000, v111
	s_nop 0
	v_cndmask_b32_e32 v111, v111, v112, vcc
	v_sqrt_f32_e32 v112, v111
	s_nop 0
	v_add_u32_e32 v113, -1, v112
	v_fma_f32 v114, -v113, v112, v111
	v_cmp_ge_f32_e64 s[20:21], 0, v114
	v_add_u32_e32 v114, 1, v112
	s_nop 0
	v_cndmask_b32_e64 v113, v112, v113, s[20:21]
	v_fma_f32 v112, -v114, v112, v111
	v_cmp_lt_f32_e64 s[20:21], 0, v112
	s_nop 1
	v_cndmask_b32_e64 v112, v113, v114, s[20:21]
	v_mul_f32_e32 v113, 0x37800000, v112
	v_cndmask_b32_e32 v112, v112, v113, vcc
	v_cmp_class_f32_e32 vcc, v111, v183
	s_nop 1
	v_cndmask_b32_e32 v111, v112, v111, vcc
	v_div_scale_f32 v112, s[20:21], v111, v111, 1.0
	v_rcp_f32_e32 v113, v112
	s_mov_b32 s20, 0x3d600000
	v_fma_f32 v114, -v112, v113, 1.0
	v_fmac_f32_e32 v113, v114, v113
	v_div_scale_f32 v114, vcc, 1.0, v111, 1.0
	v_mul_f32_e32 v115, v114, v113
	v_fma_f32 v188, -v112, v115, v114
	v_fmac_f32_e32 v115, v188, v113
	v_fma_f32 v112, -v112, v115, v114
	v_div_fmas_f32 v112, v112, v113, v115
	v_div_fixup_f32 v188, v112, v111, 1.0
	v_pk_mul_f32 v[94:95], v[94:95], v[188:189] op_sel_hi:[1,0]
	v_pk_mul_f32 v[88:89], v[88:89], v[188:189] op_sel_hi:[1,0]
	v_pk_mul_f32 v[86:87], v[86:87], v[188:189] op_sel_hi:[1,0]
	v_pk_mul_f32 v[80:81], v[80:81], v[188:189] op_sel_hi:[1,0]
	v_pk_mul_f32 v[78:79], v[78:79], v[188:189] op_sel_hi:[1,0]
	v_pk_mul_f32 v[72:73], v[72:73], v[188:189] op_sel_hi:[1,0]
	v_pk_mul_f32 v[70:71], v[70:71], v[188:189] op_sel_hi:[1,0]
	v_pk_mul_f32 v[64:65], v[64:65], v[188:189] op_sel_hi:[1,0]
	v_pk_mul_f32 v[92:93], v[92:93], v[188:189] op_sel_hi:[1,0]
	v_pk_mul_f32 v[112:113], v[2:3], v[94:95]
	v_pk_mul_f32 v[94:95], v[4:5], v[88:89]
	v_pk_mul_f32 v[88:89], v[10:11], v[86:87]
	v_pk_mul_f32 v[86:87], v[12:13], v[80:81]
	v_pk_mul_f32 v[80:81], v[18:19], v[78:79]
	v_pk_mul_f32 v[78:79], v[20:21], v[72:73]
	v_pk_mul_f32 v[72:73], v[26:27], v[70:71]
	v_pk_mul_f32 v[70:71], v[28:29], v[64:65]
	v_lshl_add_u64 v[64:65], s[54:55], 0, v[108:109]
	v_pk_mul_f32 v[114:115], v[0:1], v[92:93]
	v_pk_mul_f32 v[90:91], v[90:91], v[188:189] op_sel_hi:[1,0]
	v_pk_mul_f32 v[84:85], v[84:85], v[188:189] op_sel_hi:[1,0]
	v_pk_mul_f32 v[82:83], v[82:83], v[188:189] op_sel_hi:[1,0]
	v_pk_mul_f32 v[76:77], v[76:77], v[188:189] op_sel_hi:[1,0]
	v_pk_mul_f32 v[74:75], v[74:75], v[188:189] op_sel_hi:[1,0]
	v_pk_mul_f32 v[68:69], v[68:69], v[188:189] op_sel_hi:[1,0]
	v_pk_mul_f32 v[66:67], v[66:67], v[188:189] op_sel_hi:[1,0]
	v_add_co_u32_e32 v64, vcc, s20, v64
	v_pk_mul_f32 v[92:93], v[6:7], v[90:91]
	v_pk_mul_f32 v[90:91], v[8:9], v[84:85]
	v_pk_mul_f32 v[84:85], v[14:15], v[82:83]
	v_pk_mul_f32 v[82:83], v[16:17], v[76:77]
	v_pk_mul_f32 v[76:77], v[22:23], v[74:75]
	v_pk_mul_f32 v[74:75], v[24:25], v[68:69]
	v_pk_mul_f32 v[68:69], v[30:31], v[66:67]
	v_cvt_pk_bf16_f32 v66, v114, v115
	v_cvt_pk_bf16_f32 v67, v112, v113
	v_addc_co_u32_e32 v65, vcc, 0, v65, vcc
	global_store_dwordx2 v[64:65], v[66:67], off
	v_cvt_pk_bf16_f32 v66, v94, v95
	v_cvt_pk_bf16_f32 v67, v92, v93
	global_store_dwordx2 v[64:65], v[66:67], off offset:512
	v_cvt_pk_bf16_f32 v66, v90, v91
	v_cvt_pk_bf16_f32 v67, v88, v89
	global_store_dwordx2 v[64:65], v[66:67], off offset:1024
	v_cvt_pk_bf16_f32 v66, v86, v87
	v_cvt_pk_bf16_f32 v67, v84, v85
	global_store_dwordx2 v[64:65], v[66:67], off offset:1536
	v_cvt_pk_bf16_f32 v66, v82, v83
	v_cvt_pk_bf16_f32 v67, v80, v81
	global_store_dwordx2 v[64:65], v[66:67], off offset:2048
	v_cvt_pk_bf16_f32 v66, v78, v79
	v_cvt_pk_bf16_f32 v67, v76, v77
	global_store_dwordx2 v[64:65], v[66:67], off offset:2560
	v_cvt_pk_bf16_f32 v66, v74, v75
	v_cvt_pk_bf16_f32 v67, v72, v73
	global_store_dwordx2 v[64:65], v[66:67], off offset:3072
	v_cvt_pk_bf16_f32 v66, v70, v71
	v_cvt_pk_bf16_f32 v67, v68, v69
	global_store_dwordx2 v[64:65], v[66:67], off offset:3584
	ds_read_b128 v[216:219], v117
	ds_read_b128 v[220:223], v117 offset:1024
	ds_read_b128 v[224:227], v117 offset:2048
	ds_read_b128 v[228:231], v117 offset:3072
	ds_read_b128 v[232:235], v117 offset:4096
	ds_read_b128 v[236:239], v117 offset:5120
	ds_read_b128 v[240:243], v117 offset:6144
	ds_read_b128 v[248:251], v117 offset:7168
	s_waitcnt lgkmcnt(7)
	v_mul_f32_e32 v217, v217, v115
	v_fmac_f32_e32 v217, v216, v114
	v_mul_f32_e32 v216, v219, v113
	v_fmac_f32_e32 v216, v218, v112
	v_add_f32_e32 v216, v217, v216
	v_add_f32_e32 v111, 0, v216
	ds_read_b128 v[216:219], v117 offset:8192
	s_waitcnt lgkmcnt(7)
	v_mul_f32_e32 v221, v95, v221
	v_fmac_f32_e32 v221, v94, v220
	v_mul_f32_e32 v220, v93, v223
	v_fmac_f32_e32 v220, v92, v222
	v_add_f32_e32 v220, v221, v220
	v_add_f32_e32 v111, v220, v111
	ds_read_b128 v[220:223], v117 offset:9216
	s_waitcnt lgkmcnt(7)
	v_mul_f32_e32 v225, v91, v225
	v_fmac_f32_e32 v225, v90, v224
	v_mul_f32_e32 v224, v89, v227
	v_fmac_f32_e32 v224, v88, v226
	v_add_f32_e32 v224, v225, v224
	v_add_f32_e32 v111, v224, v111
	ds_read_b128 v[224:227], v117 offset:10240
	s_waitcnt lgkmcnt(7)
	v_mul_f32_e32 v229, v87, v229
	v_fmac_f32_e32 v229, v86, v228
	v_mul_f32_e32 v228, v85, v231
	v_fmac_f32_e32 v228, v84, v230
	v_add_f32_e32 v228, v229, v228
	v_add_f32_e32 v111, v228, v111
	ds_read_b128 v[228:231], v117 offset:11264
	s_waitcnt lgkmcnt(7)
	v_mul_f32_e32 v233, v83, v233
	v_fmac_f32_e32 v233, v82, v232
	v_mul_f32_e32 v232, v81, v235
	v_fmac_f32_e32 v232, v80, v234
	v_add_f32_e32 v232, v233, v232
	v_add_f32_e32 v111, v232, v111
	ds_read_b128 v[232:235], v117 offset:12288
	s_waitcnt lgkmcnt(7)
; #define LAS __attribute__((address_space(3)))
; template <int MODE, bool SB  > DI void norm_phase(const Params& P, const Frame& F, int L, const void* src_, const float* gain, bool combine) {
;     ...
;             for (int q = 0; q < 16; ++q) { float t = 0.f;
; #pragma unroll
;                 for (int j = 0; j < 8; ++j) { const f32x4 w = *(const LAS f32x4*)(F.lds + (size_t)(q * D + 256 * j + 4 * F.lane) * 4); t += (v[j][0] * w[0] + v[j][1] * w[1]) + (v[j][2] * w[2] + v[j][3] * w[3]); }
;                 s[q] = t; if ((q & 3) == 3) asm volatile("" ::: "memory"); }
	v_mul_f32_e32 v237, v79, v237
	v_fmac_f32_e32 v237, v78, v236
	v_mul_f32_e32 v236, v77, v239
	v_fmac_f32_e32 v236, v76, v238
	v_add_f32_e32 v236, v237, v236
	v_add_f32_e32 v111, v236, v111
	ds_read_b128 v[236:239], v117 offset:13312
	s_waitcnt lgkmcnt(7)
	v_mul_f32_e32 v241, v75, v241
	v_fmac_f32_e32 v241, v74, v240
	v_mul_f32_e32 v240, v73, v243
	v_fmac_f32_e32 v240, v72, v242
	v_add_f32_e32 v240, v241, v240
	v_add_f32_e32 v111, v240, v111
	ds_read_b128 v[240:243], v117 offset:14336
	s_waitcnt lgkmcnt(7)
	v_mul_f32_e32 v249, v71, v249
	v_fmac_f32_e32 v249, v70, v248
	v_mul_f32_e32 v248, v69, v251
	v_fmac_f32_e32 v248, v68, v250
	v_add_f32_e32 v248, v249, v248
	v_add_f32_e32 v111, v248, v111
	ds_read_b128 v[248:251], v117 offset:15360
	s_waitcnt lgkmcnt(7)
	v_mul_f32_e32 v217, v115, v217
	v_fmac_f32_e32 v217, v114, v216
	v_mul_f32_e32 v216, v113, v219
	v_fmac_f32_e32 v216, v112, v218
	v_add_f32_e32 v216, v217, v216
	v_add_f32_e32 v188, 0, v216
	ds_read_b128 v[216:219], v117 offset:16384
	s_waitcnt lgkmcnt(7)
	v_mul_f32_e32 v221, v95, v221
	v_fmac_f32_e32 v221, v94, v220
	v_mul_f32_e32 v220, v93, v223
	v_fmac_f32_e32 v220, v92, v222
	v_add_f32_e32 v220, v221, v220
	v_add_f32_e32 v188, v188, v220
	ds_read_b128 v[220:223], v117 offset:17408
	s_waitcnt lgkmcnt(7)
	v_mul_f32_e32 v225, v91, v225
	v_fmac_f32_e32 v225, v90, v224
	v_mul_f32_e32 v224, v89, v227
	v_fmac_f32_e32 v224, v88, v226
	v_add_f32_e32 v224, v225, v224
	v_add_f32_e32 v188, v188, v224
	ds_read_b128 v[224:227], v117 offset:18432
	s_waitcnt lgkmcnt(7)
	v_mul_f32_e32 v229, v87, v229
	v_fmac_f32_e32 v229, v86, v228
	v_mul_f32_e32 v228, v85, v231
	v_fmac_f32_e32 v228, v84, v230
	v_add_f32_e32 v228, v229, v228
	v_add_f32_e32 v188, v188, v228
	ds_read_b128 v[228:231], v117 offset:19456
	s_waitcnt lgkmcnt(7)
	v_mul_f32_e32 v233, v83, v233
	v_fmac_f32_e32 v233, v82, v232
	v_mul_f32_e32 v232, v81, v235
	v_fmac_f32_e32 v232, v80, v234
	v_add_f32_e32 v232, v233, v232
	v_add_f32_e32 v188, v188, v232
	ds_read_b128 v[232:235], v117 offset:20480
	s_waitcnt lgkmcnt(7)
	v_mul_f32_e32 v237, v79, v237
	v_fmac_f32_e32 v237, v78, v236
	v_mul_f32_e32 v236, v77, v239
	v_fmac_f32_e32 v236, v76, v238
	v_add_f32_e32 v236, v237, v236
	v_add_f32_e32 v188, v188, v236
	ds_read_b128 v[236:239], v117 offset:21504
	s_waitcnt lgkmcnt(7)
	v_mul_f32_e32 v241, v75, v241
	v_fmac_f32_e32 v241, v74, v240
	v_mul_f32_e32 v240, v73, v243
	v_fmac_f32_e32 v240, v72, v242
	v_add_f32_e32 v240, v241, v240
	v_add_f32_e32 v188, v188, v240
	ds_read_b128 v[240:243], v117 offset:22528
	s_waitcnt lgkmcnt(7)
	v_mul_f32_e32 v249, v71, v249
	v_fmac_f32_e32 v249, v70, v248
	v_mul_f32_e32 v248, v69, v251
	v_fmac_f32_e32 v248, v68, v250
	v_add_f32_e32 v248, v249, v248
	v_add_f32_e32 v188, v188, v248
	ds_read_b128 v[248:251], v117 offset:23552
	s_waitcnt lgkmcnt(7)
	v_mul_f32_e32 v217, v115, v217
	v_fmac_f32_e32 v217, v114, v216
	v_mul_f32_e32 v216, v113, v219
	v_fmac_f32_e32 v216, v112, v218
	v_add_f32_e32 v216, v217, v216
	v_add_f32_e32 v189, 0, v216
	ds_read_b128 v[216:219], v117 offset:24576
	s_waitcnt lgkmcnt(7)
	v_mul_f32_e32 v221, v95, v221
	v_fmac_f32_e32 v221, v94, v220
	v_mul_f32_e32 v220, v93, v223
	v_fmac_f32_e32 v220, v92, v222
	v_add_f32_e32 v220, v221, v220
	v_add_f32_e32 v189, v189, v220
	ds_read_b128 v[220:223], v117 offset:25600
	s_waitcnt lgkmcnt(7)
	v_mul_f32_e32 v225, v91, v225
	v_fmac_f32_e32 v225, v90, v224
	v_mul_f32_e32 v224, v89, v227
	v_fmac_f32_e32 v224, v88, v226
	v_add_f32_e32 v224, v225, v224
	v_add_f32_e32 v189, v189, v224
	ds_read_b128 v[224:227], v117 offset:26624
	s_waitcnt lgkmcnt(7)
	v_mul_f32_e32 v229, v87, v229
	v_fmac_f32_e32 v229, v86, v228
	v_mul_f32_e32 v228, v85, v231
	v_fmac_f32_e32 v228, v84, v230
	v_add_f32_e32 v228, v229, v228
	v_add_f32_e32 v189, v189, v228
	ds_read_b128 v[228:231], v117 offset:27648
	s_waitcnt lgkmcnt(7)
	v_mul_f32_e32 v233, v83, v233
	v_fmac_f32_e32 v233, v82, v232
	v_mul_f32_e32 v232, v81, v235
	v_fmac_f32_e32 v232, v80, v234
	v_add_f32_e32 v232, v233, v232
	v_add_f32_e32 v189, v189, v232
	ds_read_b128 v[232:235], v117 offset:28672
	s_waitcnt lgkmcnt(7)
	v_mul_f32_e32 v237, v79, v237
	v_fmac_f32_e32 v237, v78, v236
	v_mul_f32_e32 v236, v77, v239
	v_fmac_f32_e32 v236, v76, v238
	v_add_f32_e32 v236, v237, v236
	v_add_f32_e32 v189, v189, v236
	ds_read_b128 v[236:239], v117 offset:29696
	s_waitcnt lgkmcnt(7)
	v_mul_f32_e32 v241, v75, v241
	v_fmac_f32_e32 v241, v74, v240
	v_mul_f32_e32 v240, v73, v243
	v_fmac_f32_e32 v240, v72, v242
	v_add_f32_e32 v240, v241, v240
	v_add_f32_e32 v189, v189, v240
	ds_read_b128 v[240:243], v117 offset:30720
	s_waitcnt lgkmcnt(7)
	v_mul_f32_e32 v249, v71, v249
	v_fmac_f32_e32 v249, v70, v248
	v_mul_f32_e32 v248, v69, v251
	v_fmac_f32_e32 v248, v68, v250
	v_add_f32_e32 v248, v249, v248
	v_add_f32_e32 v189, v189, v248
	ds_read_b128 v[248:251], v117 offset:31744
	s_waitcnt lgkmcnt(7)
	v_mul_f32_e32 v217, v115, v217
	v_fmac_f32_e32 v217, v114, v216
	v_mul_f32_e32 v216, v113, v219
	v_fmac_f32_e32 v216, v112, v218
	v_add_f32_e32 v216, v217, v216
	v_add_f32_e32 v190, 0, v216
	ds_read_b128 v[216:219], v117 offset:32768
	s_waitcnt lgkmcnt(7)
	v_mul_f32_e32 v221, v95, v221
	v_fmac_f32_e32 v221, v94, v220
	v_mul_f32_e32 v220, v93, v223
	v_fmac_f32_e32 v220, v92, v222
	v_add_f32_e32 v220, v221, v220
	v_add_f32_e32 v190, v190, v220
	ds_read_b128 v[220:223], v117 offset:33792
	s_waitcnt lgkmcnt(7)
	v_mul_f32_e32 v225, v91, v225
	v_fmac_f32_e32 v225, v90, v224
	v_mul_f32_e32 v224, v89, v227
	v_fmac_f32_e32 v224, v88, v226
	v_add_f32_e32 v224, v225, v224
	v_add_f32_e32 v190, v190, v224
	ds_read_b128 v[224:227], v117 offset:34816
	s_waitcnt lgkmcnt(7)
; #define LAS __attribute__((address_space(3)))
; template <int MODE, bool SB  > DI void norm_phase(const Params& P, const Frame& F, int L, const void* src_, const float* gain, bool combine) {
;     ...
;             for (int q = 0; q < 16; ++q) { float t = 0.f;
; #pragma unroll
;                 for (int j = 0; j < 8; ++j) { const f32x4 w = *(const LAS f32x4*)(F.lds + (size_t)(q * D + 256 * j + 4 * F.lane) * 4); t += (v[j][0] * w[0] + v[j][1] * w[1]) + (v[j][2] * w[2] + v[j][3] * w[3]); }
;                 s[q] = t; if ((q & 3) == 3) asm volatile("" ::: "memory"); }
	v_mul_f32_e32 v229, v87, v229
	v_fmac_f32_e32 v229, v86, v228
	v_mul_f32_e32 v228, v85, v231
	v_fmac_f32_e32 v228, v84, v230
	v_add_f32_e32 v228, v229, v228
	v_add_f32_e32 v190, v190, v228
	ds_read_b128 v[228:231], v117 offset:35840
	s_waitcnt lgkmcnt(7)
	v_mul_f32_e32 v233, v83, v233
	v_fmac_f32_e32 v233, v82, v232
	v_mul_f32_e32 v232, v81, v235
	v_fmac_f32_e32 v232, v80, v234
	v_add_f32_e32 v232, v233, v232
	v_add_f32_e32 v190, v190, v232
	ds_read_b128 v[232:235], v117 offset:36864
	s_waitcnt lgkmcnt(7)
	v_mul_f32_e32 v237, v79, v237
	v_fmac_f32_e32 v237, v78, v236
	v_mul_f32_e32 v236, v77, v239
	v_fmac_f32_e32 v236, v76, v238
	v_add_f32_e32 v236, v237, v236
	v_add_f32_e32 v190, v190, v236
	ds_read_b128 v[236:239], v117 offset:37888
	s_waitcnt lgkmcnt(7)
	v_mul_f32_e32 v241, v75, v241
	v_fmac_f32_e32 v241, v74, v240
	v_mul_f32_e32 v240, v73, v243
	v_fmac_f32_e32 v240, v72, v242
	v_add_f32_e32 v240, v241, v240
	v_add_f32_e32 v190, v190, v240
	ds_read_b128 v[240:243], v117 offset:38912
	s_waitcnt lgkmcnt(7)
	v_mul_f32_e32 v249, v71, v249
	v_fmac_f32_e32 v249, v70, v248
	v_mul_f32_e32 v248, v69, v251
	v_fmac_f32_e32 v248, v68, v250
	v_add_f32_e32 v248, v249, v248
	v_add_f32_e32 v190, v190, v248
	ds_read_b128 v[248:251], v117 offset:39936
	s_waitcnt lgkmcnt(7)
	v_mul_f32_e32 v217, v115, v217
	v_fmac_f32_e32 v217, v114, v216
	v_mul_f32_e32 v216, v113, v219
	v_fmac_f32_e32 v216, v112, v218
	v_add_f32_e32 v216, v217, v216
	v_add_f32_e32 v191, 0, v216
	ds_read_b128 v[216:219], v117 offset:40960
	s_waitcnt lgkmcnt(7)
	v_mul_f32_e32 v221, v95, v221
	v_fmac_f32_e32 v221, v94, v220
	v_mul_f32_e32 v220, v93, v223
	v_fmac_f32_e32 v220, v92, v222
	v_add_f32_e32 v220, v221, v220
	v_add_f32_e32 v191, v191, v220
	ds_read_b128 v[220:223], v117 offset:41984
	s_waitcnt lgkmcnt(7)
	v_mul_f32_e32 v225, v91, v225
	v_fmac_f32_e32 v225, v90, v224
	v_mul_f32_e32 v224, v89, v227
	v_fmac_f32_e32 v224, v88, v226
	v_add_f32_e32 v224, v225, v224
	v_add_f32_e32 v191, v191, v224
	ds_read_b128 v[224:227], v117 offset:43008
	s_waitcnt lgkmcnt(7)
	v_mul_f32_e32 v229, v87, v229
	v_fmac_f32_e32 v229, v86, v228
	v_mul_f32_e32 v228, v85, v231
	v_fmac_f32_e32 v228, v84, v230
	v_add_f32_e32 v228, v229, v228
	v_add_f32_e32 v191, v191, v228
	ds_read_b128 v[228:231], v117 offset:44032
	s_waitcnt lgkmcnt(7)
	v_mul_f32_e32 v233, v83, v233
	v_fmac_f32_e32 v233, v82, v232
	v_mul_f32_e32 v232, v81, v235
	v_fmac_f32_e32 v232, v80, v234
	v_add_f32_e32 v232, v233, v232
	v_add_f32_e32 v191, v191, v232
	ds_read_b128 v[232:235], v117 offset:45056
	s_waitcnt lgkmcnt(7)
	v_mul_f32_e32 v237, v79, v237
	v_fmac_f32_e32 v237, v78, v236
	v_mul_f32_e32 v236, v77, v239
	v_fmac_f32_e32 v236, v76, v238
	v_add_f32_e32 v236, v237, v236
	v_add_f32_e32 v191, v191, v236
	ds_read_b128 v[236:239], v117 offset:46080
	s_waitcnt lgkmcnt(7)
	v_mul_f32_e32 v241, v75, v241
	v_fmac_f32_e32 v241, v74, v240
	v_mul_f32_e32 v240, v73, v243
	v_fmac_f32_e32 v240, v72, v242
	v_add_f32_e32 v240, v241, v240
	v_add_f32_e32 v191, v191, v240
	ds_read_b128 v[240:243], v117 offset:47104
	s_waitcnt lgkmcnt(7)
	v_mul_f32_e32 v249, v71, v249
	v_fmac_f32_e32 v249, v70, v248
	v_mul_f32_e32 v248, v69, v251
	v_fmac_f32_e32 v248, v68, v250
	v_add_f32_e32 v248, v249, v248
	v_add_f32_e32 v191, v191, v248
	ds_read_b128 v[248:251], v117 offset:48128
	s_waitcnt lgkmcnt(7)
	v_mul_f32_e32 v217, v115, v217
	v_fmac_f32_e32 v217, v114, v216
	v_mul_f32_e32 v216, v113, v219
	v_fmac_f32_e32 v216, v112, v218
	v_add_f32_e32 v216, v217, v216
	v_add_f32_e32 v192, 0, v216
	ds_read_b128 v[216:219], v117 offset:49152
	s_waitcnt lgkmcnt(7)
	v_mul_f32_e32 v221, v95, v221
	v_fmac_f32_e32 v221, v94, v220
	v_mul_f32_e32 v220, v93, v223
	v_fmac_f32_e32 v220, v92, v222
	v_add_f32_e32 v220, v221, v220
	v_add_f32_e32 v192, v192, v220
	ds_read_b128 v[220:223], v117 offset:50176
	s_waitcnt lgkmcnt(7)
	v_mul_f32_e32 v225, v91, v225
	v_fmac_f32_e32 v225, v90, v224
	v_mul_f32_e32 v224, v89, v227
	v_fmac_f32_e32 v224, v88, v226
	v_add_f32_e32 v224, v225, v224
	v_add_f32_e32 v192, v192, v224
	ds_read_b128 v[224:227], v117 offset:51200
	s_waitcnt lgkmcnt(7)
	v_mul_f32_e32 v229, v87, v229
	v_fmac_f32_e32 v229, v86, v228
	v_mul_f32_e32 v228, v85, v231
	v_fmac_f32_e32 v228, v84, v230
	v_add_f32_e32 v228, v229, v228
	v_add_f32_e32 v192, v192, v228
	ds_read_b128 v[228:231], v117 offset:52224
	s_waitcnt lgkmcnt(7)
	v_mul_f32_e32 v233, v83, v233
	v_fmac_f32_e32 v233, v82, v232
	v_mul_f32_e32 v232, v81, v235
	v_fmac_f32_e32 v232, v80, v234
	v_add_f32_e32 v232, v233, v232
	v_add_f32_e32 v192, v192, v232
	ds_read_b128 v[232:235], v117 offset:53248
	s_waitcnt lgkmcnt(7)
	v_mul_f32_e32 v237, v79, v237
	v_fmac_f32_e32 v237, v78, v236
	v_mul_f32_e32 v236, v77, v239
	v_fmac_f32_e32 v236, v76, v238
	v_add_f32_e32 v236, v237, v236
	v_add_f32_e32 v192, v192, v236
	ds_read_b128 v[236:239], v117 offset:54272
	s_waitcnt lgkmcnt(7)
	v_mul_f32_e32 v241, v75, v241
	v_fmac_f32_e32 v241, v74, v240
	v_mul_f32_e32 v240, v73, v243
	v_fmac_f32_e32 v240, v72, v242
	v_add_f32_e32 v240, v241, v240
	v_add_f32_e32 v192, v192, v240
	ds_read_b128 v[240:243], v117 offset:55296
	s_waitcnt lgkmcnt(7)
	v_mul_f32_e32 v249, v71, v249
	v_fmac_f32_e32 v249, v70, v248
	v_mul_f32_e32 v248, v69, v251
	v_fmac_f32_e32 v248, v68, v250
	v_add_f32_e32 v248, v249, v248
	v_add_f32_e32 v193, v192, v248
	ds_read_b128 v[248:251], v117 offset:56320
	s_waitcnt lgkmcnt(7)
	v_mul_f32_e32 v217, v115, v217
	v_fmac_f32_e32 v217, v114, v216
	v_mul_f32_e32 v216, v113, v219
	v_fmac_f32_e32 v216, v112, v218
	v_add_f32_e32 v216, v217, v216
	v_add_f32_e32 v192, 0, v216
	ds_read_b128 v[216:219], v117 offset:57344
	s_waitcnt lgkmcnt(7)
; #define LAS __attribute__((address_space(3)))
; template <int MODE, bool SB  > DI void norm_phase(const Params& P, const Frame& F, int L, const void* src_, const float* gain, bool combine) {
;     ...
;             for (int q = 0; q < 16; ++q) { float t = 0.f;
; #pragma unroll
;                 for (int j = 0; j < 8; ++j) { const f32x4 w = *(const LAS f32x4*)(F.lds + (size_t)(q * D + 256 * j + 4 * F.lane) * 4); t += (v[j][0] * w[0] + v[j][1] * w[1]) + (v[j][2] * w[2] + v[j][3] * w[3]); }
;                 s[q] = t; if ((q & 3) == 3) asm volatile("" ::: "memory"); }
	v_mul_f32_e32 v221, v95, v221
	v_fmac_f32_e32 v221, v94, v220
	v_mul_f32_e32 v220, v93, v223
	v_fmac_f32_e32 v220, v92, v222
	v_add_f32_e32 v220, v221, v220
	v_add_f32_e32 v192, v192, v220
	ds_read_b128 v[220:223], v117 offset:58368
	s_waitcnt lgkmcnt(7)
	v_mul_f32_e32 v225, v91, v225
	v_fmac_f32_e32 v225, v90, v224
	v_mul_f32_e32 v224, v89, v227
	v_fmac_f32_e32 v224, v88, v226
	v_add_f32_e32 v224, v225, v224
	v_add_f32_e32 v192, v192, v224
	ds_read_b128 v[224:227], v117 offset:59392
	s_waitcnt lgkmcnt(7)
	v_mul_f32_e32 v229, v87, v229
	v_fmac_f32_e32 v229, v86, v228
	v_mul_f32_e32 v228, v85, v231
	v_fmac_f32_e32 v228, v84, v230
	v_add_f32_e32 v228, v229, v228
	v_add_f32_e32 v192, v192, v228
	ds_read_b128 v[228:231], v117 offset:60416
	s_waitcnt lgkmcnt(7)
	v_mul_f32_e32 v233, v83, v233
	v_fmac_f32_e32 v233, v82, v232
	v_mul_f32_e32 v232, v81, v235
	v_fmac_f32_e32 v232, v80, v234
	v_add_f32_e32 v232, v233, v232
	v_add_f32_e32 v192, v192, v232
	ds_read_b128 v[232:235], v117 offset:61440
	s_waitcnt lgkmcnt(7)
	v_mul_f32_e32 v237, v79, v237
	v_fmac_f32_e32 v237, v78, v236
	v_mul_f32_e32 v236, v77, v239
	v_fmac_f32_e32 v236, v76, v238
	v_add_f32_e32 v236, v237, v236
	v_add_f32_e32 v192, v192, v236
	ds_read_b128 v[236:239], v117 offset:62464
	s_waitcnt lgkmcnt(7)
	v_mul_f32_e32 v241, v75, v241
	v_fmac_f32_e32 v241, v74, v240
	v_mul_f32_e32 v240, v73, v243
	v_fmac_f32_e32 v240, v72, v242
	v_add_f32_e32 v240, v241, v240
	v_add_f32_e32 v192, v192, v240
	ds_read_b128 v[240:243], v117 offset:63488
	s_waitcnt lgkmcnt(7)
	v_mul_f32_e32 v249, v71, v249
	v_fmac_f32_e32 v249, v70, v248
	v_mul_f32_e32 v248, v69, v251
	v_fmac_f32_e32 v248, v68, v250
	v_add_f32_e32 v248, v249, v248
	v_add_f32_e32 v194, v192, v248
	ds_read_b128 v[248:251], v117 offset:64512
	s_waitcnt lgkmcnt(7)
	v_mul_f32_e32 v217, v115, v217
	v_fmac_f32_e32 v217, v114, v216
	v_mul_f32_e32 v216, v113, v219
	v_fmac_f32_e32 v216, v112, v218
	v_add_f32_e32 v216, v217, v216
	v_add_f32_e32 v192, 0, v216
	ds_read_b128 v[216:219], v118
	s_waitcnt lgkmcnt(7)
	v_mul_f32_e32 v221, v95, v221
	v_fmac_f32_e32 v221, v94, v220
	v_mul_f32_e32 v220, v93, v223
	v_fmac_f32_e32 v220, v92, v222
	v_add_f32_e32 v220, v221, v220
	v_add_f32_e32 v192, v192, v220
	ds_read_b128 v[220:223], v119
	s_waitcnt lgkmcnt(7)
	v_mul_f32_e32 v225, v91, v225
	v_fmac_f32_e32 v225, v90, v224
	v_mul_f32_e32 v224, v89, v227
	v_fmac_f32_e32 v224, v88, v226
	v_add_f32_e32 v224, v225, v224
	v_add_f32_e32 v192, v192, v224
	ds_read_b128 v[224:227], v120
	s_waitcnt lgkmcnt(7)
	v_mul_f32_e32 v229, v87, v229
	v_fmac_f32_e32 v229, v86, v228
	v_mul_f32_e32 v228, v85, v231
	v_fmac_f32_e32 v228, v84, v230
	v_add_f32_e32 v228, v229, v228
	v_add_f32_e32 v192, v192, v228
	ds_read_b128 v[228:231], v121
	s_waitcnt lgkmcnt(7)
	v_mul_f32_e32 v233, v83, v233
	v_fmac_f32_e32 v233, v82, v232
	v_mul_f32_e32 v232, v81, v235
	v_fmac_f32_e32 v232, v80, v234
	v_add_f32_e32 v232, v233, v232
	v_add_f32_e32 v192, v192, v232
	ds_read_b128 v[232:235], v122
	s_waitcnt lgkmcnt(7)
	v_mul_f32_e32 v237, v79, v237
	v_fmac_f32_e32 v237, v78, v236
	v_mul_f32_e32 v236, v77, v239
	v_fmac_f32_e32 v236, v76, v238
	v_add_f32_e32 v236, v237, v236
	v_add_f32_e32 v192, v192, v236
	ds_read_b128 v[236:239], v123
	s_waitcnt lgkmcnt(7)
	v_mul_f32_e32 v241, v75, v241
	v_fmac_f32_e32 v241, v74, v240
	v_mul_f32_e32 v240, v73, v243
	v_fmac_f32_e32 v240, v72, v242
	v_add_f32_e32 v240, v241, v240
	v_add_f32_e32 v192, v192, v240
	ds_read_b128 v[240:243], v124
	s_waitcnt lgkmcnt(7)
	v_mul_f32_e32 v249, v71, v249
	v_fmac_f32_e32 v249, v70, v248
	v_mul_f32_e32 v248, v69, v251
	v_fmac_f32_e32 v248, v68, v250
	v_add_f32_e32 v248, v249, v248
	v_add_f32_e32 v195, v192, v248
	ds_read_b128 v[248:251], v125
	s_waitcnt lgkmcnt(7)
	v_mul_f32_e32 v217, v115, v217
	v_fmac_f32_e32 v217, v114, v216
	v_mul_f32_e32 v216, v113, v219
	v_fmac_f32_e32 v216, v112, v218
	v_add_f32_e32 v216, v217, v216
	v_add_f32_e32 v192, 0, v216
	ds_read_b128 v[216:219], v126
	s_waitcnt lgkmcnt(7)
	v_mul_f32_e32 v221, v95, v221
	v_fmac_f32_e32 v221, v94, v220
	v_mul_f32_e32 v220, v93, v223
	v_fmac_f32_e32 v220, v92, v222
	v_add_f32_e32 v220, v221, v220
	v_add_f32_e32 v192, v192, v220
	ds_read_b128 v[220:223], v127
	s_waitcnt lgkmcnt(7)
	v_mul_f32_e32 v225, v91, v225
	v_fmac_f32_e32 v225, v90, v224
	v_mul_f32_e32 v224, v89, v227
	v_fmac_f32_e32 v224, v88, v226
	v_add_f32_e32 v224, v225, v224
	v_add_f32_e32 v192, v192, v224
	ds_read_b128 v[224:227], v128
	s_waitcnt lgkmcnt(7)
	v_mul_f32_e32 v229, v87, v229
	v_fmac_f32_e32 v229, v86, v228
	v_mul_f32_e32 v228, v85, v231
	v_fmac_f32_e32 v228, v84, v230
	v_add_f32_e32 v228, v229, v228
	v_add_f32_e32 v192, v192, v228
	ds_read_b128 v[228:231], v129
	s_waitcnt lgkmcnt(7)
	v_mul_f32_e32 v233, v83, v233
	v_fmac_f32_e32 v233, v82, v232
	v_mul_f32_e32 v232, v81, v235
	v_fmac_f32_e32 v232, v80, v234
	v_add_f32_e32 v232, v233, v232
	v_add_f32_e32 v192, v192, v232
	ds_read_b128 v[232:235], v130
	s_waitcnt lgkmcnt(7)
	v_mul_f32_e32 v237, v79, v237
	v_fmac_f32_e32 v237, v78, v236
	v_mul_f32_e32 v236, v77, v239
	v_fmac_f32_e32 v236, v76, v238
	v_add_f32_e32 v236, v237, v236
	v_add_f32_e32 v192, v192, v236
	ds_read_b128 v[236:239], v131
	s_waitcnt lgkmcnt(7)
	v_mul_f32_e32 v241, v75, v241
	v_fmac_f32_e32 v241, v74, v240
	v_mul_f32_e32 v240, v73, v243
	v_fmac_f32_e32 v240, v72, v242
	v_add_f32_e32 v240, v241, v240
	v_add_f32_e32 v192, v192, v240
	ds_read_b128 v[240:243], v132
	s_waitcnt lgkmcnt(7)
	v_mul_f32_e32 v249, v71, v249
	v_fmac_f32_e32 v249, v70, v248
	v_mul_f32_e32 v248, v69, v251
	v_fmac_f32_e32 v248, v68, v250
	v_add_f32_e32 v248, v249, v248
	v_add_f32_e32 v196, v192, v248
	ds_read_b128 v[248:251], v133
	s_waitcnt lgkmcnt(7)
; #define LAS __attribute__((address_space(3)))
; template <int MODE, bool SB  > DI void norm_phase(const Params& P, const Frame& F, int L, const void* src_, const float* gain, bool combine) {
;     ...
;             for (int q = 0; q < 16; ++q) { float t = 0.f;
; #pragma unroll
;                 for (int j = 0; j < 8; ++j) { const f32x4 w = *(const LAS f32x4*)(F.lds + (size_t)(q * D + 256 * j + 4 * F.lane) * 4); t += (v[j][0] * w[0] + v[j][1] * w[1]) + (v[j][2] * w[2] + v[j][3] * w[3]); }
;                 s[q] = t; if ((q & 3) == 3) asm volatile("" ::: "memory"); }
	v_mul_f32_e32 v217, v115, v217
	v_fmac_f32_e32 v217, v114, v216
	v_mul_f32_e32 v216, v113, v219
	v_fmac_f32_e32 v216, v112, v218
	v_add_f32_e32 v216, v217, v216
	v_add_f32_e32 v192, 0, v216
	ds_read_b128 v[216:219], v134
	s_waitcnt lgkmcnt(7)
	v_mul_f32_e32 v221, v95, v221
	v_fmac_f32_e32 v221, v94, v220
	v_mul_f32_e32 v220, v93, v223
	v_fmac_f32_e32 v220, v92, v222
	v_add_f32_e32 v220, v221, v220
	v_add_f32_e32 v192, v192, v220
	ds_read_b128 v[220:223], v135
	s_waitcnt lgkmcnt(7)
	v_mul_f32_e32 v225, v91, v225
	v_fmac_f32_e32 v225, v90, v224
	v_mul_f32_e32 v224, v89, v227
	v_fmac_f32_e32 v224, v88, v226
	v_add_f32_e32 v224, v225, v224
	v_add_f32_e32 v192, v192, v224
	ds_read_b128 v[224:227], v136
	s_waitcnt lgkmcnt(7)
	v_mul_f32_e32 v229, v87, v229
	v_fmac_f32_e32 v229, v86, v228
	v_mul_f32_e32 v228, v85, v231
	v_fmac_f32_e32 v228, v84, v230
	v_add_f32_e32 v228, v229, v228
	v_add_f32_e32 v192, v192, v228
	ds_read_b128 v[228:231], v137
	s_waitcnt lgkmcnt(7)
	v_mul_f32_e32 v233, v83, v233
	v_fmac_f32_e32 v233, v82, v232
	v_mul_f32_e32 v232, v81, v235
	v_fmac_f32_e32 v232, v80, v234
	v_add_f32_e32 v232, v233, v232
	v_add_f32_e32 v192, v192, v232
	ds_read_b128 v[232:235], v138
	s_waitcnt lgkmcnt(7)
	v_mul_f32_e32 v237, v79, v237
	v_fmac_f32_e32 v237, v78, v236
	v_mul_f32_e32 v236, v77, v239
	v_fmac_f32_e32 v236, v76, v238
	v_add_f32_e32 v236, v237, v236
	v_add_f32_e32 v192, v192, v236
	ds_read_b128 v[236:239], v139
	s_waitcnt lgkmcnt(7)
	v_mul_f32_e32 v241, v75, v241
	v_fmac_f32_e32 v241, v74, v240
	v_mul_f32_e32 v240, v73, v243
	v_fmac_f32_e32 v240, v72, v242
	v_add_f32_e32 v240, v241, v240
	v_add_f32_e32 v192, v192, v240
	ds_read_b128 v[240:243], v140
	s_waitcnt lgkmcnt(7)
	v_mul_f32_e32 v249, v71, v249
	v_fmac_f32_e32 v249, v70, v248
	v_mul_f32_e32 v248, v69, v251
	v_fmac_f32_e32 v248, v68, v250
	v_add_f32_e32 v248, v249, v248
	v_add_f32_e32 v197, v192, v248
	ds_read_b128 v[248:251], v141
	s_waitcnt lgkmcnt(7)
	v_mul_f32_e32 v217, v115, v217
	v_fmac_f32_e32 v217, v114, v216
	v_mul_f32_e32 v216, v113, v219
	v_fmac_f32_e32 v216, v112, v218
	v_add_f32_e32 v216, v217, v216
	v_add_f32_e32 v192, 0, v216
	ds_read_b128 v[216:219], v142
	s_waitcnt lgkmcnt(7)
	v_mul_f32_e32 v221, v95, v221
	v_fmac_f32_e32 v221, v94, v220
	v_mul_f32_e32 v220, v93, v223
	v_fmac_f32_e32 v220, v92, v222
	v_add_f32_e32 v220, v221, v220
	v_add_f32_e32 v192, v192, v220
	ds_read_b128 v[220:223], v143
	s_waitcnt lgkmcnt(7)
	v_mul_f32_e32 v225, v91, v225
	v_fmac_f32_e32 v225, v90, v224
	v_mul_f32_e32 v224, v89, v227
	v_fmac_f32_e32 v224, v88, v226
	v_add_f32_e32 v224, v225, v224
	v_add_f32_e32 v192, v192, v224
	ds_read_b128 v[224:227], v144
	s_waitcnt lgkmcnt(7)
	v_mul_f32_e32 v229, v87, v229
	v_fmac_f32_e32 v229, v86, v228
	v_mul_f32_e32 v228, v85, v231
	v_fmac_f32_e32 v228, v84, v230
	v_add_f32_e32 v228, v229, v228
	v_add_f32_e32 v192, v192, v228
	ds_read_b128 v[228:231], v145
	s_waitcnt lgkmcnt(7)
	v_mul_f32_e32 v233, v83, v233
	v_fmac_f32_e32 v233, v82, v232
	v_mul_f32_e32 v232, v81, v235
	v_fmac_f32_e32 v232, v80, v234
	v_add_f32_e32 v232, v233, v232
	v_add_f32_e32 v192, v192, v232
	ds_read_b128 v[232:235], v146
	s_waitcnt lgkmcnt(7)
	v_mul_f32_e32 v237, v79, v237
	v_fmac_f32_e32 v237, v78, v236
	v_mul_f32_e32 v236, v77, v239
	v_fmac_f32_e32 v236, v76, v238
	v_add_f32_e32 v236, v237, v236
	v_add_f32_e32 v192, v192, v236
	ds_read_b128 v[236:239], v147
	s_waitcnt lgkmcnt(7)
	v_mul_f32_e32 v241, v75, v241
	v_fmac_f32_e32 v241, v74, v240
	v_mul_f32_e32 v240, v73, v243
	v_fmac_f32_e32 v240, v72, v242
	v_add_f32_e32 v240, v241, v240
	v_add_f32_e32 v192, v192, v240
	ds_read_b128 v[240:243], v148
	s_waitcnt lgkmcnt(7)
	v_mul_f32_e32 v249, v71, v249
	v_fmac_f32_e32 v249, v70, v248
	v_mul_f32_e32 v248, v69, v251
	v_fmac_f32_e32 v248, v68, v250
	v_add_f32_e32 v248, v249, v248
	v_add_f32_e32 v198, v192, v248
	ds_read_b128 v[248:251], v149
	s_waitcnt lgkmcnt(7)
	v_mul_f32_e32 v217, v115, v217
	v_fmac_f32_e32 v217, v114, v216
	v_mul_f32_e32 v216, v113, v219
	v_fmac_f32_e32 v216, v112, v218
	v_add_f32_e32 v216, v217, v216
	v_add_f32_e32 v192, 0, v216
	ds_read_b128 v[216:219], v150
	s_waitcnt lgkmcnt(7)
	v_mul_f32_e32 v221, v95, v221
	v_fmac_f32_e32 v221, v94, v220
	v_mul_f32_e32 v220, v93, v223
	v_fmac_f32_e32 v220, v92, v222
	v_add_f32_e32 v220, v221, v220
	v_add_f32_e32 v192, v192, v220
	ds_read_b128 v[220:223], v151
	s_waitcnt lgkmcnt(7)
	v_mul_f32_e32 v225, v91, v225
	v_fmac_f32_e32 v225, v90, v224
	v_mul_f32_e32 v224, v89, v227
	v_fmac_f32_e32 v224, v88, v226
	v_add_f32_e32 v224, v225, v224
	v_add_f32_e32 v192, v192, v224
	ds_read_b128 v[224:227], v152
	s_waitcnt lgkmcnt(7)
	v_mul_f32_e32 v229, v87, v229
	v_fmac_f32_e32 v229, v86, v228
	v_mul_f32_e32 v228, v85, v231
	v_fmac_f32_e32 v228, v84, v230
	v_add_f32_e32 v228, v229, v228
	v_add_f32_e32 v192, v192, v228
	ds_read_b128 v[228:231], v153
	s_waitcnt lgkmcnt(7)
	v_mul_f32_e32 v233, v83, v233
	v_fmac_f32_e32 v233, v82, v232
	v_mul_f32_e32 v232, v81, v235
	v_fmac_f32_e32 v232, v80, v234
	v_add_f32_e32 v232, v233, v232
	v_add_f32_e32 v192, v192, v232
	ds_read_b128 v[232:235], v154
	s_waitcnt lgkmcnt(7)
	v_mul_f32_e32 v237, v79, v237
	v_fmac_f32_e32 v237, v78, v236
	v_mul_f32_e32 v236, v77, v239
	v_fmac_f32_e32 v236, v76, v238
	v_add_f32_e32 v236, v237, v236
	v_add_f32_e32 v192, v192, v236
	ds_read_b128 v[236:239], v155
	s_waitcnt lgkmcnt(7)
	v_mul_f32_e32 v241, v75, v241
	v_fmac_f32_e32 v241, v74, v240
	v_mul_f32_e32 v240, v73, v243
	v_fmac_f32_e32 v240, v72, v242
	v_add_f32_e32 v240, v241, v240
	v_add_f32_e32 v192, v192, v240
	ds_read_b128 v[240:243], v156
	s_waitcnt lgkmcnt(7)
; #define LAS __attribute__((address_space(3)))
; template <int MODE, bool SB  > DI void norm_phase(const Params& P, const Frame& F, int L, const void* src_, const float* gain, bool combine) {
;     ...
;             for (int q = 0; q < 16; ++q) { float t = 0.f;
; #pragma unroll
;                 for (int j = 0; j < 8; ++j) { const f32x4 w = *(const LAS f32x4*)(F.lds + (size_t)(q * D + 256 * j + 4 * F.lane) * 4); t += (v[j][0] * w[0] + v[j][1] * w[1]) + (v[j][2] * w[2] + v[j][3] * w[3]); }
;                 s[q] = t; if ((q & 3) == 3) asm volatile("" ::: "memory"); }
	v_mul_f32_e32 v249, v71, v249
	v_fmac_f32_e32 v249, v70, v248
	v_mul_f32_e32 v248, v69, v251
	v_fmac_f32_e32 v248, v68, v250
	v_add_f32_e32 v248, v249, v248
	v_add_f32_e32 v199, v192, v248
	ds_read_b128 v[248:251], v157
	s_waitcnt lgkmcnt(7)
	v_mul_f32_e32 v217, v115, v217
	v_fmac_f32_e32 v217, v114, v216
	v_mul_f32_e32 v216, v113, v219
	v_fmac_f32_e32 v216, v112, v218
	v_add_f32_e32 v216, v217, v216
	v_add_f32_e32 v192, 0, v216
	ds_read_b128 v[216:219], v158
	s_waitcnt lgkmcnt(7)
	v_mul_f32_e32 v221, v95, v221
	v_fmac_f32_e32 v221, v94, v220
	v_mul_f32_e32 v220, v93, v223
	v_fmac_f32_e32 v220, v92, v222
	v_add_f32_e32 v220, v221, v220
	v_add_f32_e32 v192, v192, v220
	ds_read_b128 v[220:223], v159
	s_waitcnt lgkmcnt(7)
	v_mul_f32_e32 v225, v91, v225
	v_fmac_f32_e32 v225, v90, v224
	v_mul_f32_e32 v224, v89, v227
	v_fmac_f32_e32 v224, v88, v226
	v_add_f32_e32 v224, v225, v224
	v_add_f32_e32 v192, v192, v224
	ds_read_b128 v[224:227], v160
	s_waitcnt lgkmcnt(7)
	v_mul_f32_e32 v229, v87, v229
	v_fmac_f32_e32 v229, v86, v228
	v_mul_f32_e32 v228, v85, v231
	v_fmac_f32_e32 v228, v84, v230
	v_add_f32_e32 v228, v229, v228
	v_add_f32_e32 v192, v192, v228
	ds_read_b128 v[228:231], v161
	s_waitcnt lgkmcnt(7)
	v_mul_f32_e32 v233, v83, v233
	v_fmac_f32_e32 v233, v82, v232
	v_mul_f32_e32 v232, v81, v235
	v_fmac_f32_e32 v232, v80, v234
	v_add_f32_e32 v232, v233, v232
	v_add_f32_e32 v192, v192, v232
	ds_read_b128 v[232:235], v162
	s_waitcnt lgkmcnt(7)
	v_mul_f32_e32 v237, v79, v237
	v_fmac_f32_e32 v237, v78, v236
	v_mul_f32_e32 v236, v77, v239
	v_fmac_f32_e32 v236, v76, v238
	v_add_f32_e32 v236, v237, v236
	v_add_f32_e32 v192, v192, v236
	ds_read_b128 v[236:239], v163
	s_waitcnt lgkmcnt(7)
	v_mul_f32_e32 v241, v75, v241
	v_fmac_f32_e32 v241, v74, v240
	v_mul_f32_e32 v240, v73, v243
	v_fmac_f32_e32 v240, v72, v242
	v_add_f32_e32 v240, v241, v240
	v_add_f32_e32 v192, v192, v240
	ds_read_b128 v[240:243], v164
	s_waitcnt lgkmcnt(7)
	v_mul_f32_e32 v249, v71, v249
	v_fmac_f32_e32 v249, v70, v248
	v_mul_f32_e32 v248, v69, v251
	v_fmac_f32_e32 v248, v68, v250
	v_add_f32_e32 v248, v249, v248
	v_add_f32_e32 v200, v192, v248
	ds_read_b128 v[248:251], v165
	s_waitcnt lgkmcnt(7)
	v_mul_f32_e32 v217, v115, v217
	v_fmac_f32_e32 v217, v114, v216
	v_mul_f32_e32 v216, v113, v219
	v_fmac_f32_e32 v216, v112, v218
	v_add_f32_e32 v216, v217, v216
	v_add_f32_e32 v192, 0, v216
	ds_read_b128 v[216:219], v166
	s_waitcnt lgkmcnt(7)
	v_mul_f32_e32 v221, v95, v221
	v_fmac_f32_e32 v221, v94, v220
	v_mul_f32_e32 v220, v93, v223
	v_fmac_f32_e32 v220, v92, v222
	v_add_f32_e32 v220, v221, v220
	v_add_f32_e32 v192, v192, v220
	ds_read_b128 v[220:223], v167
	s_waitcnt lgkmcnt(7)
	v_mul_f32_e32 v225, v91, v225
	v_fmac_f32_e32 v225, v90, v224
	v_mul_f32_e32 v224, v89, v227
	v_fmac_f32_e32 v224, v88, v226
	v_add_f32_e32 v224, v225, v224
	v_add_f32_e32 v192, v192, v224
	ds_read_b128 v[224:227], v168
	s_waitcnt lgkmcnt(7)
	v_mul_f32_e32 v229, v87, v229
	v_fmac_f32_e32 v229, v86, v228
	v_mul_f32_e32 v228, v85, v231
	v_fmac_f32_e32 v228, v84, v230
	v_add_f32_e32 v228, v229, v228
	v_add_f32_e32 v192, v192, v228
	ds_read_b128 v[228:231], v169
	s_waitcnt lgkmcnt(7)
	v_mul_f32_e32 v233, v83, v233
	v_fmac_f32_e32 v233, v82, v232
	v_mul_f32_e32 v232, v81, v235
	v_fmac_f32_e32 v232, v80, v234
	v_add_f32_e32 v232, v233, v232
	v_add_f32_e32 v192, v192, v232
	ds_read_b128 v[232:235], v170
	s_waitcnt lgkmcnt(7)
	v_mul_f32_e32 v237, v79, v237
	v_fmac_f32_e32 v237, v78, v236
	v_mul_f32_e32 v236, v77, v239
	v_fmac_f32_e32 v236, v76, v238
	v_add_f32_e32 v236, v237, v236
	v_add_f32_e32 v192, v192, v236
	ds_read_b128 v[236:239], v171
	s_waitcnt lgkmcnt(7)
	v_mul_f32_e32 v241, v75, v241
	v_fmac_f32_e32 v241, v74, v240
	v_mul_f32_e32 v240, v73, v243
	v_fmac_f32_e32 v240, v72, v242
	v_add_f32_e32 v240, v241, v240
	v_add_f32_e32 v192, v192, v240
	ds_read_b128 v[240:243], v172
	s_waitcnt lgkmcnt(7)
	v_mul_f32_e32 v249, v71, v249
	v_fmac_f32_e32 v249, v70, v248
	v_mul_f32_e32 v248, v69, v251
	v_fmac_f32_e32 v248, v68, v250
	v_add_f32_e32 v248, v249, v248
	v_add_f32_e32 v201, v192, v248
	ds_read_b128 v[248:251], v173
	s_waitcnt lgkmcnt(7)
	v_mul_f32_e32 v217, v115, v217
	v_fmac_f32_e32 v217, v114, v216
	v_mul_f32_e32 v216, v113, v219
	v_fmac_f32_e32 v216, v112, v218
	v_add_f32_e32 v216, v217, v216
	v_add_f32_e32 v192, 0, v216
	ds_read_b128 v[216:219], v174
	s_waitcnt lgkmcnt(7)
	v_mul_f32_e32 v221, v95, v221
	v_fmac_f32_e32 v221, v94, v220
	v_mul_f32_e32 v220, v93, v223
	v_fmac_f32_e32 v220, v92, v222
	v_add_f32_e32 v220, v221, v220
	v_add_f32_e32 v192, v192, v220
	ds_read_b128 v[220:223], v175
	s_waitcnt lgkmcnt(7)
	v_mul_f32_e32 v225, v91, v225
	v_fmac_f32_e32 v225, v90, v224
	v_mul_f32_e32 v224, v89, v227
	v_fmac_f32_e32 v224, v88, v226
	v_add_f32_e32 v224, v225, v224
	v_add_f32_e32 v192, v192, v224
	ds_read_b128 v[224:227], v176
	s_waitcnt lgkmcnt(7)
	v_mul_f32_e32 v229, v87, v229
	v_fmac_f32_e32 v229, v86, v228
	v_mul_f32_e32 v228, v85, v231
	v_fmac_f32_e32 v228, v84, v230
	v_add_f32_e32 v228, v229, v228
	v_add_f32_e32 v192, v192, v228
	ds_read_b128 v[228:231], v177
	s_waitcnt lgkmcnt(7)
; #define LAS __attribute__((address_space(3)))
; template <int MODE, bool SB  > DI void norm_phase(const Params& P, const Frame& F, int L, const void* src_, const float* gain, bool combine) {
;     ...
;             for (int q = 0; q < 16; ++q) { float t = 0.f;
; #pragma unroll
;                 for (int j = 0; j < 8; ++j) { const f32x4 w = *(const LAS f32x4*)(F.lds + (size_t)(q * D + 256 * j + 4 * F.lane) * 4); t += (v[j][0] * w[0] + v[j][1] * w[1]) + (v[j][2] * w[2] + v[j][3] * w[3]); }
;                 s[q] = t; if ((q & 3) == 3) asm volatile("" ::: "memory"); }
; #pragma unroll
;             for (int i = 0; i < 8; ++i) { const bool hi = (F.lane & 32) != 0; const float send = hi ? s[i] : s[i + 8], keep = hi ? s[i + 8] : s[i]; s[i] = keep + shx<32>(send); }
; #pragma unroll
;             for (int i = 0; i < 4; ++i) { const bool hi = (F.lane & 16) != 0; const float send = hi ? s[i] : s[i + 4], keep = hi ? s[i + 4] : s[i]; s[i] = keep + shx<16>(send); }
; #pragma unroll
;             for (int i = 0; i < 2; ++i) { const bool hi = (F.lane & 8) != 0; const float send = hi ? s[i] : s[i + 2], keep = hi ? s[i + 2] : s[i]; s[i] = keep + shx<8>(send); }
;             { const bool hi = (F.lane & 4) != 0; const float send = hi ? s[0] : s[1], keep = hi ? s[1] : s[0]; s[0] = keep + shx<4>(send); }
;             float mine = s[0]; mine += shx<2>(mine); mine += shx<1>(mine);
	v_mul_f32_e32 v233, v83, v233
	v_fmac_f32_e32 v233, v82, v232
	v_mul_f32_e32 v232, v81, v235
	v_fmac_f32_e32 v232, v80, v234
	v_add_f32_e32 v232, v233, v232
	v_add_f32_e32 v192, v192, v232
	ds_read_b128 v[232:235], v178
	s_waitcnt lgkmcnt(7)
	v_mul_f32_e32 v237, v79, v237
	v_fmac_f32_e32 v237, v78, v236
	v_mul_f32_e32 v236, v77, v239
	v_fmac_f32_e32 v236, v76, v238
	v_add_f32_e32 v236, v237, v236
	v_add_f32_e32 v192, v192, v236
	ds_read_b128 v[236:239], v179
	s_waitcnt lgkmcnt(7)
	v_mul_f32_e32 v241, v75, v241
	v_fmac_f32_e32 v241, v74, v240
	v_mul_f32_e32 v240, v73, v243
	v_fmac_f32_e32 v240, v72, v242
	v_add_f32_e32 v240, v241, v240
	v_add_f32_e32 v192, v192, v240
	ds_read_b128 v[240:243], v180
	s_waitcnt lgkmcnt(7)
	v_mul_f32_e32 v249, v71, v249
	v_fmac_f32_e32 v249, v70, v248
	v_mul_f32_e32 v248, v69, v251
	v_fmac_f32_e32 v248, v68, v250
	v_add_f32_e32 v248, v249, v248
	v_add_f32_e32 v202, v192, v248
	ds_read_b128 v[64:67], v181
	s_waitcnt lgkmcnt(7)
	v_mul_f32_e32 v217, v115, v217
	v_fmac_f32_e32 v217, v114, v216
	v_mul_f32_e32 v216, v113, v219
	v_fmac_f32_e32 v216, v112, v218
	v_add_f32_e32 v216, v217, v216
	v_add_f32_e32 v112, 0, v216
	s_waitcnt lgkmcnt(6)
	v_mul_f32_e32 v221, v95, v221
	v_fmac_f32_e32 v221, v94, v220
	v_mul_f32_e32 v220, v93, v223
	v_fmac_f32_e32 v220, v92, v222
	v_add_f32_e32 v220, v221, v220
	v_add_f32_e32 v92, v112, v220
	s_waitcnt lgkmcnt(5)
	v_mul_f32_e32 v225, v91, v225
	v_fmac_f32_e32 v225, v90, v224
	v_mul_f32_e32 v224, v89, v227
	v_fmac_f32_e32 v224, v88, v226
	v_add_f32_e32 v224, v225, v224
	v_add_f32_e32 v88, v92, v224
	s_waitcnt lgkmcnt(4)
	v_mul_f32_e32 v229, v87, v229
	v_fmac_f32_e32 v229, v86, v228
	v_mul_f32_e32 v228, v85, v231
	v_fmac_f32_e32 v228, v84, v230
	v_add_f32_e32 v228, v229, v228
	v_add_f32_e32 v84, v88, v228
	s_waitcnt lgkmcnt(3)
	v_mul_f32_e32 v233, v83, v233
	v_fmac_f32_e32 v233, v82, v232
	v_mul_f32_e32 v232, v81, v235
	v_fmac_f32_e32 v232, v80, v234
	v_add_f32_e32 v232, v233, v232
	v_add_f32_e32 v80, v84, v232
	s_waitcnt lgkmcnt(2)
	v_mul_f32_e32 v237, v79, v237
	v_fmac_f32_e32 v237, v78, v236
	v_mul_f32_e32 v236, v77, v239
	v_fmac_f32_e32 v236, v76, v238
	v_add_f32_e32 v236, v237, v236
	v_add_f32_e32 v76, v80, v236
	s_waitcnt lgkmcnt(1)
	v_mul_f32_e32 v241, v75, v241
	v_fmac_f32_e32 v241, v74, v240
	v_mul_f32_e32 v240, v73, v243
	v_fmac_f32_e32 v240, v72, v242
	v_add_f32_e32 v240, v241, v240
	v_add_f32_e32 v72, v76, v240
	s_waitcnt lgkmcnt(0)
	v_mul_f32_e32 v65, v71, v65
	v_fmac_f32_e32 v65, v70, v64
	v_mul_f32_e32 v64, v69, v67
	v_fmac_f32_e32 v64, v68, v66
	v_add_f32_e32 v64, v65, v64
	s_waitcnt lgkmcnt(0)
	s_nop 1
	v_permlane32_swap_b32_e32 v111, v196
	v_add_f32_e32 v65, v111, v196
	v_add_f32_e32 v64, v72, v64
	s_waitcnt lgkmcnt(0)
	s_nop 1
	v_permlane32_swap_b32_e32 v188, v197
	v_add_f32_e32 v66, v188, v197
	s_waitcnt lgkmcnt(0)
	s_nop 1
	v_permlane32_swap_b32_e32 v189, v198
	v_add_f32_e32 v67, v189, v198
	s_waitcnt lgkmcnt(0)
	s_nop 1
	v_permlane32_swap_b32_e32 v190, v199
	v_add_f32_e32 v68, v190, v199
	s_waitcnt lgkmcnt(0)
	s_nop 1
	v_permlane32_swap_b32_e32 v191, v200
	v_add_f32_e32 v69, v191, v200
	s_waitcnt lgkmcnt(0)
	s_nop 1
	v_permlane32_swap_b32_e32 v193, v201
	v_add_f32_e32 v70, v193, v201
	s_waitcnt lgkmcnt(0)
	s_nop 1
	v_permlane32_swap_b32_e32 v194, v202
	v_add_f32_e32 v71, v194, v202
	s_waitcnt lgkmcnt(0)
	s_nop 1
	v_permlane32_swap_b32_e32 v195, v64
	v_add_f32_e32 v64, v195, v64
	s_waitcnt lgkmcnt(0)
	s_nop 1
	v_permlane16_swap_b32_e32 v65, v69
	v_add_f32_e32 v65, v65, v69
	s_waitcnt lgkmcnt(0)
	s_nop 1
	v_permlane16_swap_b32_e32 v66, v70
	v_add_f32_e32 v66, v66, v70
	s_waitcnt lgkmcnt(0)
	s_nop 1
	v_permlane16_swap_b32_e32 v67, v71
	v_add_f32_e32 v67, v67, v71
	s_waitcnt lgkmcnt(0)
	s_nop 1
	v_permlane16_swap_b32_e32 v68, v64
	v_add_f32_e32 v64, v68, v64
	v_cndmask_b32_e64 v68, v65, v67, s[10:11]
	v_cndmask_b32_e64 v65, v67, v65, s[10:11]
	ds_swizzle_b32 v67, v68 offset:swizzle(SWAP,8)
	s_waitcnt lgkmcnt(0)
	v_add_f32_e32 v65, v65, v67
	v_cndmask_b32_e64 v67, v66, v64, s[10:11]
	v_cndmask_b32_e64 v64, v64, v66, s[10:11]
	ds_swizzle_b32 v66, v67 offset:swizzle(SWAP,8)
	s_waitcnt lgkmcnt(0)
	v_add_f32_e32 v64, v64, v66
	v_cndmask_b32_e64 v66, v65, v64, s[12:13]
	v_cndmask_b32_e64 v64, v64, v65, s[12:13]
	ds_swizzle_b32 v65, v66 offset:swizzle(SWAP,4)
	s_waitcnt lgkmcnt(0)
	v_add_f32_e32 v64, v64, v65
	s_nop 1
	v_add_f32_dpp v64, v64, v64 quad_perm:[2,3,0,1] row_mask:0xf bank_mask:0xf bound_ctrl:1
	s_nop 1
	v_mov_b32_dpp v65, v64 quad_perm:[1,0,3,2] row_mask:0xf bank_mask:0xf bound_ctrl:1
	s_and_saveexec_b64 s[20:21], s[14:15]
	s_cbranch_execz .LBB0_82
	v_add_f32_e32 v65, v64, v65
	s_and_saveexec_b64 s[24:25], s[16:17]
	s_xor_b64 s[24:25], exec, s[24:25]
	s_cbranch_execz .LBB0_94
	s_and_saveexec_b64 s[26:27], s[6:7]
	s_xor_b64 s[26:27], exec, s[26:27]
	s_cbranch_execz .LBB0_91
	s_and_saveexec_b64 s[28:29], s[18:19]
	s_xor_b64 s[28:29], exec, s[28:29]
	s_cbranch_execz .LBB0_88
	v_mov_b32_e32 v64, v203
	v_add_f32_e32 v64, v65, v64

.LBB0_139:
	global_load_dword v1, v0, s[10:11] sc1
	s_waitcnt vmcnt(0)
	v_cmp_eq_u32_e32 vcc, 0, v1
	s_cbranch_vccnz .LBB0_141
	s_mov_b64 s[18:19], -1
	s_mov_b64 s[22:23], -1
	s_branch .LBB0_135
	s_nop 0
	s_nop 0
	s_nop 0
	s_nop 0
	s_nop 0
	s_nop 0
	s_nop 0
	s_nop 0
	s_nop 0
	s_nop 0
	s_nop 0
	s_nop 0
	s_nop 0
	s_nop 0
	s_nop 0
	s_nop 0
	s_nop 0
	s_nop 0
	s_nop 0
	s_nop 0
	s_nop 0
	s_nop 0
	s_nop 0
	s_nop 0
	s_nop 0
	s_nop 0
	s_nop 0
	s_nop 0
	s_nop 0
	s_nop 0
	s_nop 0
	s_nop 0
	s_nop 0
	s_nop 0
	s_nop 0
	s_nop 0
	s_nop 0
	s_nop 0
	s_nop 0
	s_nop 0
	s_nop 0
	s_nop 0
	s_nop 0
	s_nop 0
	s_nop 0
	s_nop 0

; DI void attn_block(const Params& P, const Frame& F, int L, int b, int h, int qb, float lam, float oml) {
;     ...
;     const float* nw = P.in[I_DIFF_NORM] + L * 128;
;     f32x4 nwv[8];
; #pragma unroll
;     for (int d = 0; d < 8; ++d) nwv[d] = *(const f32x4*)(nw + 16 * d + 4 * rq);
;     float inv[2];
; #pragma unroll
;     for (int j = 0; j < 2; ++j) { float l = lrun[j]; l += shx<16>(l); l += shx<32>(l); inv[j] = __builtin_amdgcn_rcpf(l); }
;     const float inv1l = lam * inv[1];
;     float ss = 0.f;
; #pragma unroll
;     for (int d = 0; d < 8; ++d)
; #pragma unroll
;         for (int e = 0; e < 4; ++e) { const float o = O[0][d][e] * inv[0] - O[1][d][e] * inv1l; O[0][d][e] = o; ss += o * o; }
;     ss += shx<16>(ss); ss += shx<32>(ss);
;     const float r = oml * __builtin_amdgcn_rsqf(ss * (1.0f / 128.0f) + EPS);
.LBB0_1046:
	s_mov_b64 s[6:7], exec
	s_and_b64 exec, exec, s[4:5]
	v_mov_b32_e32 v252, 1
	global_atomic_add v252, v113, v252, s[0:1] sc0
	s_mov_b64 exec, s[6:7]
	global_load_dwordx4 v[0:3], v[134:135], off
	global_load_dwordx4 v[4:7], v[134:135], off offset:64
	ds_swizzle_b32 v8, v203 offset:swizzle(SWAP,16)
	ds_swizzle_b32 v9, v204 offset:swizzle(SWAP,16)
	s_lshl_b32 s38, s66, 1
	s_mov_b64 s[6:7], 0x61400400
	v_readlane_b32 s68, v254, 37
	s_waitcnt lgkmcnt(1)
	v_add_f32_e32 v24, v203, v8
	s_waitcnt lgkmcnt(0)
	v_add_f32_e32 v25, v204, v9
	ds_bpermute_b32 v26, v190, v24
	ds_bpermute_b32 v27, v190, v25
	global_load_dwordx4 v[8:11], v[134:135], off offset:128
	global_load_dwordx4 v[12:15], v[134:135], off offset:192
	global_load_dwordx4 v[16:19], v[134:135], off offset:256
	global_load_dwordx4 v[20:23], v[134:135], off offset:320
	v_readlane_b32 s70, v254, 39
	v_readlane_b32 s71, v254, 40
	s_waitcnt lgkmcnt(1)
	v_add_f32_e32 v24, v24, v26
	s_waitcnt lgkmcnt(0)
	v_add_f32_e32 v25, v25, v27
	v_rcp_f32_e32 v97, v25
	v_rcp_f32_e32 v96, v24
	global_load_dwordx4 v[24:27], v[134:135], off offset:384
	global_load_dwordx4 v[28:31], v[134:135], off offset:448
	v_readlane_b32 s72, v254, 41
	v_mul_f32_e32 v98, v197, v97
	v_pk_mul_f32 v[36:37], v[36:37], v[98:99] op_sel_hi:[1,0]
	v_pk_mul_f32 v[38:39], v[38:39], v[98:99] op_sel_hi:[1,0]
	v_pk_fma_f32 v[32:33], v[32:33], v[96:97], v[36:37] op_sel_hi:[1,0,1] neg_lo:[0,0,1] neg_hi:[0,0,1]
	v_pk_fma_f32 v[34:35], v[34:35], v[96:97], v[38:39] op_sel_hi:[1,0,1] neg_lo:[0,0,1] neg_hi:[0,0,1]
	v_pk_mul_f32 v[36:37], v[32:33], v[32:33]
	v_pk_mul_f32 v[56:57], v[56:57], v[98:99] op_sel_hi:[1,0]
	v_pk_mul_f32 v[38:39], v[34:35], v[34:35]
	v_add_f32_e32 v36, v36, v37
	v_pk_fma_f32 v[40:41], v[40:41], v[96:97], v[56:57] op_sel_hi:[1,0,1] neg_lo:[0,0,1] neg_hi:[0,0,1]
	v_add_f32_e32 v36, v38, v36
	v_pk_mul_f32 v[58:59], v[58:59], v[98:99] op_sel_hi:[1,0]
	v_pk_mul_f32 v[56:57], v[40:41], v[40:41]
	v_add_f32_e32 v36, v39, v36
	v_pk_fma_f32 v[42:43], v[42:43], v[96:97], v[58:59] op_sel_hi:[1,0,1] neg_lo:[0,0,1] neg_hi:[0,0,1]
	v_add_f32_e32 v36, v56, v36
	v_pk_mul_f32 v[80:81], v[80:81], v[98:99] op_sel_hi:[1,0]
	v_pk_mul_f32 v[58:59], v[42:43], v[42:43]
	v_add_f32_e32 v36, v57, v36
	v_pk_fma_f32 v[60:61], v[60:61], v[96:97], v[80:81] op_sel_hi:[1,0,1] neg_lo:[0,0,1] neg_hi:[0,0,1]
	v_add_f32_e32 v36, v58, v36
	v_pk_mul_f32 v[82:83], v[82:83], v[98:99] op_sel_hi:[1,0]
	v_pk_mul_f32 v[80:81], v[60:61], v[60:61]
	v_add_f32_e32 v36, v59, v36
	v_pk_fma_f32 v[62:63], v[62:63], v[96:97], v[82:83] op_sel_hi:[1,0,1] neg_lo:[0,0,1] neg_hi:[0,0,1]
	v_add_f32_e32 v36, v80, v36
	v_pk_mul_f32 v[64:65], v[64:65], v[98:99] op_sel_hi:[1,0]
	v_pk_mul_f32 v[82:83], v[62:63], v[62:63]
	v_add_f32_e32 v36, v81, v36
	v_pk_fma_f32 v[64:65], v[68:69], v[96:97], v[64:65] op_sel_hi:[1,0,1] neg_lo:[0,0,1] neg_hi:[0,0,1]
	v_add_f32_e32 v36, v82, v36
	v_pk_mul_f32 v[66:67], v[66:67], v[98:99] op_sel_hi:[1,0]
	v_pk_mul_f32 v[68:69], v[64:65], v[64:65]
	v_add_f32_e32 v36, v83, v36
	v_pk_fma_f32 v[66:67], v[70:71], v[96:97], v[66:67] op_sel_hi:[1,0,1] neg_lo:[0,0,1] neg_hi:[0,0,1]
	v_add_f32_e32 v36, v68, v36
	v_pk_mul_f32 v[48:49], v[48:49], v[98:99] op_sel_hi:[1,0]
	v_pk_mul_f32 v[70:71], v[66:67], v[66:67]
	v_add_f32_e32 v36, v69, v36
	v_pk_fma_f32 v[44:45], v[44:45], v[96:97], v[48:49] op_sel_hi:[1,0,1] neg_lo:[0,0,1] neg_hi:[0,0,1]
	v_add_f32_e32 v36, v70, v36
	v_pk_mul_f32 v[50:51], v[50:51], v[98:99] op_sel_hi:[1,0]
	v_pk_mul_f32 v[48:49], v[44:45], v[44:45]
	v_add_f32_e32 v36, v71, v36
	v_pk_fma_f32 v[46:47], v[46:47], v[96:97], v[50:51] op_sel_hi:[1,0,1] neg_lo:[0,0,1] neg_hi:[0,0,1]
	v_add_f32_e32 v36, v48, v36
	v_pk_mul_f32 v[72:73], v[72:73], v[98:99] op_sel_hi:[1,0]
	v_pk_mul_f32 v[50:51], v[46:47], v[46:47]
	v_add_f32_e32 v36, v49, v36
	v_pk_fma_f32 v[52:53], v[52:53], v[96:97], v[72:73] op_sel_hi:[1,0,1] neg_lo:[0,0,1] neg_hi:[0,0,1]
	v_add_f32_e32 v36, v50, v36
	v_pk_mul_f32 v[74:75], v[74:75], v[98:99] op_sel_hi:[1,0]
	v_pk_mul_f32 v[72:73], v[52:53], v[52:53]
	v_add_f32_e32 v36, v51, v36
	v_pk_fma_f32 v[54:55], v[54:55], v[96:97], v[74:75] op_sel_hi:[1,0,1] neg_lo:[0,0,1] neg_hi:[0,0,1]
	v_add_f32_e32 v36, v72, v36
	v_pk_mul_f32 v[84:85], v[84:85], v[98:99] op_sel_hi:[1,0]
	v_pk_mul_f32 v[74:75], v[54:55], v[54:55]
	v_add_f32_e32 v36, v73, v36
	v_pk_fma_f32 v[76:77], v[76:77], v[96:97], v[84:85] op_sel_hi:[1,0,1] neg_lo:[0,0,1] neg_hi:[0,0,1]
	v_add_f32_e32 v36, v74, v36
	v_pk_mul_f32 v[86:87], v[86:87], v[98:99] op_sel_hi:[1,0]
	v_pk_mul_f32 v[84:85], v[76:77], v[76:77]
	v_add_f32_e32 v36, v75, v36
	v_pk_fma_f32 v[78:79], v[78:79], v[96:97], v[86:87] op_sel_hi:[1,0,1] neg_lo:[0,0,1] neg_hi:[0,0,1]
	v_add_f32_e32 v36, v84, v36
	v_pk_mul_f32 v[92:93], v[92:93], v[98:99] op_sel_hi:[1,0]
	v_pk_mul_f32 v[86:87], v[78:79], v[78:79]
	v_add_f32_e32 v36, v85, v36
	v_pk_fma_f32 v[88:89], v[88:89], v[96:97], v[92:93] op_sel_hi:[1,0,1] neg_lo:[0,0,1] neg_hi:[0,0,1]
	v_add_f32_e32 v36, v86, v36
	v_pk_mul_f32 v[94:95], v[94:95], v[98:99] op_sel_hi:[1,0]
	v_pk_mul_f32 v[92:93], v[88:89], v[88:89]
	v_add_f32_e32 v36, v87, v36
	v_pk_fma_f32 v[90:91], v[90:91], v[96:97], v[94:95] op_sel_hi:[1,0,1] neg_lo:[0,0,1] neg_hi:[0,0,1]
	v_add_f32_e32 v36, v92, v36
	v_pk_mul_f32 v[94:95], v[90:91], v[90:91]
	v_add_f32_e32 v36, v93, v36
	v_add_f32_e32 v36, v94, v36
	v_add_f32_e32 v36, v95, v36
	v_mov_b32_e32 v37, v36
	v_readlane_b32 s73, v254, 42
	v_readlane_b32 s74, v254, 43
	v_readlane_b32 s75, v254, 44
	v_readlane_b32 s76, v254, 45
	s_waitcnt lgkmcnt(0)
; DI unsigned pk2(float lo, float hi) { const f32x2 v = {lo, hi}; return __builtin_bit_cast(unsigned, __builtin_convertvector(v, bf16x2_t)); }
; DI void attn_block(const Params& P, const Frame& F, int L, int b, int h, int qb, float lam, float oml) {
;     ...
;     const float r = oml * __builtin_amdgcn_rsqf(ss * (1.0f / 128.0f) + EPS);
;     unsigned long long ov[8];
; #pragma unroll
;     for (int d = 0; d < 8; ++d) ov[d] = (unsigned long long)pk2(O[0][d][0] * r * nwv[d][0], O[0][d][1] * r * nwv[d][1]) | ((unsigned long long)pk2(O[0][d][2] * r * nwv[d][2], O[0][d][3] * r * nwv[d][3]) << 32);
; #pragma unroll
;     for (int d = 0; d < 8; ++d) *(unsigned long long*)(MIX + (rowbase + qrow) * D + 512 + h * 128 + 16 * d + 4 * rq) = ov[d];
	s_nop 1
	v_permlane16_swap_b32_e32 v36, v37
	v_add_f32_e32 v36, v36, v37
	ds_bpermute_b32 v37, v190, v36
	v_readlane_b32 s77, v254, 46
	v_readlane_b32 s78, v254, 47
	v_readlane_b32 s79, v254, 48
	v_readlane_b32 s80, v254, 49
	s_waitcnt lgkmcnt(0)
	v_add_f32_e32 v36, v36, v37
	v_fmamk_f32 v36, v36, 0x3c000000, v179
	v_rsq_f32_e32 v36, v36
	v_readlane_b32 s81, v254, 50
	v_readlane_b32 s82, v254, 51
	v_readlane_b32 s83, v254, 52
	v_mul_f32_e32 v36, 0x3f4ccccd, v36
	v_pk_mul_f32 v[32:33], v[32:33], v[36:37] op_sel_hi:[1,0]
	v_readlane_b32 s69, v254, 38
	s_waitcnt vmcnt(7)
	v_pk_mul_f32 v[0:1], v[0:1], v[32:33]
	v_pk_mul_f32 v[32:33], v[34:35], v[36:37] op_sel_hi:[1,0]
	v_cvt_pk_bf16_f32 v0, v0, v1
	v_pk_mul_f32 v[2:3], v[2:3], v[32:33]
	s_nop 0
	v_cvt_pk_bf16_f32 v1, v2, v3
	v_pk_mul_f32 v[2:3], v[40:41], v[36:37] op_sel_hi:[1,0]
	s_waitcnt vmcnt(6)
	v_pk_mul_f32 v[2:3], v[4:5], v[2:3]
	v_pk_mul_f32 v[4:5], v[42:43], v[36:37] op_sel_hi:[1,0]
	v_cvt_pk_bf16_f32 v2, v2, v3
	v_pk_mul_f32 v[4:5], v[6:7], v[4:5]
	v_pk_mul_f32 v[6:7], v[62:63], v[36:37] op_sel_hi:[1,0]
	v_cvt_pk_bf16_f32 v3, v4, v5
	v_pk_mul_f32 v[4:5], v[60:61], v[36:37] op_sel_hi:[1,0]
	s_waitcnt vmcnt(5)
	v_pk_mul_f32 v[6:7], v[10:11], v[6:7]
	v_pk_mul_f32 v[4:5], v[8:9], v[4:5]
	v_pk_mul_f32 v[8:9], v[66:67], v[36:37] op_sel_hi:[1,0]
	v_cvt_pk_bf16_f32 v4, v4, v5
	v_cvt_pk_bf16_f32 v5, v6, v7
	v_pk_mul_f32 v[6:7], v[64:65], v[36:37] op_sel_hi:[1,0]
	s_waitcnt vmcnt(4)
	v_pk_mul_f32 v[8:9], v[14:15], v[8:9]
	v_pk_mul_f32 v[6:7], v[12:13], v[6:7]
	v_pk_mul_f32 v[10:11], v[46:47], v[36:37] op_sel_hi:[1,0]
	v_cvt_pk_bf16_f32 v6, v6, v7
	v_cvt_pk_bf16_f32 v7, v8, v9
	v_pk_mul_f32 v[8:9], v[44:45], v[36:37] op_sel_hi:[1,0]
	s_waitcnt vmcnt(3)
	v_pk_mul_f32 v[10:11], v[18:19], v[10:11]
	v_pk_mul_f32 v[8:9], v[16:17], v[8:9]
	v_pk_mul_f32 v[12:13], v[54:55], v[36:37] op_sel_hi:[1,0]
	v_cvt_pk_bf16_f32 v8, v8, v9
	v_cvt_pk_bf16_f32 v9, v10, v11
	v_pk_mul_f32 v[10:11], v[52:53], v[36:37] op_sel_hi:[1,0]
	s_waitcnt vmcnt(2)
	v_pk_mul_f32 v[12:13], v[22:23], v[12:13]
	v_pk_mul_f32 v[10:11], v[20:21], v[10:11]
	v_pk_mul_f32 v[14:15], v[78:79], v[36:37] op_sel_hi:[1,0]
	v_cvt_pk_bf16_f32 v10, v10, v11
	v_cvt_pk_bf16_f32 v11, v12, v13
	v_pk_mul_f32 v[12:13], v[76:77], v[36:37] op_sel_hi:[1,0]
	s_waitcnt vmcnt(1)
	v_pk_mul_f32 v[14:15], v[26:27], v[14:15]
	v_pk_mul_f32 v[12:13], v[24:25], v[12:13]
	v_pk_mul_f32 v[16:17], v[90:91], v[36:37] op_sel_hi:[1,0]
	v_cvt_pk_bf16_f32 v12, v12, v13
	v_cvt_pk_bf16_f32 v13, v14, v15
	v_pk_mul_f32 v[14:15], v[88:89], v[36:37] op_sel_hi:[1,0]
	s_waitcnt vmcnt(0)
	v_pk_mul_f32 v[16:17], v[30:31], v[16:17]
	v_pk_mul_f32 v[14:15], v[28:29], v[14:15]
	s_nop 0
	v_cvt_pk_bf16_f32 v14, v14, v15
	v_cvt_pk_bf16_f32 v15, v16, v17
	v_lshlrev_b64 v[16:17], 12, v[142:143]
	v_lshl_add_u64 v[16:17], s[54:55], 0, v[16:17]
	v_lshl_add_u64 v[16:17], v[16:17], 0, s[38:39]
	v_lshl_add_u64 v[16:17], v[130:131], 1, v[16:17]
	v_lshl_add_u64 v[18:19], v[16:17], 0, s[6:7]
	s_mov_b32 s6, 0x61400000
	v_add_co_u32_e32 v16, vcc, s6, v16
	s_mov_b64 s[6:7], 0
	s_nop 0
	v_addc_co_u32_e32 v17, vcc, 0, v17, vcc
	global_store_dwordx2 v[16:17], v[0:1], off offset:1024
	global_store_dwordx2 v[18:19], v[2:3], off offset:32
	global_store_dwordx2 v[18:19], v[4:5], off offset:64
	global_store_dwordx2 v[18:19], v[6:7], off offset:96
	global_store_dwordx2 v[18:19], v[8:9], off offset:128
	global_store_dwordx2 v[18:19], v[10:11], off offset:160
	global_store_dwordx2 v[18:19], v[12:13], off offset:192
	global_store_dwordx2 v[18:19], v[14:15], off offset:224

; DI void attn_block(const Params& P, const Frame& F, int L, int b, int h, int qb, float lam, float oml) {
;     ...
;                 for (int i = 0; i < 8; ++i) { mx = fmaxf(mx, x2[i].x); mx = fmaxf(mx, x2[i].y); }
;                 mx += base2;
;                 mx = fmaxf(mx, shx<16>(mx)); mx = fmaxf(mx, shx<32>(mx));
;                 const float mnew = fmaxf(mrun[j], mx), alpha = __builtin_amdgcn_exp2f(mrun[j] - mnew), msub = mnew - base2;
;                 const f32x2 ms2 = (f32x2){msub, msub}; f32x2 ps2 = (f32x2){0.f, 0.f};
; #pragma unroll
;                 for (int i = 0; i < 8; ++i) { const f32x2 t = x2[i] - ms2; x2[i] = (f32x2){__builtin_amdgcn_exp2f(t.x), __builtin_amdgcn_exp2f(t.y)}; ps2 = ps2 + x2[i]; }
;                 lrun[j] = lrun[j] * alpha + (ps2.x + ps2.y); mrun[j] = mnew;
;                 if (__builtin_amdgcn_ballot_w64(alpha != 1.0f) != 0ull) {
; #pragma unroll
;                     for (int d = 0; d < 8; ++d) O[j][d] = O[j][d] * alpha; }
.LBB0_1059:
	v_max3_f32 v162, v98, s57, v99
	v_max3_f32 v162, v162, v96, v97
	v_max3_f32 v162, v162, v102, v103
	v_max3_f32 v162, v162, v100, v101
	v_cvt_f32_i32_e32 v205, v201
	v_max3_f32 v162, v162, v106, v107
	v_max3_f32 v162, v162, v104, v105
	v_max3_f32 v162, v162, v110, v111
	v_max3_f32 v162, v162, v108, v109
	v_fmac_f32_e32 v162, v199, v205
	v_mov_b32_e32 v163, v162
	s_waitcnt lgkmcnt(0)
	v_max_f32_e32 v163, v163, v163
	s_nop 1
	v_permlane16_swap_b32_e32 v162, v163
	v_max_f32_e32 v162, v162, v163
	v_mov_b32_e32 v163, v162
	s_waitcnt lgkmcnt(0)
	s_nop 1
	v_permlane32_swap_b32_e32 v162, v163
	v_max3_f32 v202, v160, v162, v163
	v_sub_f32_e32 v160, v160, v202
	v_exp_f32_e32 v160, v160
	s_nop 0
	v_cmp_neq_f32_e32 vcc, 1.0, v160
	s_cbranch_vccz .LBB0_1061
	v_pk_mul_f32 v[34:35], v[34:35], v[160:161] op_sel_hi:[1,0]
	v_pk_mul_f32 v[32:33], v[32:33], v[160:161] op_sel_hi:[1,0]
	v_pk_mul_f32 v[42:43], v[42:43], v[160:161] op_sel_hi:[1,0]
	v_pk_mul_f32 v[40:41], v[40:41], v[160:161] op_sel_hi:[1,0]
	v_pk_mul_f32 v[62:63], v[62:63], v[160:161] op_sel_hi:[1,0]
	v_pk_mul_f32 v[60:61], v[60:61], v[160:161] op_sel_hi:[1,0]
	v_pk_mul_f32 v[70:71], v[70:71], v[160:161] op_sel_hi:[1,0]
	v_pk_mul_f32 v[68:69], v[68:69], v[160:161] op_sel_hi:[1,0]
	v_pk_mul_f32 v[46:47], v[46:47], v[160:161] op_sel_hi:[1,0]
	v_pk_mul_f32 v[44:45], v[44:45], v[160:161] op_sel_hi:[1,0]
	v_pk_mul_f32 v[54:55], v[54:55], v[160:161] op_sel_hi:[1,0]
	v_pk_mul_f32 v[52:53], v[52:53], v[160:161] op_sel_hi:[1,0]
	v_pk_mul_f32 v[78:79], v[78:79], v[160:161] op_sel_hi:[1,0]
	v_pk_mul_f32 v[76:77], v[76:77], v[160:161] op_sel_hi:[1,0]
	v_pk_mul_f32 v[90:91], v[90:91], v[160:161] op_sel_hi:[1,0]
	v_pk_mul_f32 v[88:89], v[88:89], v[160:161] op_sel_hi:[1,0]

; DI void attn_block(const Params& P, const Frame& F, int L, int b, int h, int qb, float lam, float oml) {
;     ...
;                 for (int i = 0; i < 8; ++i) { mx = fmaxf(mx, x2[i].x); mx = fmaxf(mx, x2[i].y); }
;                 mx += base2;
;                 mx = fmaxf(mx, shx<16>(mx)); mx = fmaxf(mx, shx<32>(mx));
;                 const float mnew = fmaxf(mrun[j], mx), alpha = __builtin_amdgcn_exp2f(mrun[j] - mnew), msub = mnew - base2;
;                 const f32x2 ms2 = (f32x2){msub, msub}; f32x2 ps2 = (f32x2){0.f, 0.f};
; #pragma unroll
;                 for (int i = 0; i < 8; ++i) { const f32x2 t = x2[i] - ms2; x2[i] = (f32x2){__builtin_amdgcn_exp2f(t.x), __builtin_amdgcn_exp2f(t.y)}; ps2 = ps2 + x2[i]; }
;                 lrun[j] = lrun[j] * alpha + (ps2.x + ps2.y); mrun[j] = mnew;
;                 if (__builtin_amdgcn_ballot_w64(alpha != 1.0f) != 0ull) {
; #pragma unroll
;                     for (int d = 0; d < 8; ++d) O[j][d] = O[j][d] * alpha; }
.LBB0_1063:
	v_max3_f32 v192, v166, s57, v167
	v_max3_f32 v192, v192, v162, v163
	v_max3_f32 v192, v192, v168, v169
	v_max3_f32 v192, v192, v164, v165
	v_max3_f32 v192, v192, v172, v173
	v_max3_f32 v192, v192, v170, v171
	v_max3_f32 v192, v192, v174, v175
	v_mul_f32_e32 v207, v199, v205
	v_max3_f32 v192, v192, v176, v177
	v_add_f32_e32 v192, v207, v192
	v_mov_b32_e32 v205, v192
	s_waitcnt lgkmcnt(0)
	v_max_f32_e32 v205, v205, v205
	s_nop 1
	v_permlane16_swap_b32_e32 v192, v205
	v_max_f32_e32 v192, v192, v205
	v_mov_b32_e32 v205, v192
	s_waitcnt lgkmcnt(0)
	s_nop 1
	v_permlane32_swap_b32_e32 v192, v205
	v_max3_f32 v205, v178, v192, v205
	v_sub_f32_e32 v178, v178, v205
	v_exp_f32_e32 v178, v178
	s_nop 0
	v_cmp_neq_f32_e32 vcc, 1.0, v178
	s_cbranch_vccz .LBB0_1065
	v_pk_mul_f32 v[38:39], v[38:39], v[178:179] op_sel_hi:[1,0]
	v_pk_mul_f32 v[36:37], v[36:37], v[178:179] op_sel_hi:[1,0]
	v_pk_mul_f32 v[58:59], v[58:59], v[178:179] op_sel_hi:[1,0]
	v_pk_mul_f32 v[56:57], v[56:57], v[178:179] op_sel_hi:[1,0]
	v_pk_mul_f32 v[82:83], v[82:83], v[178:179] op_sel_hi:[1,0]
	v_pk_mul_f32 v[80:81], v[80:81], v[178:179] op_sel_hi:[1,0]
	v_pk_mul_f32 v[66:67], v[66:67], v[178:179] op_sel_hi:[1,0]
	v_pk_mul_f32 v[64:65], v[64:65], v[178:179] op_sel_hi:[1,0]
	v_pk_mul_f32 v[50:51], v[50:51], v[178:179] op_sel_hi:[1,0]
	v_pk_mul_f32 v[48:49], v[48:49], v[178:179] op_sel_hi:[1,0]
	v_pk_mul_f32 v[74:75], v[74:75], v[178:179] op_sel_hi:[1,0]
	v_pk_mul_f32 v[72:73], v[72:73], v[178:179] op_sel_hi:[1,0]
	v_pk_mul_f32 v[86:87], v[86:87], v[178:179] op_sel_hi:[1,0]
	v_pk_mul_f32 v[84:85], v[84:85], v[178:179] op_sel_hi:[1,0]
	v_pk_mul_f32 v[94:95], v[94:95], v[178:179] op_sel_hi:[1,0]
	v_pk_mul_f32 v[92:93], v[92:93], v[178:179] op_sel_hi:[1,0]

.LBB0_1115:
	s_cmp_lt_u32 s3, 0x40001
	s_mov_b64 s[18:19], 0
	s_cselect_b64 s[20:21], -1, 0
	s_mov_b64 s[22:23], -1
	s_and_b64 vcc, exec, s[20:21]
	s_cbranch_vccnz .LBB0_1112
	s_branch .LBB0_1109
	s_nop 0
	s_nop 0
	s_nop 0
	s_nop 0
	s_nop 0
	s_nop 0
	s_nop 0
	s_nop 0
	s_nop 0
	s_nop 0
	s_nop 0
	s_nop 0
	s_nop 0
	s_nop 0
	s_nop 0
	s_nop 0
	s_nop 0
	s_nop 0
	s_nop 0
	s_nop 0
	s_nop 0
	s_nop 0
	s_nop 0
	s_nop 0
	s_nop 0
	s_nop 0
	s_nop 0
	s_nop 0
	s_nop 0
	s_nop 0
	s_nop 0
	s_nop 0
	s_nop 0
	s_nop 0
	s_nop 0
	s_nop 0
	s_nop 0
	s_nop 0
	s_nop 0
	s_nop 0
.LBB0_1116:
	s_or_b64 exec, exec, s[14:15]
	s_and_b64 s[14:15], s[16:17], exec

; DI unsigned pk2(float lo, float hi) { const f32x2 v = {lo, hi}; return __builtin_bit_cast(unsigned, __builtin_convertvector(v, bf16x2_t)); }
; template <int MODE, bool SB  > DI void norm_phase(const Params& P, const Frame& F, int L, const void* src_, const float* gain, bool combine) {
;     ...
;     for (int row = r_lo + F.wave; row < r_hi; row += NWAVES) {
;         f32x4 v[8];
; #pragma unroll
;         for (int j = 0; j < 8; ++j) { if constexpr (SB) v[j] = (f32x4){bflo(vb[j].x), bfhi(vb[j].x), bflo(vb[j].y), bfhi(vb[j].y)}; else v[j] = vn[j]; }
;         { const int rnx = (row + NWAVES < r_hi) ? row + NWAVES : row;
; #pragma unroll
;           for (int j = 0; j < 8; ++j) { if constexpr (SB) vb[j] = *(const u32x2*)(srcb + (size_t)rnx * D + 4 * F.lane + 256 * j); else vn[j] = *(const f32x4*)(src + (size_t)rnx * D + 4 * F.lane + 256 * j); } }
;         if (MODE == 3 && combine) {
;             const int* SLOT = (const int*)(ws + WS_SLOT); const float* TOPW = (const float*)(ws + WS_TOPW); const bf16* Y = (const bf16*)(ws + WS_T + T_YPERM);
;             const int s1 = SLOT[row * 2], s2 = SLOT[row * 2 + 1]; const float w1 = TOPW[row * 2], w2 = TOPW[row * 2 + 1];
;             u32x2 ya[8], yb[8];
; #pragma unroll
;             for (int j = 0; j < 8; ++j) { ya[j] = *(const u32x2*)(Y + (size_t)s1 * D + 4 * F.lane + 256 * j); yb[j] = *(const u32x2*)(Y + (size_t)s2 * D + 4 * F.lane + 256 * j); }
; #pragma unroll
;             for (int j = 0; j < 8; ++j) { const f32x4 y1 = (f32x4){bflo(ya[j].x), bfhi(ya[j].x), bflo(ya[j].y), bfhi(ya[j].y)}, y2 = (f32x4){bflo(yb[j].x), bfhi(yb[j].x), bflo(yb[j].y), bfhi(yb[j].y)};
;                 v[j] = v[j] + w1 * y1 + w2 * y2;
;                 const u32x2 hb = {pk2(v[j][0], v[j][1]), pk2(v[j][2], v[j][3])}; *(u32x2*)(const_cast<bf16*>(srcb) + (size_t)row * D + 4 * F.lane + 256 * j) = hb;
;                 v[j] = (f32x4){bflo(hb.x), bfhi(hb.x), bflo(hb.y), bfhi(hb.y)}; }
;         }
;         float ss = 0.f;
; #pragma unroll
;         for (int j = 0; j < 8; ++j) ss += (v[j][0] * v[j][0] + v[j][1] * v[j][1]) + (v[j][2] * v[j][2] + v[j][3] * v[j][3]);
;         const float rstd = 1.0f / sqrtf(wave_sum(ss) * (1.0f / D) + EPS);
; #pragma unroll
;         for (int j = 0; j < 8; ++j) v[j] = v[j] * rstd * g[j];
.LBB0_1308:
	s_add_i32 s6, s10, 8
	s_waitcnt vmcnt(3)
	v_lshlrev_b32_e32 v42, 16, v40
	v_and_b32_e32 v43, 0xffff0000, v40
	v_lshlrev_b32_e32 v40, 16, v62
	v_and_b32_e32 v71, 0xffff0000, v62
	v_lshlrev_b32_e32 v46, 16, v63
	v_and_b32_e32 v47, 0xffff0000, v63
	v_lshlrev_b32_e32 v38, 16, v36
	v_and_b32_e32 v39, 0xffff0000, v36
	v_lshlrev_b32_e32 v36, 16, v60
	v_and_b32_e32 v89, 0xffff0000, v60
	v_lshlrev_b32_e32 v44, 16, v61
	v_and_b32_e32 v45, 0xffff0000, v61
	s_waitcnt vmcnt(0)
	v_and_b32_e32 v61, 0xffff0000, v58
	v_and_b32_e32 v60, 0xffff0000, v54
	v_and_b32_e32 v63, 0xffff0000, v59
	v_and_b32_e32 v62, 0xffff0000, v55
	s_cmp_lt_i32 s6, s3
	v_lshlrev_b32_e32 v49, 16, v58
	v_lshlrev_b32_e32 v48, 16, v54
	v_lshlrev_b32_e32 v51, 16, v59
	v_lshlrev_b32_e32 v50, 16, v55
	v_lshlrev_b32_e32 v65, 16, v53
	v_lshlrev_b32_e32 v64, 16, v52
	v_and_b32_e32 v53, 0xffff0000, v53
	v_and_b32_e32 v52, 0xffff0000, v52
	v_pk_mul_f32 v[72:73], v[60:61], v[60:61]
	v_pk_mul_f32 v[74:75], v[62:63], v[62:63]
	s_cselect_b64 s[4:5], -1, 0
	v_lshlrev_b32_e32 v54, 16, v41
	v_pk_mul_f32 v[76:77], v[52:53], v[52:53]
	v_pk_fma_f32 v[72:73], v[48:49], v[48:49], v[72:73]
	v_pk_fma_f32 v[74:75], v[50:51], v[50:51], v[74:75]
	s_and_b64 s[4:5], s[4:5], exec
	v_and_b32_e32 v55, 0xffff0000, v41
	v_lshlrev_b32_e32 v67, 16, v57
	v_lshlrev_b32_e32 v66, 16, v56
	v_and_b32_e32 v57, 0xffff0000, v57
	v_and_b32_e32 v56, 0xffff0000, v56
	v_lshlrev_b32_e32 v58, 16, v37
	v_mul_f32_e32 v41, v42, v42
	v_mul_f32_e32 v79, v43, v43
	v_mul_f32_e32 v80, v54, v54
	v_mov_b32_e32 v78, v40
	v_mov_b32_e32 v92, v49
	v_mov_b32_e32 v93, v61
	v_mov_b32_e32 v96, v64
	v_mov_b32_e32 v97, v52
	v_mov_b32_e32 v52, v65
	v_pk_fma_f32 v[64:65], v[64:65], v[64:65], v[76:77]
	v_mov_b32_e32 v49, v60
	v_pk_add_f32 v[60:61], v[72:73], v[74:75]
	s_cselect_b32 s14, s6, s10
	v_and_b32_e32 v59, 0xffff0000, v37
	v_pk_mul_f32 v[84:85], v[56:57], v[56:57]
	v_mul_f32_e32 v37, v38, v38
	v_mul_f32_e32 v87, v39, v39
	v_mul_f32_e32 v88, v58, v58
	v_mov_b32_e32 v86, v36
	v_mov_b32_e32 v94, v51
	v_mov_b32_e32 v95, v63
	v_pk_fma_f32 v[76:77], v[54:55], v[54:55], v[80:81] op_sel_hi:[1,1,0]
	v_pk_add_f32 v[78:79], v[40:41], v[78:79]
	v_mov_b32_e32 v51, v62
	v_pk_add_f32 v[62:63], v[64:65], v[64:65] op_sel_hi:[0,1]
	v_pk_add_f32 v[60:61], v[60:61], v[60:61] op_sel_hi:[0,1]
	s_ashr_i32 s15, s14, 31
	v_mul_f32_e32 v82, v40, v40
	v_mov_b32_e32 v98, v66
	v_mov_b32_e32 v99, v56
	v_mov_b32_e32 v56, v67
	v_pk_fma_f32 v[66:67], v[66:67], v[66:67], v[84:85]
	v_pk_fma_f32 v[80:81], v[58:59], v[58:59], v[88:89] op_sel_hi:[1,1,0]
	v_pk_add_f32 v[84:85], v[36:37], v[86:87]
	v_mul_f32_e32 v76, v71, v71
	v_mov_b32_e32 v83, v79
	v_mul_f32_e32 v62, v46, v46
	s_mov_b32 s10, s6
	v_mul_f32_e32 v60, v47, v47
	s_lshl_b64 s[6:7], s[14:15], 12
	v_mul_f32_e32 v90, v36, v36
	v_pk_add_f32 v[64:65], v[66:67], v[66:67] op_sel_hi:[0,1]
	v_mul_f32_e32 v80, v89, v89
	v_mov_b32_e32 v91, v85
	v_pk_add_f32 v[66:67], v[82:83], v[76:77]
	v_pk_add_f32 v[60:61], v[62:63], v[60:61]
	v_lshl_add_u64 v[74:75], v[32:33], 0, s[6:7]
	v_pk_add_f32 v[72:73], v[90:91], v[80:81]
	v_pk_add_f32 v[66:67], v[66:67], v[60:61]
	global_load_dwordx2 v[76:77], v[74:75], off
	global_load_dwordx2 v[78:79], v[74:75], off offset:512
	global_load_dwordx2 v[80:81], v[74:75], off offset:1024
	global_load_dwordx2 v[82:83], v[74:75], off offset:1536
	global_load_dwordx2 v[62:63], v[74:75], off offset:2048
	global_load_dwordx2 v[84:85], v[74:75], off offset:2560
	global_load_dwordx2 v[86:87], v[74:75], off offset:3072
	global_load_dwordx2 v[60:61], v[74:75], off offset:3584
	v_pk_add_f32 v[66:67], v[66:67], v[66:67] op_sel_hi:[0,1]
	v_mul_f32_e32 v64, v44, v44
	v_mul_f32_e32 v66, v45, v45
	v_pk_add_f32 v[64:65], v[64:65], v[66:67]
	v_mov_b32_e32 v41, v71
	v_pk_add_f32 v[64:65], v[72:73], v[64:65]
	v_mov_b32_e32 v100, 0
	v_add_f32_e32 v64, v64, v65
	v_mov_b32_e32 v37, v89
	v_mov_b32_e32 v101, 0
	v_add_f32_dpp v64, v64, v64 quad_perm:[1,0,3,2] row_mask:0xf bank_mask:0xf bound_ctrl:1
	v_mov_b32_e32 v102, 0
	v_mov_b32_e32 v103, 0
	v_add_f32_dpp v64, v64, v64 quad_perm:[2,3,0,1] row_mask:0xf bank_mask:0xf bound_ctrl:1
	ds_swizzle_b32 v65, v64 offset:swizzle(SWAP,4)
	v_mov_b32_e32 v104, 0
	v_mov_b32_e32 v105, 0
	v_mov_b32_e32 v106, 0
	v_mov_b32_e32 v107, 0
	s_waitcnt lgkmcnt(0)
	v_add_f32_e32 v64, v64, v65
	ds_swizzle_b32 v65, v64 offset:swizzle(SWAP,8)
	s_waitcnt lgkmcnt(0)
	v_add_f32_e32 v64, v64, v65
	v_mov_b32_e32 v65, v64
	s_waitcnt lgkmcnt(0)
	s_nop 1
	v_permlane16_swap_b32_e32 v64, v65
	v_add_f32_e32 v64, v64, v65
	v_mov_b32_e32 v65, v64
	s_waitcnt lgkmcnt(0)
; DI unsigned pk4_fp8(float a, float b, float c, float d) { unsigned w = 0u; w = __builtin_amdgcn_cvt_pk_fp8_f32(a, b, w, false); w = __builtin_amdgcn_cvt_pk_fp8_f32(c, d, w, true); return w; }
; DI float wave_sum(float v) { v += shx<1>(v); v += shx<2>(v); v += shx<4>(v); v += shx<8>(v); v += shx<16>(v); v += shx<32>(v); return v; }
; template <int MODE, bool SB  > DI void norm_phase(const Params& P, const Frame& F, int L, const void* src_, const float* gain, bool combine) {
;     ...
;         const float rstd = 1.0f / sqrtf(wave_sum(ss) * (1.0f / D) + EPS);
; #pragma unroll
;         for (int j = 0; j < 8; ++j) v[j] = v[j] * rstd * g[j];
;         if (MODE == 4) {
; #pragma unroll
;             for (int j = 0; j < 8; ++j) *(f32x4*)(P.out + (size_t)row * D + 4 * F.lane + 256 * j) = v[j];
;         } else if (MODE == 0 || MODE == 2 || (MODE == 3 && L == 1)) {
;             unsigned* o4 = (unsigned*)((unsigned char*)HN + (size_t)row * D) + F.lane; const float hs = (float)(1 << LS_HN);
; #pragma unroll
;             for (int j = 0; j < 8; ++j) o4[64 * j] = pk4_fp8(v[j][0] * hs, v[j][1] * hs, v[j][2] * hs, v[j][3] * hs);
	s_nop 1
	v_permlane32_swap_b32_e32 v64, v65
	v_add_f32_e32 v64, v64, v65
	v_fmamk_f32 v64, v64, 0x3a000000, v69
	v_mul_f32_e32 v65, 0x4f800000, v64
	v_cmp_gt_f32_e32 vcc, s9, v64
	s_nop 1
	v_cndmask_b32_e32 v64, v64, v65, vcc
	v_sqrt_f32_e32 v65, v64
	s_nop 0
	v_add_u32_e32 v66, -1, v65
	v_add_u32_e32 v67, 1, v65
	v_fma_f32 v71, -v66, v65, v64
	v_fma_f32 v72, -v67, v65, v64
	v_cmp_ge_f32_e64 s[6:7], 0, v71
	s_nop 1
	v_cndmask_b32_e64 v65, v65, v66, s[6:7]
	v_cmp_lt_f32_e64 s[6:7], 0, v72
	s_nop 1
	v_cndmask_b32_e64 v65, v65, v67, s[6:7]
	v_mul_f32_e32 v66, 0x37800000, v65
	v_cndmask_b32_e32 v65, v65, v66, vcc
	v_cmp_class_f32_e32 vcc, v64, v70
	s_nop 1
	v_cndmask_b32_e32 v64, v65, v64, vcc
	v_div_scale_f32 v65, s[6:7], v64, v64, 1.0
	v_rcp_f32_e32 v67, v65
	v_div_scale_f32 v66, vcc, 1.0, v64, 1.0
	v_fma_f32 v71, -v65, v67, 1.0
	v_fmac_f32_e32 v67, v71, v67
	v_mul_f32_e32 v71, v66, v67
	v_fma_f32 v72, -v65, v71, v66
	v_fmac_f32_e32 v71, v72, v67
	v_fma_f32 v65, -v65, v71, v66
	v_div_fmas_f32 v65, v65, v67, v71
	v_div_fixup_f32 v64, v65, v64, 1.0
	v_pk_mul_f32 v[66:67], v[92:93], v[64:65] op_sel_hi:[1,0]
	v_pk_mul_f32 v[48:49], v[48:49], v[64:65] op_sel_hi:[1,0]
	v_pk_mul_f32 v[66:67], v[0:1], v[66:67]
	v_pk_mul_f32 v[72:73], v[94:95], v[64:65] op_sel_hi:[1,0]
	v_pk_mul_f32 v[74:75], v[64:65], v[96:97] op_sel_hi:[0,1]
	v_pk_mul_f32 v[48:49], v[4:5], v[48:49]
	v_mul_f32_e32 v66, 4.0, v66
	v_mul_f32_e32 v67, 4.0, v67
	v_pk_mul_f32 v[50:51], v[50:51], v[64:65] op_sel_hi:[1,0]
	v_pk_mul_f32 v[52:53], v[64:65], v[52:53] op_sel_hi:[0,1]
	v_pk_mul_f32 v[42:43], v[42:43], v[64:65] op_sel_hi:[1,0]
	v_pk_mul_f32 v[54:55], v[54:55], v[64:65] op_sel_hi:[1,0]
	v_pk_mul_f32 v[40:41], v[40:41], v[64:65] op_sel_hi:[1,0]
	v_pk_mul_f32 v[46:47], v[46:47], v[64:65] op_sel_hi:[1,0]
	v_pk_mul_f32 v[88:89], v[64:65], v[98:99] op_sel_hi:[0,1]
	v_pk_mul_f32 v[56:57], v[64:65], v[56:57] op_sel_hi:[0,1]
	v_pk_mul_f32 v[38:39], v[38:39], v[64:65] op_sel_hi:[1,0]
	v_pk_mul_f32 v[58:59], v[58:59], v[64:65] op_sel_hi:[1,0]
	v_pk_mul_f32 v[36:37], v[36:37], v[64:65] op_sel_hi:[1,0]
	v_pk_mul_f32 v[44:45], v[44:45], v[64:65] op_sel_hi:[1,0]
	v_pk_mul_f32 v[64:65], v[2:3], v[72:73]
	v_pk_mul_f32 v[72:73], v[8:9], v[74:75]
	v_mul_f32_e32 v48, 4.0, v48
	v_mul_f32_e32 v49, 4.0, v49
	v_cvt_pk_fp8_f32 v100, v66, v67
	v_pk_mul_f32 v[42:43], v[12:13], v[42:43]
	v_mul_f32_e32 v71, 4.0, v72
	v_mul_f32_e32 v72, 4.0, v73
	v_cvt_pk_fp8_f32 v101, v48, v49
	v_pk_mul_f32 v[40:41], v[16:17], v[40:41]
	v_pk_mul_f32 v[74:75], v[20:21], v[88:89]
	v_pk_mul_f32 v[38:39], v[24:25], v[38:39]
	v_pk_mul_f32 v[36:37], v[28:29], v[36:37]
	v_mul_f32_e32 v42, 4.0, v42
	v_mul_f32_e32 v43, 4.0, v43
	v_cvt_pk_fp8_f32 v102, v71, v72
	v_pk_mul_f32 v[50:51], v[6:7], v[50:51]
	v_mul_f32_e32 v64, 4.0, v64
	v_mul_f32_e32 v65, 4.0, v65
	v_mul_f32_e32 v40, 4.0, v40
	v_mul_f32_e32 v41, 4.0, v41
	v_mul_f32_e32 v73, 4.0, v74
	v_mul_f32_e32 v74, 4.0, v75
	v_mul_f32_e32 v38, 4.0, v38
	v_mul_f32_e32 v39, 4.0, v39
	v_mul_f32_e32 v36, 4.0, v36
	v_mul_f32_e32 v37, 4.0, v37
	v_cvt_pk_fp8_f32 v103, v42, v43
	v_pk_mul_f32 v[52:53], v[10:11], v[52:53]
	v_mul_f32_e32 v50, 4.0, v50
	v_mul_f32_e32 v51, 4.0, v51
	v_cvt_pk_fp8_f32 v104, v40, v41
	v_cvt_pk_fp8_f32 v105, v73, v74
	v_cvt_pk_fp8_f32 v106, v38, v39
	v_cvt_pk_fp8_f32 v107, v36, v37
	v_cvt_pk_fp8_f32 v100, v64, v65 op_sel:[0,0,1]
	v_pk_mul_f32 v[54:55], v[14:15], v[54:55]
	v_mul_f32_e32 v52, 4.0, v52
	v_mul_f32_e32 v53, 4.0, v53
	v_cvt_pk_fp8_f32 v101, v50, v51 op_sel:[0,0,1]
	v_pk_mul_f32 v[46:47], v[18:19], v[46:47]
	v_pk_mul_f32 v[56:57], v[22:23], v[56:57]
	v_pk_mul_f32 v[58:59], v[26:27], v[58:59]
	v_pk_mul_f32 v[44:45], v[30:31], v[44:45]
	v_mul_f32_e32 v54, 4.0, v54
	v_mul_f32_e32 v55, 4.0, v55
	v_cvt_pk_fp8_f32 v102, v52, v53 op_sel:[0,0,1]
	v_mul_f32_e32 v46, 4.0, v46
	v_mul_f32_e32 v47, 4.0, v47
	v_mul_f32_e32 v56, 4.0, v56
	v_mul_f32_e32 v57, 4.0, v57
	v_mul_f32_e32 v58, 4.0, v58
	v_mul_f32_e32 v59, 4.0, v59
	v_mul_f32_e32 v44, 4.0, v44
	v_mul_f32_e32 v45, 4.0, v45
	v_cvt_pk_fp8_f32 v103, v54, v55 op_sel:[0,0,1]
	v_cvt_pk_fp8_f32 v104, v46, v47 op_sel:[0,0,1]
	v_cvt_pk_fp8_f32 v105, v56, v57 op_sel:[0,0,1]
	v_cvt_pk_fp8_f32 v106, v58, v59 op_sel:[0,0,1]
	v_cvt_pk_fp8_f32 v107, v44, v45 op_sel:[0,0,1]
	global_store_dword v[34:35], v100, off
	global_store_dword v[34:35], v101, off offset:256
	global_store_dword v[34:35], v102, off offset:512
	global_store_dword v[34:35], v103, off offset:768
	global_store_dword v[34:35], v104, off offset:1024
	global_store_dword v[34:35], v105, off offset:1280
	global_store_dword v[34:35], v106, off offset:1536
	global_store_dword v[34:35], v107, off offset:1792
	v_lshl_add_u64 v[34:35], v[34:35], 0, s[12:13]
	s_waitcnt vmcnt(9)
	v_mov_b64_e32 v[36:37], v[86:87]
	v_mov_b64_e32 v[56:57], v[84:85]
	v_mov_b64_e32 v[40:41], v[82:83]
	v_mov_b64_e32 v[52:53], v[80:81]
	v_mov_b64_e32 v[54:55], v[78:79]
	v_mov_b64_e32 v[58:59], v[76:77]
	s_mov_b64 vcc, s[4:5]
	s_cbranch_vccnz .LBB0_1308

.LBB0_1354:
	s_cmp_lt_u32 s3, 0x40001
	s_mov_b64 s[22:23], 0
	s_cselect_b64 s[24:25], -1, 0
	s_mov_b64 s[26:27], -1
	s_and_b64 vcc, exec, s[24:25]
	s_cbranch_vccnz .LBB0_1351
	s_branch .LBB0_1348
	s_nop 0
	s_nop 0
	s_nop 0
	s_nop 0
	s_nop 0
	s_nop 0
	s_nop 0
	s_nop 0
	s_nop 0
	s_nop 0
	s_nop 0
	s_nop 0
	s_nop 0
	s_nop 0
	s_nop 0
	s_nop 0
	s_nop 0
	s_nop 0
	s_nop 0
	s_nop 0
	s_nop 0
	s_nop 0
	s_nop 0
	s_nop 0
	s_nop 0
	s_nop 0
	s_nop 0
	s_nop 0
	s_nop 0
	s_nop 0
	s_nop 0
	s_nop 0
	s_nop 0
	s_nop 0
	s_nop 0
	s_nop 0
	s_nop 0
	s_nop 0
	s_nop 0
	s_nop 0
	s_nop 0
	s_nop 0
	s_nop 0
	s_nop 0
	s_nop 0
	s_nop 0
	s_nop 0
	s_nop 0
	s_nop 0
	s_nop 0
	s_nop 0
	s_nop 0
	s_nop 0
	s_nop 0
	s_nop 0
	s_nop 0
	s_nop 0
	s_nop 0
	s_nop 0
	s_nop 0
	s_nop 0
	s_nop 0

;     __device__ __forceinline__ void operator()(const f32x4 (&acc)[2][2][4][2], const Unit& u, int wr, int wc, int fr, int fq) const {
;     ...
;                     for (int bj = 0; bj < 2; ++bj) { const size_t off = (size_t)(row0 + ai * HALF + (m0 + mm) * 16) * ld + col0 + bj * HALF;
;                         if constexpr (RF32) { rf[mm][bj][0] = *(const f32x4*)((const float*)R + off); rf[mm][bj][1] = *(const f32x4*)((const float*)R + off + 4); }
;                         else rb[mm][bj] = *(const u32x4*)((const bf16_t*)R + off);
;                         if constexpr (MODE == 2) pb[mm][bj] = *(const u32x4*)(P + off); }
; #pragma unroll
;                 for (int mm = 0; mm < MB; ++mm) { float ssum = 0.f; float rr = 1.0f; if constexpr (RS) rr = rs[(row0 + ai * HALF + (m0 + mm) * 16) & 2047];
; #pragma unroll
;                     for (int bj = 0; bj < 2; ++bj) { const size_t off = (size_t)(row0 + ai * HALF + (m0 + mm) * 16) * ld + col0 + bj * HALF;
;                         f32x4 r0, r1;
;                         if constexpr (RF32) { r0 = rf[mm][bj][0]; r1 = rf[mm][bj][1]; }
;                         else { const u32x4 w = rb[mm][bj]; r0 = (f32x4){lo_(w.x), hi_(w.x), lo_(w.y), hi_(w.y)}; r1 = (f32x4){lo_(w.z), hi_(w.z), lo_(w.w), hi_(w.w)}; }
;                         f32x4 v0 = acc[ai][bj][m0 + mm][0], v1 = acc[ai][bj][m0 + mm][1]; if constexpr (RS) { v0 = v0 * rr; v1 = v1 * rr; }
;                         if constexpr (MODE == 2) { const u32x4 w = pb[mm][bj]; const f32x4 p0 = {lo_(w.x), hi_(w.x), lo_(w.y), hi_(w.y)}, p1 = {lo_(w.z), hi_(w.z), lo_(w.w), hi_(w.w)};
; #pragma unroll
;                             for (int j = 0; j < 4; ++j) { v0[j] = p0[j] * __builtin_amdgcn_rcpf(1.0f + __expf(-v0[j])); v1[j] = p1[j] * __builtin_amdgcn_rcpf(1.0f + __expf(-v1[j])); } }
;                         v0 = v0 + r0; v1 = v1 + r1;
;                         u32x4 o; o.x = cvt_pk_bf16(v0[0], v0[1]); o.y = cvt_pk_bf16(v0[2], v0[3]); o.z = cvt_pk_bf16(v1[0], v1[1]); o.w = cvt_pk_bf16(v1[2], v1[3]);
;                         *(u32x4*)(C + off) = o;
;                         if constexpr (EMIT) { const float a0 = lo_(o.x), a1 = hi_(o.x), a2 = lo_(o.y), a3 = hi_(o.y), a4 = lo_(o.z), a5 = hi_(o.z), a6 = lo_(o.w), a7 = hi_(o.w);
;                             ssum += ((a0 * a0 + a1 * a1) + (a2 * a2 + a3 * a3)) + ((a4 * a4 + a5 * a5) + (a6 * a6 + a7 * a7)); } }
.LBB0_1457:
	v_mov_b32_e32 v181, v168
	s_lshl_b32 s11, s11, 8
	s_add_i32 s14, s11, s38
	v_and_b32_e32 v182, 15, v181
	v_or_b32_e32 v160, s14, v182
	s_lshl_b32 s14, s10, 8
	v_ashrrev_i32_e32 v128, 1, v181
	s_or_b32 s14, s14, s39
	v_and_b32_e32 v128, -8, v128
	v_add_u32_e32 v156, s14, v128
	v_ashrrev_i32_e32 v157, 31, v156
	v_lshlrev_b64 v[188:189], 1, v[156:157]
	v_ashrrev_i32_e32 v161, 31, v160
	v_lshl_add_u64 v[158:159], s[0:1], 0, v[188:189]
	v_lshlrev_b64 v[190:191], 12, v[160:161]
	v_lshl_add_u64 v[128:129], v[158:159], 0, v[190:191]
	global_load_dwordx4 v[184:187], v[128:129], off
	global_load_dwordx4 v[152:155], v[128:129], off offset:256
	v_or_b32_e32 v166, 16, v160
	v_ashrrev_i32_e32 v167, 31, v166
	v_lshlrev_b64 v[128:129], 12, v[166:167]
	v_or_b32_e32 v164, 32, v160
	v_lshl_add_u64 v[128:129], v[158:159], 0, v[128:129]
	v_ashrrev_i32_e32 v165, 31, v164
	global_load_dwordx4 v[148:151], v[128:129], off
	global_load_dwordx4 v[144:147], v[128:129], off offset:256
	v_lshlrev_b64 v[128:129], 12, v[164:165]
	v_or_b32_e32 v162, 48, v160
	v_lshl_add_u64 v[128:129], v[158:159], 0, v[128:129]
	v_ashrrev_i32_e32 v163, 31, v162
	global_load_dwordx4 v[140:143], v[128:129], off
	global_load_dwordx4 v[136:139], v[128:129], off offset:256
	v_lshlrev_b64 v[128:129], 12, v[162:163]
	v_lshl_add_u64 v[128:129], v[158:159], 0, v[128:129]
	global_load_dwordx4 v[132:135], v[128:129], off
	s_nop 0
	global_load_dwordx4 v[128:131], v[128:129], off offset:256
	v_or_b32_e32 v183, s38, v182
	v_cmp_gt_u32_e32 vcc, 16, v181
	s_waitcnt vmcnt(7)
	v_lshlrev_b32_e32 v192, 16, v184
	v_and_b32_e32 v193, 0xffff0000, v184
	v_lshlrev_b32_e32 v184, 16, v185
	v_and_b32_e32 v185, 0xffff0000, v185
	v_lshlrev_b32_e32 v194, 16, v186
	v_and_b32_e32 v195, 0xffff0000, v186
	v_lshlrev_b32_e32 v186, 16, v187
	v_and_b32_e32 v187, 0xffff0000, v187
	v_pk_add_f32 v[124:125], v[124:125], v[192:193]
	v_pk_add_f32 v[126:127], v[126:127], v[184:185]
	v_pk_add_f32 v[184:185], v[122:123], v[186:187]
	v_pk_add_f32 v[122:123], v[120:121], v[194:195]
	v_cvt_pk_bf16_f32 v120, v124, v125
	v_lshl_add_u64 v[124:125], s[0:1], 0, v[190:191]
	v_cvt_pk_bf16_f32 v121, v126, v127
	v_cvt_pk_bf16_f32 v122, v122, v123
	v_cvt_pk_bf16_f32 v123, v184, v185
	v_lshl_add_u64 v[124:125], v[124:125], 0, v[188:189]
	global_store_dwordx4 v[124:125], v[120:123], off
	v_lshlrev_b32_e32 v126, 16, v120
	v_lshlrev_b32_e32 v127, 16, v121
	v_and_b32_e32 v120, 0xffff0000, v120
	v_and_b32_e32 v121, 0xffff0000, v121
	v_mul_f32_e32 v120, v120, v120
	v_mul_f32_e32 v121, v121, v121
	v_lshlrev_b32_e32 v184, 16, v122
	v_and_b32_e32 v122, 0xffff0000, v122
	v_lshlrev_b32_e32 v185, 16, v123
	v_and_b32_e32 v123, 0xffff0000, v123
	v_fmac_f32_e32 v120, v126, v126
	v_fmac_f32_e32 v121, v127, v127
	v_add_f32_e32 v120, v120, v121
	v_mul_f32_e32 v121, v122, v122
	v_mul_f32_e32 v122, v123, v123
	v_fmac_f32_e32 v121, v184, v184
	v_fmac_f32_e32 v122, v185, v185
	v_add_f32_e32 v121, v121, v122
	v_add_f32_e32 v184, v120, v121
	s_waitcnt vmcnt(7)
	v_lshlrev_b32_e32 v120, 16, v152
	v_and_b32_e32 v121, 0xffff0000, v152
	v_lshlrev_b32_e32 v122, 16, v153
	v_and_b32_e32 v123, 0xffff0000, v153
	v_lshlrev_b32_e32 v126, 16, v154
	v_and_b32_e32 v127, 0xffff0000, v154
	v_lshlrev_b32_e32 v152, 16, v155
	v_and_b32_e32 v153, 0xffff0000, v155
	v_pk_add_f32 v[118:119], v[118:119], v[122:123]
	v_pk_add_f32 v[116:117], v[116:117], v[120:121]
	v_pk_add_f32 v[120:121], v[114:115], v[152:153]
	v_pk_add_f32 v[114:115], v[112:113], v[126:127]
	v_cvt_pk_bf16_f32 v112, v116, v117
	v_cvt_pk_bf16_f32 v113, v118, v119
	v_cvt_pk_bf16_f32 v114, v114, v115
	v_cvt_pk_bf16_f32 v115, v120, v121
	global_store_dwordx4 v[124:125], v[112:115], off offset:256
	v_lshlrev_b32_e32 v116, 16, v112
	v_lshlrev_b32_e32 v117, 16, v113
	v_and_b32_e32 v112, 0xffff0000, v112
	v_and_b32_e32 v113, 0xffff0000, v113
	v_mul_f32_e32 v112, v112, v112
	v_mul_f32_e32 v113, v113, v113
	v_lshlrev_b32_e32 v118, 16, v114
	v_and_b32_e32 v114, 0xffff0000, v114
	v_lshlrev_b32_e32 v119, 16, v115
	v_and_b32_e32 v115, 0xffff0000, v115
	v_fmac_f32_e32 v112, v116, v116
	v_fmac_f32_e32 v113, v117, v117
	v_add_f32_e32 v112, v112, v113
	v_mul_f32_e32 v113, v114, v114
	v_mul_f32_e32 v114, v115, v115
	v_fmac_f32_e32 v113, v118, v118
	v_fmac_f32_e32 v114, v119, v119
	v_add_f32_e32 v113, v113, v114
	v_add_f32_e32 v112, v112, v113
	v_add_f32_e32 v112, v184, v112
	v_mov_b32_e32 v113, v112
	s_waitcnt lgkmcnt(0)
	s_nop 1
	v_permlane16_swap_b32_e32 v112, v113
	v_add_f32_e32 v112, v112, v113
	ds_bpermute_b32 v113, v173, v112
	s_and_saveexec_b64 s[14:15], vcc
	s_cbranch_execz .LBB0_1459
	s_waitcnt lgkmcnt(0)
	v_add_f32_e32 v112, v112, v113
	v_lshl_add_u32 v113, v183, 4, s59
	ds_write_b32 v113, v112
; __device__ __forceinline__ unsigned cvt_pk_bf16(float lo, float hi) { const f32x2_ v = {lo, hi}; return __builtin_bit_cast(unsigned, __builtin_convertvector(v, bf16x2_)); }
;     __device__ __forceinline__ void operator()(const f32x4 (&acc)[2][2][4][2], const Unit& u, int wr, int wc, int fr, int fq) const {
;     ...
;                 for (int mm = 0; mm < MB; ++mm) { float ssum = 0.f; float rr = 1.0f; if constexpr (RS) rr = rs[(row0 + ai * HALF + (m0 + mm) * 16) & 2047];
; #pragma unroll
;                     for (int bj = 0; bj < 2; ++bj) { const size_t off = (size_t)(row0 + ai * HALF + (m0 + mm) * 16) * ld + col0 + bj * HALF;
;                         f32x4 r0, r1;
;                         if constexpr (RF32) { r0 = rf[mm][bj][0]; r1 = rf[mm][bj][1]; }
;                         else { const u32x4 w = rb[mm][bj]; r0 = (f32x4){lo_(w.x), hi_(w.x), lo_(w.y), hi_(w.y)}; r1 = (f32x4){lo_(w.z), hi_(w.z), lo_(w.w), hi_(w.w)}; }
;                         f32x4 v0 = acc[ai][bj][m0 + mm][0], v1 = acc[ai][bj][m0 + mm][1]; if constexpr (RS) { v0 = v0 * rr; v1 = v1 * rr; }
;                         if constexpr (MODE == 2) { const u32x4 w = pb[mm][bj]; const f32x4 p0 = {lo_(w.x), hi_(w.x), lo_(w.y), hi_(w.y)}, p1 = {lo_(w.z), hi_(w.z), lo_(w.w), hi_(w.w)};
; #pragma unroll
;                             for (int j = 0; j < 4; ++j) { v0[j] = p0[j] * __builtin_amdgcn_rcpf(1.0f + __expf(-v0[j])); v1[j] = p1[j] * __builtin_amdgcn_rcpf(1.0f + __expf(-v1[j])); } }
;                         v0 = v0 + r0; v1 = v1 + r1;
;                         u32x4 o; o.x = cvt_pk_bf16(v0[0], v0[1]); o.y = cvt_pk_bf16(v0[2], v0[3]); o.z = cvt_pk_bf16(v1[0], v1[1]); o.w = cvt_pk_bf16(v1[2], v1[3]);
;                         *(u32x4*)(C + off) = o;
;                         if constexpr (EMIT) { const float a0 = lo_(o.x), a1 = hi_(o.x), a2 = lo_(o.y), a3 = hi_(o.y), a4 = lo_(o.z), a5 = hi_(o.z), a6 = lo_(o.w), a7 = hi_(o.w);
;                             ssum += ((a0 * a0 + a1 * a1) + (a2 * a2 + a3 * a3)) + ((a4 * a4 + a5 * a5) + (a6 * a6 + a7 * a7)); } }
;                     if constexpr (EMIT) {
;                         ssum += __builtin_bit_cast(float, __builtin_amdgcn_ds_swizzle(__builtin_bit_cast(int, ssum), (16 << 10) | 0x1F)); ssum += __shfl_xor(ssum, 32);
;                         if (fq == 0) part[(ai * HALF + wr * 64 + (m0 + mm) * 16 + fr) * 4 + wc] = ssum; } }
.LBB0_1459:
	s_or_b64 exec, exec, s[14:15]
	s_waitcnt vmcnt(7)
	v_lshlrev_b32_e32 v112, 16, v148
	s_waitcnt lgkmcnt(0)
	v_and_b32_e32 v113, 0xffff0000, v148
	v_lshlrev_b32_e32 v114, 16, v149
	v_and_b32_e32 v115, 0xffff0000, v149
	v_lshlrev_b32_e32 v116, 16, v150
	v_and_b32_e32 v117, 0xffff0000, v150
	v_lshlrev_b32_e32 v118, 16, v151
	v_and_b32_e32 v119, 0xffff0000, v151
	v_pk_add_f32 v[108:109], v[108:109], v[112:113]
	v_pk_add_f32 v[110:111], v[110:111], v[114:115]
	v_pk_add_f32 v[112:113], v[106:107], v[118:119]
	v_pk_add_f32 v[106:107], v[104:105], v[116:117]
	v_cvt_pk_bf16_f32 v104, v108, v109
	v_cvt_pk_bf16_f32 v105, v110, v111
	v_and_b32_e32 v109, 0xffff0000, v104
	v_lshlrev_b32_e32 v108, 16, v104
	v_and_b32_e32 v111, 0xffff0000, v105
	v_mul_f32_e32 v109, v109, v109
	v_cvt_pk_bf16_f32 v106, v106, v107
	v_cvt_pk_bf16_f32 v107, v112, v113
	v_lshlrev_b32_e32 v110, 16, v105
	v_fmac_f32_e32 v109, v108, v108
	v_mul_f32_e32 v108, v111, v111
	v_and_b32_e32 v113, 0xffff0000, v106
	v_and_b32_e32 v115, 0xffff0000, v107
	v_fmac_f32_e32 v108, v110, v110
	v_lshlrev_b32_e32 v112, 16, v106
	v_lshlrev_b32_e32 v114, 16, v107
	v_add_f32_e32 v108, v109, v108
	v_mul_f32_e32 v109, v113, v113
	v_mul_f32_e32 v110, v115, v115
	v_fmac_f32_e32 v109, v112, v112
	v_fmac_f32_e32 v110, v114, v114
	v_add_f32_e32 v109, v109, v110
	v_add_f32_e32 v116, v108, v109
	s_waitcnt vmcnt(6)
	v_lshlrev_b32_e32 v108, 16, v144
	v_and_b32_e32 v109, 0xffff0000, v144
	v_lshlrev_b32_e32 v110, 16, v145
	v_and_b32_e32 v111, 0xffff0000, v145
	v_lshlrev_b32_e32 v112, 16, v146
	v_and_b32_e32 v113, 0xffff0000, v146
	v_lshlrev_b32_e32 v114, 16, v147
	v_and_b32_e32 v115, 0xffff0000, v147
	v_pk_add_f32 v[100:101], v[100:101], v[108:109]
	v_pk_add_f32 v[102:103], v[102:103], v[110:111]
	v_pk_add_f32 v[108:109], v[98:99], v[114:115]
	v_pk_add_f32 v[96:97], v[96:97], v[112:113]
	v_cvt_pk_bf16_f32 v98, v100, v101
	v_cvt_pk_bf16_f32 v99, v102, v103
	v_cvt_pk_bf16_f32 v100, v96, v97
	v_and_b32_e32 v97, 0xffff0000, v98
	v_lshlrev_b32_e32 v96, 16, v98
	v_and_b32_e32 v103, 0xffff0000, v99
	v_mul_f32_e32 v97, v97, v97
	v_cvt_pk_bf16_f32 v101, v108, v109
	v_lshlrev_b32_e32 v102, 16, v99
	v_fmac_f32_e32 v97, v96, v96
	v_mul_f32_e32 v96, v103, v103
	v_and_b32_e32 v109, 0xffff0000, v100
	v_and_b32_e32 v111, 0xffff0000, v101
	v_fmac_f32_e32 v96, v102, v102
	v_lshlrev_b32_e32 v108, 16, v100
	v_lshlrev_b32_e32 v110, 16, v101
	v_add_f32_e32 v96, v97, v96
	v_mul_f32_e32 v97, v109, v109
	v_mul_f32_e32 v102, v111, v111
	v_fmac_f32_e32 v97, v108, v108
	v_fmac_f32_e32 v102, v110, v110
	v_add_f32_e32 v97, v97, v102
	v_add_f32_e32 v96, v96, v97
	v_add_f32_e32 v96, v116, v96
	v_mov_b32_e32 v97, v96
	v_lshlrev_b64 v[102:103], 11, v[166:167]
	v_lshl_add_u64 v[102:103], v[102:103], 1, s[0:1]
	v_lshl_add_u64 v[102:103], v[156:157], 1, v[102:103]
	global_store_dwordx4 v[102:103], v[104:107], off
	global_store_dwordx4 v[102:103], v[98:101], off offset:256
	s_waitcnt lgkmcnt(0)
	s_nop 1
	v_permlane16_swap_b32_e32 v96, v97
	v_add_f32_e32 v96, v96, v97
	ds_bpermute_b32 v97, v173, v96
	s_and_saveexec_b64 s[14:15], vcc
	s_cbranch_execz .LBB0_1461
	s_waitcnt lgkmcnt(0)
	v_add_f32_e32 v96, v96, v97
	v_lshl_add_u32 v97, v183, 4, s60
	ds_write_b32 v97, v96
.LBB0_1461:
	s_or_b64 exec, exec, s[14:15]
	s_waitcnt vmcnt(7)
	v_lshlrev_b32_e32 v96, 16, v140
	s_waitcnt lgkmcnt(0)
	v_and_b32_e32 v97, 0xffff0000, v140
	v_lshlrev_b32_e32 v98, 16, v141
	v_and_b32_e32 v99, 0xffff0000, v141
	v_lshlrev_b32_e32 v100, 16, v142
	v_and_b32_e32 v101, 0xffff0000, v142
	v_lshlrev_b32_e32 v102, 16, v143
	v_and_b32_e32 v103, 0xffff0000, v143
	v_pk_add_f32 v[92:93], v[92:93], v[96:97]
	v_pk_add_f32 v[94:95], v[94:95], v[98:99]
	v_pk_add_f32 v[96:97], v[90:91], v[102:103]
	v_pk_add_f32 v[90:91], v[88:89], v[100:101]
	v_cvt_pk_bf16_f32 v88, v92, v93
	v_cvt_pk_bf16_f32 v89, v94, v95
	v_and_b32_e32 v93, 0xffff0000, v88
	v_lshlrev_b32_e32 v92, 16, v88
	v_and_b32_e32 v95, 0xffff0000, v89
	v_mul_f32_e32 v93, v93, v93
	v_cvt_pk_bf16_f32 v90, v90, v91
	v_cvt_pk_bf16_f32 v91, v96, v97
	v_lshlrev_b32_e32 v94, 16, v89
	v_fmac_f32_e32 v93, v92, v92
	v_mul_f32_e32 v92, v95, v95
	v_and_b32_e32 v97, 0xffff0000, v90
	v_and_b32_e32 v99, 0xffff0000, v91
	v_fmac_f32_e32 v92, v94, v94
	v_lshlrev_b32_e32 v96, 16, v90
	v_lshlrev_b32_e32 v98, 16, v91
	v_add_f32_e32 v92, v93, v92
	v_mul_f32_e32 v93, v97, v97
	v_mul_f32_e32 v94, v99, v99
	v_fmac_f32_e32 v93, v96, v96
	v_fmac_f32_e32 v94, v98, v98
	v_add_f32_e32 v93, v93, v94
	v_add_f32_e32 v100, v92, v93
	s_waitcnt vmcnt(6)
	v_lshlrev_b32_e32 v92, 16, v136
	v_and_b32_e32 v93, 0xffff0000, v136
	v_lshlrev_b32_e32 v94, 16, v137
	v_and_b32_e32 v95, 0xffff0000, v137
	v_lshlrev_b32_e32 v96, 16, v138
	v_and_b32_e32 v97, 0xffff0000, v138
	v_lshlrev_b32_e32 v98, 16, v139
	v_and_b32_e32 v99, 0xffff0000, v139
	v_pk_add_f32 v[84:85], v[84:85], v[92:93]
	v_pk_add_f32 v[86:87], v[86:87], v[94:95]
	v_pk_add_f32 v[92:93], v[82:83], v[98:99]
	v_pk_add_f32 v[80:81], v[80:81], v[96:97]
	v_cvt_pk_bf16_f32 v82, v84, v85
	v_cvt_pk_bf16_f32 v83, v86, v87
	v_cvt_pk_bf16_f32 v84, v80, v81
	v_and_b32_e32 v81, 0xffff0000, v82
	v_lshlrev_b32_e32 v80, 16, v82
	v_and_b32_e32 v87, 0xffff0000, v83
	v_mul_f32_e32 v81, v81, v81
	v_cvt_pk_bf16_f32 v85, v92, v93
	v_lshlrev_b32_e32 v86, 16, v83
	v_fmac_f32_e32 v81, v80, v80
	v_mul_f32_e32 v80, v87, v87
	v_and_b32_e32 v93, 0xffff0000, v84
	v_and_b32_e32 v95, 0xffff0000, v85
	v_fmac_f32_e32 v80, v86, v86
	v_lshlrev_b32_e32 v92, 16, v84
	v_lshlrev_b32_e32 v94, 16, v85
	v_add_f32_e32 v80, v81, v80
	v_mul_f32_e32 v81, v93, v93
	v_mul_f32_e32 v86, v95, v95
	v_fmac_f32_e32 v81, v92, v92
	v_fmac_f32_e32 v86, v94, v94
	v_add_f32_e32 v81, v81, v86
	v_add_f32_e32 v80, v80, v81
	v_add_f32_e32 v80, v100, v80
	v_mov_b32_e32 v81, v80
	v_lshlrev_b64 v[86:87], 11, v[164:165]
	v_lshl_add_u64 v[86:87], v[86:87], 1, s[0:1]
	v_lshl_add_u64 v[86:87], v[156:157], 1, v[86:87]
	global_store_dwordx4 v[86:87], v[88:91], off
	global_store_dwordx4 v[86:87], v[82:85], off offset:256
	s_waitcnt lgkmcnt(0)
	s_nop 1
	v_permlane16_swap_b32_e32 v80, v81
	v_add_f32_e32 v80, v80, v81
	ds_bpermute_b32 v81, v173, v80
	s_and_saveexec_b64 s[14:15], vcc
	s_cbranch_execz .LBB0_1463
	s_waitcnt lgkmcnt(0)
	v_add_f32_e32 v80, v80, v81
	v_lshl_add_u32 v81, v183, 4, s61
	ds_write_b32 v81, v80
; __device__ __forceinline__ unsigned cvt_pk_bf16(float lo, float hi) { const f32x2_ v = {lo, hi}; return __builtin_bit_cast(unsigned, __builtin_convertvector(v, bf16x2_)); }
;     __device__ __forceinline__ void operator()(const f32x4 (&acc)[2][2][4][2], const Unit& u, int wr, int wc, int fr, int fq) const {
;     ...
;                 for (int mm = 0; mm < MB; ++mm) { float ssum = 0.f; float rr = 1.0f; if constexpr (RS) rr = rs[(row0 + ai * HALF + (m0 + mm) * 16) & 2047];
; #pragma unroll
;                     for (int bj = 0; bj < 2; ++bj) { const size_t off = (size_t)(row0 + ai * HALF + (m0 + mm) * 16) * ld + col0 + bj * HALF;
;                         f32x4 r0, r1;
;                         if constexpr (RF32) { r0 = rf[mm][bj][0]; r1 = rf[mm][bj][1]; }
;                         else { const u32x4 w = rb[mm][bj]; r0 = (f32x4){lo_(w.x), hi_(w.x), lo_(w.y), hi_(w.y)}; r1 = (f32x4){lo_(w.z), hi_(w.z), lo_(w.w), hi_(w.w)}; }
;                         f32x4 v0 = acc[ai][bj][m0 + mm][0], v1 = acc[ai][bj][m0 + mm][1]; if constexpr (RS) { v0 = v0 * rr; v1 = v1 * rr; }
;                         if constexpr (MODE == 2) { const u32x4 w = pb[mm][bj]; const f32x4 p0 = {lo_(w.x), hi_(w.x), lo_(w.y), hi_(w.y)}, p1 = {lo_(w.z), hi_(w.z), lo_(w.w), hi_(w.w)};
; #pragma unroll
;                             for (int j = 0; j < 4; ++j) { v0[j] = p0[j] * __builtin_amdgcn_rcpf(1.0f + __expf(-v0[j])); v1[j] = p1[j] * __builtin_amdgcn_rcpf(1.0f + __expf(-v1[j])); } }
;                         v0 = v0 + r0; v1 = v1 + r1;
;                         u32x4 o; o.x = cvt_pk_bf16(v0[0], v0[1]); o.y = cvt_pk_bf16(v0[2], v0[3]); o.z = cvt_pk_bf16(v1[0], v1[1]); o.w = cvt_pk_bf16(v1[2], v1[3]);
;                         *(u32x4*)(C + off) = o;
;                         if constexpr (EMIT) { const float a0 = lo_(o.x), a1 = hi_(o.x), a2 = lo_(o.y), a3 = hi_(o.y), a4 = lo_(o.z), a5 = hi_(o.z), a6 = lo_(o.w), a7 = hi_(o.w);
;                             ssum += ((a0 * a0 + a1 * a1) + (a2 * a2 + a3 * a3)) + ((a4 * a4 + a5 * a5) + (a6 * a6 + a7 * a7)); } }
;                     if constexpr (EMIT) {
;                         ssum += __builtin_bit_cast(float, __builtin_amdgcn_ds_swizzle(__builtin_bit_cast(int, ssum), (16 << 10) | 0x1F)); ssum += __shfl_xor(ssum, 32);
;                         if (fq == 0) part[(ai * HALF + wr * 64 + (m0 + mm) * 16 + fr) * 4 + wc] = ssum; } }
.LBB0_1463:
	s_or_b64 exec, exec, s[14:15]
	s_waitcnt vmcnt(7)
	v_lshlrev_b32_e32 v80, 16, v132
	s_waitcnt lgkmcnt(0)
	v_and_b32_e32 v81, 0xffff0000, v132
	v_lshlrev_b32_e32 v82, 16, v133
	v_and_b32_e32 v83, 0xffff0000, v133
	v_lshlrev_b32_e32 v84, 16, v134
	v_and_b32_e32 v85, 0xffff0000, v134
	v_lshlrev_b32_e32 v86, 16, v135
	v_and_b32_e32 v87, 0xffff0000, v135
	v_pk_add_f32 v[76:77], v[76:77], v[80:81]
	v_pk_add_f32 v[78:79], v[78:79], v[82:83]
	v_pk_add_f32 v[80:81], v[74:75], v[86:87]
	v_pk_add_f32 v[74:75], v[72:73], v[84:85]
	v_cvt_pk_bf16_f32 v72, v76, v77
	v_cvt_pk_bf16_f32 v73, v78, v79
	v_and_b32_e32 v77, 0xffff0000, v72
	v_lshlrev_b32_e32 v76, 16, v72
	v_and_b32_e32 v79, 0xffff0000, v73
	v_mul_f32_e32 v77, v77, v77
	v_cvt_pk_bf16_f32 v74, v74, v75
	v_cvt_pk_bf16_f32 v75, v80, v81
	v_lshlrev_b32_e32 v78, 16, v73
	v_fmac_f32_e32 v77, v76, v76
	v_mul_f32_e32 v76, v79, v79
	v_and_b32_e32 v81, 0xffff0000, v74
	v_and_b32_e32 v83, 0xffff0000, v75
	v_fmac_f32_e32 v76, v78, v78
	v_lshlrev_b32_e32 v80, 16, v74
	v_lshlrev_b32_e32 v82, 16, v75
	v_add_f32_e32 v76, v77, v76
	v_mul_f32_e32 v77, v81, v81
	v_mul_f32_e32 v78, v83, v83
	v_fmac_f32_e32 v77, v80, v80
	v_fmac_f32_e32 v78, v82, v82
	v_add_f32_e32 v77, v77, v78
	v_add_f32_e32 v84, v76, v77
	s_waitcnt vmcnt(6)
	v_lshlrev_b32_e32 v76, 16, v128
	v_and_b32_e32 v77, 0xffff0000, v128
	v_lshlrev_b32_e32 v78, 16, v129
	v_and_b32_e32 v79, 0xffff0000, v129
	v_lshlrev_b32_e32 v80, 16, v130
	v_and_b32_e32 v81, 0xffff0000, v130
	v_lshlrev_b32_e32 v82, 16, v131
	v_and_b32_e32 v83, 0xffff0000, v131
	v_pk_add_f32 v[68:69], v[68:69], v[76:77]
	v_pk_add_f32 v[70:71], v[70:71], v[78:79]
	v_pk_add_f32 v[76:77], v[66:67], v[82:83]
	v_pk_add_f32 v[64:65], v[64:65], v[80:81]
	v_cvt_pk_bf16_f32 v66, v68, v69
	v_cvt_pk_bf16_f32 v67, v70, v71
	v_cvt_pk_bf16_f32 v68, v64, v65
	v_and_b32_e32 v65, 0xffff0000, v66
	v_lshlrev_b32_e32 v64, 16, v66
	v_and_b32_e32 v71, 0xffff0000, v67
	v_mul_f32_e32 v65, v65, v65
	v_cvt_pk_bf16_f32 v69, v76, v77
	v_lshlrev_b32_e32 v70, 16, v67
	v_fmac_f32_e32 v65, v64, v64
	v_mul_f32_e32 v64, v71, v71
	v_and_b32_e32 v77, 0xffff0000, v68
	v_and_b32_e32 v79, 0xffff0000, v69
	v_fmac_f32_e32 v64, v70, v70
	v_lshlrev_b32_e32 v76, 16, v68
	v_lshlrev_b32_e32 v78, 16, v69
	v_add_f32_e32 v64, v65, v64
	v_mul_f32_e32 v65, v77, v77
	v_mul_f32_e32 v70, v79, v79
	v_fmac_f32_e32 v65, v76, v76
	v_fmac_f32_e32 v70, v78, v78
	v_add_f32_e32 v65, v65, v70
	v_add_f32_e32 v64, v64, v65
	v_add_f32_e32 v64, v84, v64
	v_mov_b32_e32 v65, v64
	v_lshlrev_b64 v[70:71], 11, v[162:163]
	v_lshl_add_u64 v[70:71], v[70:71], 1, s[0:1]
	v_lshl_add_u64 v[70:71], v[156:157], 1, v[70:71]
	global_store_dwordx4 v[70:71], v[72:75], off
	global_store_dwordx4 v[70:71], v[66:69], off offset:256
	s_waitcnt lgkmcnt(0)
	s_nop 1
	v_permlane16_swap_b32_e32 v64, v65
	v_add_f32_e32 v64, v64, v65
	ds_bpermute_b32 v65, v173, v64
	s_and_saveexec_b64 s[14:15], vcc
	s_cbranch_execz .LBB0_1465
	s_waitcnt lgkmcnt(0)
	v_add_f32_e32 v64, v64, v65
	v_lshl_add_u32 v65, v183, 4, s62
	ds_write_b32 v65, v64
.LBB0_1465:
	s_or_b64 exec, exec, s[14:15]
	s_waitcnt lgkmcnt(0)
	v_lshlrev_b64 v[64:65], 12, v[160:161]
	s_mov_b64 s[14:15], 0x80000
	v_lshl_add_u64 v[102:103], v[64:65], 0, s[14:15]
	v_lshl_add_u64 v[64:65], v[158:159], 0, v[102:103]
	global_load_dwordx4 v[98:101], v[64:65], off
	global_load_dwordx4 v[88:91], v[64:65], off offset:256
	v_add_u32_e32 v96, 0x90, v160
	v_ashrrev_i32_e32 v97, 31, v96
	v_lshlrev_b64 v[64:65], 12, v[96:97]
	v_add_u32_e32 v94, 0xa0, v160
	v_lshl_add_u64 v[64:65], v[158:159], 0, v[64:65]
	v_ashrrev_i32_e32 v95, 31, v94
	global_load_dwordx4 v[84:87], v[64:65], off
	global_load_dwordx4 v[80:83], v[64:65], off offset:256
	v_lshlrev_b64 v[64:65], 12, v[94:95]
	v_add_u32_e32 v92, 0xb0, v160
	v_lshl_add_u64 v[64:65], v[158:159], 0, v[64:65]
	v_ashrrev_i32_e32 v93, 31, v92
	global_load_dwordx4 v[76:79], v[64:65], off
	global_load_dwordx4 v[72:75], v[64:65], off offset:256
	v_lshlrev_b64 v[64:65], 12, v[92:93]
	v_lshl_add_u64 v[64:65], v[158:159], 0, v[64:65]
	global_load_dwordx4 v[68:71], v[64:65], off
	s_nop 0
	global_load_dwordx4 v[64:67], v[64:65], off offset:256
	s_waitcnt vmcnt(7)
	v_lshlrev_b32_e32 v104, 16, v98
	v_and_b32_e32 v105, 0xffff0000, v98
	v_lshlrev_b32_e32 v98, 16, v99
	v_and_b32_e32 v99, 0xffff0000, v99
	v_lshlrev_b32_e32 v106, 16, v100
	v_and_b32_e32 v107, 0xffff0000, v100
	v_lshlrev_b32_e32 v100, 16, v101
	v_and_b32_e32 v101, 0xffff0000, v101
	v_pk_add_f32 v[60:61], v[60:61], v[104:105]
	v_pk_add_f32 v[62:63], v[62:63], v[98:99]
	v_pk_add_f32 v[98:99], v[58:59], v[100:101]
	v_pk_add_f32 v[58:59], v[56:57], v[106:107]
	v_cvt_pk_bf16_f32 v56, v60, v61
	v_lshl_add_u64 v[60:61], s[0:1], 0, v[102:103]
	v_cvt_pk_bf16_f32 v57, v62, v63
	v_cvt_pk_bf16_f32 v58, v58, v59
	v_cvt_pk_bf16_f32 v59, v98, v99
	v_lshl_add_u64 v[60:61], v[156:157], 1, v[60:61]
	global_store_dwordx4 v[60:61], v[56:59], off
	v_lshlrev_b32_e32 v62, 16, v56
	v_lshlrev_b32_e32 v63, 16, v57
	v_and_b32_e32 v56, 0xffff0000, v56
	v_and_b32_e32 v57, 0xffff0000, v57
	v_mul_f32_e32 v56, v56, v56
	v_mul_f32_e32 v57, v57, v57
	v_lshlrev_b32_e32 v98, 16, v58
	v_and_b32_e32 v58, 0xffff0000, v58
	v_lshlrev_b32_e32 v99, 16, v59
	v_and_b32_e32 v59, 0xffff0000, v59
	v_fmac_f32_e32 v56, v62, v62
	v_fmac_f32_e32 v57, v63, v63
	v_add_f32_e32 v56, v56, v57
	v_mul_f32_e32 v57, v58, v58
	v_mul_f32_e32 v58, v59, v59
	v_fmac_f32_e32 v57, v98, v98
	v_fmac_f32_e32 v58, v99, v99
	v_add_f32_e32 v57, v57, v58
	v_add_f32_e32 v98, v56, v57
	s_waitcnt vmcnt(7)
	v_lshlrev_b32_e32 v56, 16, v88
	v_and_b32_e32 v57, 0xffff0000, v88
	v_lshlrev_b32_e32 v58, 16, v89
	v_and_b32_e32 v59, 0xffff0000, v89
	v_lshlrev_b32_e32 v62, 16, v90
	v_and_b32_e32 v63, 0xffff0000, v90
	v_lshlrev_b32_e32 v88, 16, v91
	v_and_b32_e32 v89, 0xffff0000, v91
	v_pk_add_f32 v[54:55], v[54:55], v[58:59]
	v_pk_add_f32 v[52:53], v[52:53], v[56:57]
	v_pk_add_f32 v[56:57], v[50:51], v[88:89]
	v_pk_add_f32 v[50:51], v[48:49], v[62:63]
	v_cvt_pk_bf16_f32 v48, v52, v53
	v_cvt_pk_bf16_f32 v49, v54, v55
	v_cvt_pk_bf16_f32 v50, v50, v51
	v_cvt_pk_bf16_f32 v51, v56, v57
	global_store_dwordx4 v[60:61], v[48:51], off offset:256
	v_lshlrev_b32_e32 v52, 16, v48
	v_lshlrev_b32_e32 v53, 16, v49
	v_and_b32_e32 v48, 0xffff0000, v48
	v_and_b32_e32 v49, 0xffff0000, v49
	v_mul_f32_e32 v48, v48, v48
	v_mul_f32_e32 v49, v49, v49
	v_lshlrev_b32_e32 v54, 16, v50
	v_and_b32_e32 v50, 0xffff0000, v50
	v_lshlrev_b32_e32 v55, 16, v51
	v_and_b32_e32 v51, 0xffff0000, v51
	v_fmac_f32_e32 v48, v52, v52
	v_fmac_f32_e32 v49, v53, v53
	v_add_f32_e32 v48, v48, v49
	v_mul_f32_e32 v49, v50, v50
	v_mul_f32_e32 v50, v51, v51
	v_fmac_f32_e32 v49, v54, v54
	v_fmac_f32_e32 v50, v55, v55
	v_add_f32_e32 v49, v49, v50
	v_add_f32_e32 v48, v48, v49
	v_add_f32_e32 v48, v98, v48
	v_mov_b32_e32 v49, v48
	s_waitcnt lgkmcnt(0)
	s_nop 1
	v_permlane16_swap_b32_e32 v48, v49
	v_add_f32_e32 v48, v48, v49
	ds_bpermute_b32 v49, v173, v48
	s_and_saveexec_b64 s[14:15], vcc
	s_cbranch_execz .LBB0_1467
; __device__ __forceinline__ unsigned cvt_pk_bf16(float lo, float hi) { const f32x2_ v = {lo, hi}; return __builtin_bit_cast(unsigned, __builtin_convertvector(v, bf16x2_)); }
;     __device__ __forceinline__ void operator()(const f32x4 (&acc)[2][2][4][2], const Unit& u, int wr, int wc, int fr, int fq) const {
;     ...
;                 for (int mm = 0; mm < MB; ++mm) { float ssum = 0.f; float rr = 1.0f; if constexpr (RS) rr = rs[(row0 + ai * HALF + (m0 + mm) * 16) & 2047];
; #pragma unroll
;                     for (int bj = 0; bj < 2; ++bj) { const size_t off = (size_t)(row0 + ai * HALF + (m0 + mm) * 16) * ld + col0 + bj * HALF;
;                         f32x4 r0, r1;
;                         if constexpr (RF32) { r0 = rf[mm][bj][0]; r1 = rf[mm][bj][1]; }
;                         else { const u32x4 w = rb[mm][bj]; r0 = (f32x4){lo_(w.x), hi_(w.x), lo_(w.y), hi_(w.y)}; r1 = (f32x4){lo_(w.z), hi_(w.z), lo_(w.w), hi_(w.w)}; }
;                         f32x4 v0 = acc[ai][bj][m0 + mm][0], v1 = acc[ai][bj][m0 + mm][1]; if constexpr (RS) { v0 = v0 * rr; v1 = v1 * rr; }
;                         if constexpr (MODE == 2) { const u32x4 w = pb[mm][bj]; const f32x4 p0 = {lo_(w.x), hi_(w.x), lo_(w.y), hi_(w.y)}, p1 = {lo_(w.z), hi_(w.z), lo_(w.w), hi_(w.w)};
; #pragma unroll
;                             for (int j = 0; j < 4; ++j) { v0[j] = p0[j] * __builtin_amdgcn_rcpf(1.0f + __expf(-v0[j])); v1[j] = p1[j] * __builtin_amdgcn_rcpf(1.0f + __expf(-v1[j])); } }
;                         v0 = v0 + r0; v1 = v1 + r1;
;                         u32x4 o; o.x = cvt_pk_bf16(v0[0], v0[1]); o.y = cvt_pk_bf16(v0[2], v0[3]); o.z = cvt_pk_bf16(v1[0], v1[1]); o.w = cvt_pk_bf16(v1[2], v1[3]);
;                         *(u32x4*)(C + off) = o;
;                         if constexpr (EMIT) { const float a0 = lo_(o.x), a1 = hi_(o.x), a2 = lo_(o.y), a3 = hi_(o.y), a4 = lo_(o.z), a5 = hi_(o.z), a6 = lo_(o.w), a7 = hi_(o.w);
;                             ssum += ((a0 * a0 + a1 * a1) + (a2 * a2 + a3 * a3)) + ((a4 * a4 + a5 * a5) + (a6 * a6 + a7 * a7)); } }
;                     if constexpr (EMIT) {
;                         ssum += __builtin_bit_cast(float, __builtin_amdgcn_ds_swizzle(__builtin_bit_cast(int, ssum), (16 << 10) | 0x1F)); ssum += __shfl_xor(ssum, 32);
;                         if (fq == 0) part[(ai * HALF + wr * 64 + (m0 + mm) * 16 + fr) * 4 + wc] = ssum; } }
	s_waitcnt lgkmcnt(0)
	v_add_f32_e32 v48, v48, v49
	v_lshl_add_u32 v49, v183, 4, s63
	ds_write_b32 v49, v48
.LBB0_1467:
	s_or_b64 exec, exec, s[14:15]
	s_waitcnt vmcnt(7)
	v_lshlrev_b32_e32 v48, 16, v84
	s_waitcnt lgkmcnt(0)
	v_and_b32_e32 v49, 0xffff0000, v84
	v_lshlrev_b32_e32 v50, 16, v85
	v_and_b32_e32 v51, 0xffff0000, v85
	v_lshlrev_b32_e32 v52, 16, v86
	v_and_b32_e32 v53, 0xffff0000, v86
	v_lshlrev_b32_e32 v54, 16, v87
	v_and_b32_e32 v55, 0xffff0000, v87
	v_pk_add_f32 v[44:45], v[44:45], v[48:49]
	v_pk_add_f32 v[46:47], v[46:47], v[50:51]
	v_pk_add_f32 v[48:49], v[42:43], v[54:55]
	v_pk_add_f32 v[42:43], v[40:41], v[52:53]
	v_cvt_pk_bf16_f32 v40, v44, v45
	v_cvt_pk_bf16_f32 v41, v46, v47
	v_and_b32_e32 v45, 0xffff0000, v40
	v_lshlrev_b32_e32 v44, 16, v40
	v_and_b32_e32 v47, 0xffff0000, v41
	v_mul_f32_e32 v45, v45, v45
	v_cvt_pk_bf16_f32 v42, v42, v43
	v_cvt_pk_bf16_f32 v43, v48, v49
	v_lshlrev_b32_e32 v46, 16, v41
	v_fmac_f32_e32 v45, v44, v44
	v_mul_f32_e32 v44, v47, v47
	v_and_b32_e32 v49, 0xffff0000, v42
	v_and_b32_e32 v51, 0xffff0000, v43
	v_fmac_f32_e32 v44, v46, v46
	v_lshlrev_b32_e32 v48, 16, v42
	v_lshlrev_b32_e32 v50, 16, v43
	v_add_f32_e32 v44, v45, v44
	v_mul_f32_e32 v45, v49, v49
	v_mul_f32_e32 v46, v51, v51
	v_fmac_f32_e32 v45, v48, v48
	v_fmac_f32_e32 v46, v50, v50
	v_add_f32_e32 v45, v45, v46
	v_add_f32_e32 v52, v44, v45
	s_waitcnt vmcnt(6)
	v_lshlrev_b32_e32 v44, 16, v80
	v_and_b32_e32 v45, 0xffff0000, v80
	v_lshlrev_b32_e32 v46, 16, v81
	v_and_b32_e32 v47, 0xffff0000, v81
	v_lshlrev_b32_e32 v48, 16, v82
	v_and_b32_e32 v49, 0xffff0000, v82
	v_lshlrev_b32_e32 v50, 16, v83
	v_and_b32_e32 v51, 0xffff0000, v83
	v_pk_add_f32 v[36:37], v[36:37], v[44:45]
	v_pk_add_f32 v[38:39], v[38:39], v[46:47]
	v_pk_add_f32 v[44:45], v[34:35], v[50:51]
	v_pk_add_f32 v[32:33], v[32:33], v[48:49]
	v_cvt_pk_bf16_f32 v34, v36, v37
	v_cvt_pk_bf16_f32 v35, v38, v39
	v_cvt_pk_bf16_f32 v36, v32, v33
	v_and_b32_e32 v33, 0xffff0000, v34
	v_lshlrev_b32_e32 v32, 16, v34
	v_and_b32_e32 v39, 0xffff0000, v35
	v_mul_f32_e32 v33, v33, v33
	v_cvt_pk_bf16_f32 v37, v44, v45
	v_lshlrev_b32_e32 v38, 16, v35
	v_fmac_f32_e32 v33, v32, v32
	v_mul_f32_e32 v32, v39, v39
	v_and_b32_e32 v45, 0xffff0000, v36
	v_and_b32_e32 v47, 0xffff0000, v37
	v_fmac_f32_e32 v32, v38, v38
	v_lshlrev_b32_e32 v44, 16, v36
	v_lshlrev_b32_e32 v46, 16, v37
	v_add_f32_e32 v32, v33, v32
	v_mul_f32_e32 v33, v45, v45
	v_mul_f32_e32 v38, v47, v47
	v_fmac_f32_e32 v33, v44, v44
	v_fmac_f32_e32 v38, v46, v46
	v_add_f32_e32 v33, v33, v38
	v_add_f32_e32 v32, v32, v33
	v_add_f32_e32 v32, v52, v32
	v_mov_b32_e32 v33, v32
	v_lshlrev_b64 v[38:39], 11, v[96:97]
	v_lshl_add_u64 v[38:39], v[38:39], 1, s[0:1]
	v_lshl_add_u64 v[38:39], v[156:157], 1, v[38:39]
	global_store_dwordx4 v[38:39], v[40:43], off
	global_store_dwordx4 v[38:39], v[34:37], off offset:256
	s_waitcnt lgkmcnt(0)
	s_nop 1
	v_permlane16_swap_b32_e32 v32, v33
	v_add_f32_e32 v32, v32, v33
	ds_bpermute_b32 v33, v173, v32
	s_and_saveexec_b64 s[14:15], vcc
	s_cbranch_execz .LBB0_1469
	s_waitcnt lgkmcnt(0)
	v_add_f32_e32 v32, v32, v33
	v_lshl_add_u32 v33, v183, 4, s64
	ds_write_b32 v33, v32
; __device__ __forceinline__ unsigned cvt_pk_bf16(float lo, float hi) { const f32x2_ v = {lo, hi}; return __builtin_bit_cast(unsigned, __builtin_convertvector(v, bf16x2_)); }
;     __device__ __forceinline__ void operator()(const f32x4 (&acc)[2][2][4][2], const Unit& u, int wr, int wc, int fr, int fq) const {
;     ...
;                 for (int mm = 0; mm < MB; ++mm) { float ssum = 0.f; float rr = 1.0f; if constexpr (RS) rr = rs[(row0 + ai * HALF + (m0 + mm) * 16) & 2047];
; #pragma unroll
;                     for (int bj = 0; bj < 2; ++bj) { const size_t off = (size_t)(row0 + ai * HALF + (m0 + mm) * 16) * ld + col0 + bj * HALF;
;                         f32x4 r0, r1;
;                         if constexpr (RF32) { r0 = rf[mm][bj][0]; r1 = rf[mm][bj][1]; }
;                         else { const u32x4 w = rb[mm][bj]; r0 = (f32x4){lo_(w.x), hi_(w.x), lo_(w.y), hi_(w.y)}; r1 = (f32x4){lo_(w.z), hi_(w.z), lo_(w.w), hi_(w.w)}; }
;                         f32x4 v0 = acc[ai][bj][m0 + mm][0], v1 = acc[ai][bj][m0 + mm][1]; if constexpr (RS) { v0 = v0 * rr; v1 = v1 * rr; }
;                         if constexpr (MODE == 2) { const u32x4 w = pb[mm][bj]; const f32x4 p0 = {lo_(w.x), hi_(w.x), lo_(w.y), hi_(w.y)}, p1 = {lo_(w.z), hi_(w.z), lo_(w.w), hi_(w.w)};
; #pragma unroll
;                             for (int j = 0; j < 4; ++j) { v0[j] = p0[j] * __builtin_amdgcn_rcpf(1.0f + __expf(-v0[j])); v1[j] = p1[j] * __builtin_amdgcn_rcpf(1.0f + __expf(-v1[j])); } }
;                         v0 = v0 + r0; v1 = v1 + r1;
;                         u32x4 o; o.x = cvt_pk_bf16(v0[0], v0[1]); o.y = cvt_pk_bf16(v0[2], v0[3]); o.z = cvt_pk_bf16(v1[0], v1[1]); o.w = cvt_pk_bf16(v1[2], v1[3]);
;                         *(u32x4*)(C + off) = o;
;                         if constexpr (EMIT) { const float a0 = lo_(o.x), a1 = hi_(o.x), a2 = lo_(o.y), a3 = hi_(o.y), a4 = lo_(o.z), a5 = hi_(o.z), a6 = lo_(o.w), a7 = hi_(o.w);
;                             ssum += ((a0 * a0 + a1 * a1) + (a2 * a2 + a3 * a3)) + ((a4 * a4 + a5 * a5) + (a6 * a6 + a7 * a7)); } }
;                     if constexpr (EMIT) {
;                         ssum += __builtin_bit_cast(float, __builtin_amdgcn_ds_swizzle(__builtin_bit_cast(int, ssum), (16 << 10) | 0x1F)); ssum += __shfl_xor(ssum, 32);
;                         if (fq == 0) part[(ai * HALF + wr * 64 + (m0 + mm) * 16 + fr) * 4 + wc] = ssum; } }
.LBB0_1469:
	s_or_b64 exec, exec, s[14:15]
	s_waitcnt vmcnt(7)
	v_lshlrev_b32_e32 v32, 16, v76
	s_waitcnt lgkmcnt(0)
	v_and_b32_e32 v33, 0xffff0000, v76
	v_lshlrev_b32_e32 v34, 16, v77
	v_and_b32_e32 v35, 0xffff0000, v77
	v_lshlrev_b32_e32 v36, 16, v78
	v_and_b32_e32 v37, 0xffff0000, v78
	v_lshlrev_b32_e32 v38, 16, v79
	v_and_b32_e32 v39, 0xffff0000, v79
	v_pk_add_f32 v[28:29], v[28:29], v[32:33]
	v_pk_add_f32 v[30:31], v[30:31], v[34:35]
	v_pk_add_f32 v[32:33], v[26:27], v[38:39]
	v_pk_add_f32 v[26:27], v[24:25], v[36:37]
	v_cvt_pk_bf16_f32 v24, v28, v29
	v_cvt_pk_bf16_f32 v25, v30, v31
	v_and_b32_e32 v29, 0xffff0000, v24
	v_lshlrev_b32_e32 v28, 16, v24
	v_and_b32_e32 v31, 0xffff0000, v25
	v_mul_f32_e32 v29, v29, v29
	v_cvt_pk_bf16_f32 v26, v26, v27
	v_cvt_pk_bf16_f32 v27, v32, v33
	v_lshlrev_b32_e32 v30, 16, v25
	v_fmac_f32_e32 v29, v28, v28
	v_mul_f32_e32 v28, v31, v31
	v_and_b32_e32 v33, 0xffff0000, v26
	v_and_b32_e32 v35, 0xffff0000, v27
	v_fmac_f32_e32 v28, v30, v30
	v_lshlrev_b32_e32 v32, 16, v26
	v_lshlrev_b32_e32 v34, 16, v27
	v_add_f32_e32 v28, v29, v28
	v_mul_f32_e32 v29, v33, v33
	v_mul_f32_e32 v30, v35, v35
	v_fmac_f32_e32 v29, v32, v32
	v_fmac_f32_e32 v30, v34, v34
	v_add_f32_e32 v29, v29, v30
	v_add_f32_e32 v36, v28, v29
	s_waitcnt vmcnt(6)
	v_lshlrev_b32_e32 v28, 16, v72
	v_and_b32_e32 v29, 0xffff0000, v72
	v_lshlrev_b32_e32 v30, 16, v73
	v_and_b32_e32 v31, 0xffff0000, v73
	v_lshlrev_b32_e32 v32, 16, v74
	v_and_b32_e32 v33, 0xffff0000, v74
	v_lshlrev_b32_e32 v34, 16, v75
	v_and_b32_e32 v35, 0xffff0000, v75
	v_pk_add_f32 v[20:21], v[20:21], v[28:29]
	v_pk_add_f32 v[22:23], v[22:23], v[30:31]
	v_pk_add_f32 v[28:29], v[18:19], v[34:35]
	v_pk_add_f32 v[16:17], v[16:17], v[32:33]
	v_cvt_pk_bf16_f32 v18, v20, v21
	v_cvt_pk_bf16_f32 v19, v22, v23
	v_cvt_pk_bf16_f32 v20, v16, v17
	v_and_b32_e32 v17, 0xffff0000, v18
	v_lshlrev_b32_e32 v16, 16, v18
	v_and_b32_e32 v23, 0xffff0000, v19
	v_mul_f32_e32 v17, v17, v17
	v_cvt_pk_bf16_f32 v21, v28, v29
	v_lshlrev_b32_e32 v22, 16, v19
	v_fmac_f32_e32 v17, v16, v16
	v_mul_f32_e32 v16, v23, v23
	v_and_b32_e32 v29, 0xffff0000, v20
	v_and_b32_e32 v31, 0xffff0000, v21
	v_fmac_f32_e32 v16, v22, v22
	v_lshlrev_b32_e32 v28, 16, v20
	v_lshlrev_b32_e32 v30, 16, v21
	v_add_f32_e32 v16, v17, v16
	v_mul_f32_e32 v17, v29, v29
	v_mul_f32_e32 v22, v31, v31
	v_fmac_f32_e32 v17, v28, v28
	v_fmac_f32_e32 v22, v30, v30
	v_add_f32_e32 v17, v17, v22
	v_add_f32_e32 v16, v16, v17
	v_add_f32_e32 v16, v36, v16
	v_mov_b32_e32 v17, v16
	v_lshlrev_b64 v[22:23], 11, v[94:95]
	v_lshl_add_u64 v[22:23], v[22:23], 1, s[0:1]
	v_lshl_add_u64 v[22:23], v[156:157], 1, v[22:23]
	global_store_dwordx4 v[22:23], v[24:27], off
	global_store_dwordx4 v[22:23], v[18:21], off offset:256
	s_waitcnt lgkmcnt(0)
	s_nop 1
	v_permlane16_swap_b32_e32 v16, v17
	v_add_f32_e32 v16, v16, v17
	ds_bpermute_b32 v17, v173, v16
	s_and_saveexec_b64 s[14:15], vcc
	s_cbranch_execz .LBB0_1471
	s_waitcnt lgkmcnt(0)
	v_add_f32_e32 v16, v16, v17
	v_lshl_add_u32 v17, v183, 4, s65
	ds_write_b32 v17, v16
.LBB0_1471:
	s_or_b64 exec, exec, s[14:15]
	s_waitcnt vmcnt(7)
	v_lshlrev_b32_e32 v16, 16, v68
	s_waitcnt lgkmcnt(0)
	v_and_b32_e32 v17, 0xffff0000, v68
	v_lshlrev_b32_e32 v18, 16, v69
	v_and_b32_e32 v19, 0xffff0000, v69
	v_lshlrev_b32_e32 v20, 16, v70
	v_and_b32_e32 v21, 0xffff0000, v70
	v_lshlrev_b32_e32 v22, 16, v71
	v_and_b32_e32 v23, 0xffff0000, v71
	v_pk_add_f32 v[12:13], v[12:13], v[16:17]
	v_pk_add_f32 v[14:15], v[14:15], v[18:19]
	v_pk_add_f32 v[16:17], v[10:11], v[22:23]
	v_pk_add_f32 v[10:11], v[8:9], v[20:21]
	v_cvt_pk_bf16_f32 v8, v12, v13
	v_cvt_pk_bf16_f32 v9, v14, v15
	v_and_b32_e32 v13, 0xffff0000, v8
	v_lshlrev_b32_e32 v12, 16, v8
	v_and_b32_e32 v15, 0xffff0000, v9
	v_mul_f32_e32 v13, v13, v13
	v_cvt_pk_bf16_f32 v10, v10, v11
	v_cvt_pk_bf16_f32 v11, v16, v17
	v_lshlrev_b32_e32 v14, 16, v9
	v_fmac_f32_e32 v13, v12, v12
	v_mul_f32_e32 v12, v15, v15
	v_and_b32_e32 v17, 0xffff0000, v10
	v_and_b32_e32 v19, 0xffff0000, v11
	v_fmac_f32_e32 v12, v14, v14
	v_lshlrev_b32_e32 v16, 16, v10
	v_lshlrev_b32_e32 v18, 16, v11
	v_add_f32_e32 v12, v13, v12
	v_mul_f32_e32 v13, v17, v17
	v_mul_f32_e32 v14, v19, v19
	v_fmac_f32_e32 v13, v16, v16
	v_fmac_f32_e32 v14, v18, v18
	v_add_f32_e32 v13, v13, v14
	v_add_f32_e32 v20, v12, v13
	s_waitcnt vmcnt(6)
	v_lshlrev_b32_e32 v12, 16, v64
	v_and_b32_e32 v13, 0xffff0000, v64
	v_lshlrev_b32_e32 v14, 16, v65
	v_and_b32_e32 v15, 0xffff0000, v65
	v_lshlrev_b32_e32 v16, 16, v66
	v_and_b32_e32 v17, 0xffff0000, v66
	v_lshlrev_b32_e32 v18, 16, v67
	v_and_b32_e32 v19, 0xffff0000, v67
	v_pk_add_f32 v[4:5], v[4:5], v[12:13]
	v_pk_add_f32 v[6:7], v[6:7], v[14:15]
	v_pk_add_f32 v[12:13], v[2:3], v[18:19]
	v_pk_add_f32 v[0:1], v[0:1], v[16:17]
	v_cvt_pk_bf16_f32 v2, v4, v5
	v_cvt_pk_bf16_f32 v3, v6, v7
	v_cvt_pk_bf16_f32 v4, v0, v1
	v_and_b32_e32 v1, 0xffff0000, v2
	v_lshlrev_b32_e32 v0, 16, v2
	v_and_b32_e32 v7, 0xffff0000, v3
	v_mul_f32_e32 v1, v1, v1
	v_cvt_pk_bf16_f32 v5, v12, v13
	v_lshlrev_b32_e32 v6, 16, v3
	v_fmac_f32_e32 v1, v0, v0
	v_mul_f32_e32 v0, v7, v7
	v_and_b32_e32 v13, 0xffff0000, v4
	v_and_b32_e32 v15, 0xffff0000, v5
	v_fmac_f32_e32 v0, v6, v6
	v_lshlrev_b32_e32 v12, 16, v4
	v_lshlrev_b32_e32 v14, 16, v5
	v_add_f32_e32 v0, v1, v0
	v_mul_f32_e32 v1, v13, v13
	v_mul_f32_e32 v6, v15, v15
	v_fmac_f32_e32 v1, v12, v12
	v_fmac_f32_e32 v6, v14, v14
	v_add_f32_e32 v1, v1, v6
	v_add_f32_e32 v0, v0, v1
	v_add_f32_e32 v0, v20, v0
	v_mov_b32_e32 v1, v0
	v_lshlrev_b64 v[6:7], 11, v[92:93]
	v_lshl_add_u64 v[6:7], v[6:7], 1, s[0:1]
	v_lshl_add_u64 v[6:7], v[156:157], 1, v[6:7]
	global_store_dwordx4 v[6:7], v[8:11], off
	global_store_dwordx4 v[6:7], v[2:5], off offset:256
	s_waitcnt lgkmcnt(0)
	s_nop 1
	v_permlane16_swap_b32_e32 v0, v1
	v_add_f32_e32 v0, v0, v1
	ds_bpermute_b32 v1, v173, v0
	s_and_saveexec_b64 s[14:15], vcc
	s_cbranch_execz .LBB0_1473
	s_waitcnt lgkmcnt(0)
	v_add_f32_e32 v0, v0, v1
	v_lshl_add_u32 v1, v183, 4, s66
	ds_write_b32 v1, v0

.LBB0_1524:
	s_cmp_lt_u32 s3, 0x40001
	s_mov_b64 s[22:23], 0
	s_cselect_b64 s[24:25], -1, 0
	s_mov_b64 s[26:27], -1
	s_and_b64 vcc, exec, s[24:25]
	s_cbranch_vccnz .LBB0_1521
	s_branch .LBB0_1518
	s_nop 0
	s_nop 0
	s_nop 0
	s_nop 0
	s_nop 0
	s_nop 0
	s_nop 0
	s_nop 0
	s_nop 0
	s_nop 0
	s_nop 0
	s_nop 0
	s_nop 0
	s_nop 0
	s_nop 0
	s_nop 0
	s_nop 0
	s_nop 0
	s_nop 0
	s_nop 0
	s_nop 0
	s_nop 0
	s_nop 0
	s_nop 0
	s_nop 0
	s_nop 0
	s_nop 0
	s_nop 0
	s_nop 0
	s_nop 0
	s_nop 0
	s_nop 0
	s_nop 0
	s_nop 0
	s_nop 0
	s_nop 0
	s_nop 0
	s_nop 0
	s_nop 0
	s_nop 0
	s_nop 0
	s_nop 0
	s_nop 0
	s_nop 0
	s_nop 0
	s_nop 0
	s_nop 0
	s_nop 0
	s_nop 0
	s_nop 0
	s_nop 0
	s_nop 0
	s_nop 0
	s_nop 0
	s_nop 0
	s_nop 0

; DI unsigned pk2(float lo, float hi) { const f32x2 v = {lo, hi}; return __builtin_bit_cast(unsigned, __builtin_convertvector(v, bf16x2_t)); }
; template <int MODE, bool SB  > DI void norm_phase(const Params& P, const Frame& F, int L, const void* src_, const float* gain, bool combine) {
;     ...
;     for (int row = r_lo + F.wave; row < r_hi; row += NWAVES) {
;         f32x4 v[8];
; #pragma unroll
;         for (int j = 0; j < 8; ++j) { if constexpr (SB) v[j] = (f32x4){bflo(vb[j].x), bfhi(vb[j].x), bflo(vb[j].y), bfhi(vb[j].y)}; else v[j] = vn[j]; }
;         { const int rnx = (row + NWAVES < r_hi) ? row + NWAVES : row;
; #pragma unroll
;           for (int j = 0; j < 8; ++j) { if constexpr (SB) vb[j] = *(const u32x2*)(srcb + (size_t)rnx * D + 4 * F.lane + 256 * j); else vn[j] = *(const f32x4*)(src + (size_t)rnx * D + 4 * F.lane + 256 * j); } }
;         if (MODE == 3 && combine) {
;             const int* SLOT = (const int*)(ws + WS_SLOT); const float* TOPW = (const float*)(ws + WS_TOPW); const bf16* Y = (const bf16*)(ws + WS_T + T_YPERM);
;             const int s1 = SLOT[row * 2], s2 = SLOT[row * 2 + 1]; const float w1 = TOPW[row * 2], w2 = TOPW[row * 2 + 1];
;             u32x2 ya[8], yb[8];
; #pragma unroll
;             for (int j = 0; j < 8; ++j) { ya[j] = *(const u32x2*)(Y + (size_t)s1 * D + 4 * F.lane + 256 * j); yb[j] = *(const u32x2*)(Y + (size_t)s2 * D + 4 * F.lane + 256 * j); }
; #pragma unroll
;             for (int j = 0; j < 8; ++j) { const f32x4 y1 = (f32x4){bflo(ya[j].x), bfhi(ya[j].x), bflo(ya[j].y), bfhi(ya[j].y)}, y2 = (f32x4){bflo(yb[j].x), bfhi(yb[j].x), bflo(yb[j].y), bfhi(yb[j].y)};
;                 v[j] = v[j] + w1 * y1 + w2 * y2;
;                 const u32x2 hb = {pk2(v[j][0], v[j][1]), pk2(v[j][2], v[j][3])}; *(u32x2*)(const_cast<bf16*>(srcb) + (size_t)row * D + 4 * F.lane + 256 * j) = hb;
;                 v[j] = (f32x4){bflo(hb.x), bfhi(hb.x), bflo(hb.y), bfhi(hb.y)}; }
;         }
;         float ss = 0.f;
; #pragma unroll
;         for (int j = 0; j < 8; ++j) ss += (v[j][0] * v[j][0] + v[j][1] * v[j][1]) + (v[j][2] * v[j][2] + v[j][3] * v[j][3]);
;         const float rstd = 1.0f / sqrtf(wave_sum(ss) * (1.0f / D) + EPS);
; #pragma unroll
;         for (int j = 0; j < 8; ++j) v[j] = v[j] * rstd * g[j];
.LBB0_1648:
	s_waitcnt vmcnt(0)
	v_and_b32_e32 v75, 0xffff0000, v50
	v_and_b32_e32 v77, 0xffff0000, v51
	v_lshlrev_b32_e32 v65, 16, v48
	v_and_b32_e32 v69, 0xffff0000, v48
	v_lshlrev_b32_e32 v74, 16, v50
	v_lshlrev_b32_e32 v76, 16, v51
	v_mul_f32_e32 v48, v77, v77
	v_lshlrev_b32_e32 v78, 16, v52
	v_and_b32_e32 v81, 0xffff0000, v53
	v_and_b32_e32 v80, 0xffff0000, v52
	v_mul_f32_e32 v52, v75, v75
	v_lshlrev_b32_e32 v72, 16, v49
	v_and_b32_e32 v73, 0xffff0000, v49
	v_pk_fma_f32 v[48:49], v[76:77], v[76:77], v[48:49] op_sel_hi:[1,1,0]
	v_lshlrev_b32_e32 v79, 16, v53
	v_pk_mul_f32 v[50:51], v[80:81], v[80:81]
	v_pk_fma_f32 v[52:53], v[74:75], v[74:75], v[52:53] op_sel_hi:[1,1,0]
	v_pk_fma_f32 v[50:51], v[78:79], v[78:79], v[50:51]
	v_lshlrev_b32_e32 v82, 16, v54
	v_and_b32_e32 v83, 0xffff0000, v54
	v_lshlrev_b32_e32 v84, 16, v55
	v_and_b32_e32 v85, 0xffff0000, v55
	v_mov_b32_e32 v64, v52
	v_mov_b32_e32 v54, v48
	v_mov_b32_e32 v55, v65
	v_mul_f32_e32 v47, v69, v69
	v_pk_add_f32 v[48:49], v[52:53], v[48:49]
	v_pk_mul_f32 v[52:53], v[64:65], v[54:55]
	v_pk_add_f32 v[50:51], v[50:51], v[50:51] op_sel:[0,1] op_sel_hi:[1,0]
	v_mov_b32_e32 v49, v53
	v_mov_b32_e32 v51, v47
	v_pk_add_f32 v[48:49], v[48:49], v[50:51]
	v_mul_f32_e32 v50, v83, v83
	v_mul_f32_e32 v52, v85, v85
	v_lshlrev_b32_e32 v97, 16, v56
	v_and_b32_e32 v71, 0xffff0000, v56
	v_lshlrev_b32_e32 v66, 16, v57
	v_and_b32_e32 v67, 0xffff0000, v57
	v_mul_f32_e32 v56, v72, v72
	v_mul_f32_e32 v57, v73, v73
	v_pk_fma_f32 v[50:51], v[82:83], v[82:83], v[50:51] op_sel_hi:[1,1,0]
	v_pk_fma_f32 v[52:53], v[84:85], v[84:85], v[52:53] op_sel_hi:[1,1,0]
	v_mov_b32_e32 v51, v56
	v_mov_b32_e32 v53, v57
	v_pk_add_f32 v[50:51], v[50:51], v[52:53]
	v_and_b32_e32 v173, 0xffff0000, v59
	v_and_b32_e32 v172, 0xffff0000, v58
	v_pk_add_f32 v[48:49], v[48:49], v[50:51]
	v_lshlrev_b32_e32 v171, 16, v59
	v_lshlrev_b32_e32 v170, 16, v58
	v_pk_mul_f32 v[50:51], v[172:173], v[172:173]
	v_and_b32_e32 v177, 0xffff0000, v61
	v_pk_fma_f32 v[50:51], v[170:171], v[170:171], v[50:51]
	v_and_b32_e32 v176, 0xffff0000, v60
	v_pk_add_f32 v[50:51], v[50:51], v[50:51] op_sel:[0,1] op_sel_hi:[1,0]
	v_pk_add_f32 v[48:49], v[48:49], v[48:49] op_sel:[0,1] op_sel_hi:[1,0]
	v_lshlrev_b32_e32 v175, 16, v61
	v_lshlrev_b32_e32 v174, 16, v60
	v_pk_mul_f32 v[52:53], v[176:177], v[176:177]
	v_mov_b32_e32 v96, v48
	v_mov_b32_e32 v54, v50
	v_mov_b32_e32 v55, v97
	v_pk_fma_f32 v[52:53], v[174:175], v[174:175], v[52:53]
	v_pk_add_f32 v[48:49], v[48:49], v[50:51]
	v_pk_mul_f32 v[50:51], v[96:97], v[54:55]
	v_mul_f32_e32 v47, v71, v71
	v_mov_b32_e32 v49, v51
	v_pk_add_f32 v[50:51], v[52:53], v[52:53] op_sel:[0,1] op_sel_hi:[1,0]
	v_and_b32_e32 v179, 0xffff0000, v62
	v_and_b32_e32 v181, 0xffff0000, v63
	v_mov_b32_e32 v51, v47
	v_lshlrev_b32_e32 v178, 16, v62
	v_lshlrev_b32_e32 v180, 16, v63
	v_pk_add_f32 v[48:49], v[48:49], v[50:51]
	v_mul_f32_e32 v50, v179, v179
	v_mul_f32_e32 v52, v181, v181
	v_mul_f32_e32 v56, v66, v66
	v_mul_f32_e32 v57, v67, v67
	v_pk_fma_f32 v[50:51], v[178:179], v[178:179], v[50:51] op_sel_hi:[1,1,0]
	v_pk_fma_f32 v[52:53], v[180:181], v[180:181], v[52:53] op_sel_hi:[1,1,0]
	v_mov_b32_e32 v51, v56
	v_mov_b32_e32 v53, v57
	v_pk_add_f32 v[50:51], v[50:51], v[52:53]
	s_mov_b32 s20, s0
	v_pk_add_f32 v[48:49], v[48:49], v[50:51]
	s_add_i32 s0, s0, 8
	v_add_f32_e32 v47, v48, v49
	s_cmp_ge_i32 s0, s3
	s_cselect_b64 s[22:23], -1, 0
	v_add_f32_dpp v47, v47, v47 quad_perm:[1,0,3,2] row_mask:0xf bank_mask:0xf bound_ctrl:1
	s_cmp_lt_i32 s0, s3
	s_cselect_b32 s20, s0, s20
	v_add_f32_dpp v47, v47, v47 quad_perm:[2,3,0,1] row_mask:0xf bank_mask:0xf bound_ctrl:1
	ds_swizzle_b32 v48, v47 offset:swizzle(SWAP,4)
	s_ashr_i32 s21, s20, 31
	s_lshl_b64 s[20:21], s[20:21], 12
	v_lshl_add_u64 v[56:57], v[32:33], 0, s[20:21]
	s_mov_b32 s20, 0xf800000
	s_waitcnt lgkmcnt(0)
	v_add_f32_e32 v47, v47, v48
	ds_swizzle_b32 v48, v47 offset:swizzle(SWAP,8)
	s_waitcnt lgkmcnt(0)
	v_add_f32_e32 v47, v47, v48
	v_mov_b32_e32 v48, v47
	s_waitcnt lgkmcnt(0)
	s_nop 1
	v_permlane16_swap_b32_e32 v47, v48
	v_add_f32_e32 v47, v47, v48
	v_mov_b32_e32 v48, v47
	s_waitcnt lgkmcnt(0)
	s_nop 1
	v_permlane32_swap_b32_e32 v47, v48
	v_add_f32_e32 v47, v47, v48
	v_fmamk_f32 v47, v47, 0x3a000000, v164
	v_mul_f32_e32 v48, 0x4f800000, v47
	v_cmp_gt_f32_e32 vcc, s20, v47
	s_nop 1
	v_cndmask_b32_e32 v47, v47, v48, vcc
	v_sqrt_f32_e32 v58, v47
	global_load_dwordx2 v[50:51], v[56:57], off
	global_load_dwordx2 v[52:53], v[56:57], off offset:512
	global_load_dwordx2 v[54:55], v[56:57], off offset:1024
	global_load_dwordx2 v[48:49], v[56:57], off offset:1536
	v_add_u32_e32 v59, -1, v58
	v_fma_f32 v60, -v59, v58, v47
	v_cmp_ge_f32_e64 s[20:21], 0, v60
	v_add_u32_e32 v60, 1, v58
	s_nop 0
	v_cndmask_b32_e64 v59, v58, v59, s[20:21]
	v_fma_f32 v58, -v60, v58, v47
	v_cmp_lt_f32_e64 s[20:21], 0, v58
	s_nop 1
	v_cndmask_b32_e64 v58, v59, v60, s[20:21]
	v_mul_f32_e32 v59, 0x37800000, v58
	v_cndmask_b32_e32 v58, v58, v59, vcc
	v_cmp_class_f32_e32 vcc, v47, v165
	s_nop 1
	v_cndmask_b32_e32 v47, v58, v47, vcc
	v_div_scale_f32 v64, s[20:21], v47, v47, 1.0
	v_rcp_f32_e32 v68, v64
	s_mov_b32 s20, 0x3d600000
	global_load_dwordx2 v[58:59], v[56:57], off offset:2048
	global_load_dwordx2 v[60:61], v[56:57], off offset:2560
	global_load_dwordx2 v[62:63], v[56:57], off offset:3072
	s_nop 0
	global_load_dwordx2 v[56:57], v[56:57], off offset:3584
	v_fma_f32 v70, -v64, v68, 1.0
	v_fmac_f32_e32 v68, v70, v68
	v_div_scale_f32 v70, vcc, 1.0, v47, 1.0
	v_mul_f32_e32 v86, v70, v68
	v_fma_f32 v87, -v64, v86, v70
	v_fmac_f32_e32 v86, v87, v68
	v_fma_f32 v64, -v64, v86, v70
	v_div_fmas_f32 v64, v64, v68, v86
; #define LAS __attribute__((address_space(3)))
; DI unsigned pk2(float lo, float hi) { const f32x2 v = {lo, hi}; return __builtin_bit_cast(unsigned, __builtin_convertvector(v, bf16x2_t)); }
; DI unsigned pk4_fp8(float a, float b, float c, float d) { unsigned w = 0u; w = __builtin_amdgcn_cvt_pk_fp8_f32(a, b, w, false); w = __builtin_amdgcn_cvt_pk_fp8_f32(c, d, w, true); return w; }
; template <int MODE, bool SB  > DI void norm_phase(const Params& P, const Frame& F, int L, const void* src_, const float* gain, bool combine) {
;     ...
;         for (int j = 0; j < 8; ++j) v[j] = v[j] * rstd * g[j];
;         if (MODE == 4) {
; #pragma unroll
;             for (int j = 0; j < 8; ++j) *(f32x4*)(P.out + (size_t)row * D + 4 * F.lane + 256 * j) = v[j];
;         } else if (MODE == 0 || MODE == 2 || (MODE == 3 && L == 1)) {
;             unsigned* o4 = (unsigned*)((unsigned char*)HN + (size_t)row * D) + F.lane; const float hs = (float)(1 << LS_HN);
; #pragma unroll
;             for (int j = 0; j < 8; ++j) o4[64 * j] = pk4_fp8(v[j][0] * hs, v[j][1] * hs, v[j][2] * hs, v[j][3] * hs);
;         } else {
;             unsigned long long* o8 = (unsigned long long*)(HN + (size_t)row * D) + F.lane;
; #pragma unroll
;             for (int j = 0; j < 8; ++j) o8[64 * j] = (unsigned long long)pk2(v[j][0], v[j][1]) | ((unsigned long long)pk2(v[j][2], v[j][3]) << 32);
;         }
;         if (MODE == 1) {
;             float s[16];
; #pragma unroll
;             for (int q = 0; q < 16; ++q) { float t = 0.f;
; #pragma unroll
;                 for (int j = 0; j < 8; ++j) { const f32x4 w = *(const LAS f32x4*)(F.lds + (size_t)(q * D + 256 * j + 4 * F.lane) * 4); t += (v[j][0] * w[0] + v[j][1] * w[1]) + (v[j][2] * w[2] + v[j][3] * w[3]); }
;                 s[q] = t; if ((q & 3) == 3) asm volatile("" ::: "memory"); }
	v_div_fixup_f32 v96, v64, v47, 1.0
	v_pk_mul_f32 v[74:75], v[96:97], v[74:75] op_sel_hi:[0,1]
	v_mov_b32_e32 v68, v65
	v_pk_mul_f32 v[76:77], v[96:97], v[76:77] op_sel_hi:[0,1]
	v_pk_mul_f32 v[92:93], v[8:9], v[74:75]
	v_mov_b32_e32 v75, v80
	v_mov_b32_e32 v80, v79
	v_pk_mul_f32 v[64:65], v[68:69], v[96:97] op_sel_hi:[1,0]
	v_pk_mul_f32 v[90:91], v[10:11], v[76:77]
	v_mov_b32_e32 v74, v78
	v_pk_mul_f32 v[76:77], v[96:97], v[80:81] op_sel_hi:[0,1]
	v_pk_mul_f32 v[86:87], v[12:13], v[64:65]
	v_mov_b32_e32 v64, v170
	v_mov_b32_e32 v65, v172
	v_pk_mul_f32 v[74:75], v[96:97], v[74:75] op_sel_hi:[0,1]
	v_pk_mul_f32 v[88:89], v[2:3], v[76:77]
	v_pk_mul_f32 v[76:77], v[96:97], v[84:85] op_sel_hi:[0,1]
	v_pk_mul_f32 v[68:69], v[72:73], v[96:97] op_sel_hi:[1,0]
	v_pk_mul_f32 v[64:65], v[96:97], v[64:65] op_sel_hi:[0,1]
	v_mov_b32_e32 v172, v171
	v_pk_mul_f32 v[94:95], v[0:1], v[74:75]
	v_pk_mul_f32 v[74:75], v[96:97], v[82:83] op_sel_hi:[0,1]
	v_pk_mul_f32 v[82:83], v[6:7], v[76:77]
	v_pk_mul_f32 v[78:79], v[14:15], v[68:69]
	v_pk_mul_f32 v[68:69], v[96:97], v[172:173] op_sel_hi:[0,1]
	v_pk_mul_f32 v[76:77], v[16:17], v[64:65]
	v_mov_b32_e32 v64, v174
	v_mov_b32_e32 v65, v176
	v_mov_b32_e32 v176, v175
	v_pk_mul_f32 v[84:85], v[4:5], v[74:75]
	v_pk_mul_f32 v[74:75], v[18:19], v[68:69]
	v_pk_mul_f32 v[64:65], v[96:97], v[64:65] op_sel_hi:[0,1]
	v_pk_mul_f32 v[68:69], v[96:97], v[176:177] op_sel_hi:[0,1]
	v_mov_b32_e32 v70, v97
	v_pk_mul_f32 v[72:73], v[22:23], v[68:69]
	v_pk_mul_f32 v[80:81], v[20:21], v[64:65]
	v_pk_mul_f32 v[68:69], v[96:97], v[178:179] op_sel_hi:[0,1]
	v_pk_mul_f32 v[64:65], v[96:97], v[180:181] op_sel_hi:[0,1]
	v_pk_mul_f32 v[70:71], v[70:71], v[96:97] op_sel_hi:[1,0]
	v_pk_mul_f32 v[66:67], v[66:67], v[96:97] op_sel_hi:[1,0]
	v_lshl_add_u64 v[96:97], s[54:55], 0, v[44:45]
	v_add_co_u32_e32 v96, vcc, s20, v96
	v_cvt_pk_bf16_f32 v170, v92, v93
	v_cvt_pk_bf16_f32 v171, v90, v91
	v_addc_co_u32_e32 v97, vcc, 0, v97, vcc
	global_store_dwordx2 v[96:97], v[170:171], off
	v_cvt_pk_bf16_f32 v170, v94, v95
	v_cvt_pk_bf16_f32 v171, v88, v89
	global_store_dwordx2 v[96:97], v[170:171], off offset:512
	v_cvt_pk_bf16_f32 v170, v84, v85
	v_cvt_pk_bf16_f32 v171, v82, v83
	global_store_dwordx2 v[96:97], v[170:171], off offset:1024
	v_cvt_pk_bf16_f32 v170, v86, v87
	v_cvt_pk_bf16_f32 v171, v78, v79
	global_store_dwordx2 v[96:97], v[170:171], off offset:1536
	v_cvt_pk_bf16_f32 v170, v76, v77
	v_cvt_pk_bf16_f32 v171, v74, v75
	v_pk_mul_f32 v[64:65], v[26:27], v[64:65]
	v_pk_mul_f32 v[68:69], v[24:25], v[68:69]
	global_store_dwordx2 v[96:97], v[170:171], off offset:2048
	v_cvt_pk_bf16_f32 v170, v80, v81
	v_cvt_pk_bf16_f32 v171, v72, v73
	global_store_dwordx2 v[96:97], v[170:171], off offset:2560
	v_cvt_pk_bf16_f32 v170, v68, v69
	v_cvt_pk_bf16_f32 v171, v64, v65
	global_store_dwordx2 v[96:97], v[170:171], off offset:3072
	ds_read_b128 v[170:173], v99
	v_pk_mul_f32 v[66:67], v[30:31], v[66:67]
	v_pk_mul_f32 v[70:71], v[28:29], v[70:71]
	v_cvt_pk_bf16_f32 v175, v66, v67
	v_cvt_pk_bf16_f32 v174, v70, v71
	global_store_dwordx2 v[96:97], v[174:175], off offset:3584
	ds_read_b128 v[174:177], v99 offset:1024
	s_waitcnt lgkmcnt(1)
	v_mul_f32_e32 v47, v171, v93
	v_mul_f32_e32 v96, v173, v91
	v_fmac_f32_e32 v47, v170, v92
	v_fmac_f32_e32 v96, v172, v90
	ds_read_b128 v[170:173], v99 offset:2048
	v_add_f32_e32 v47, v47, v96
	s_waitcnt lgkmcnt(1)
	v_mul_f32_e32 v96, v95, v175
	v_mul_f32_e32 v97, v89, v177
	v_fmac_f32_e32 v96, v94, v174
	v_fmac_f32_e32 v97, v88, v176
	ds_read_b128 v[174:177], v99 offset:3072
	v_add_f32_e32 v47, 0, v47
	v_add_f32_e32 v96, v96, v97
	v_add_f32_e32 v47, v96, v47
	s_waitcnt lgkmcnt(1)
	v_mul_f32_e32 v96, v85, v171
	v_mul_f32_e32 v97, v83, v173
	v_fmac_f32_e32 v96, v84, v170
	v_fmac_f32_e32 v97, v82, v172
	ds_read_b128 v[170:173], v99 offset:4096
	v_add_f32_e32 v96, v96, v97
	v_add_f32_e32 v47, v96, v47
	s_waitcnt lgkmcnt(1)
	v_mul_f32_e32 v96, v87, v175
	v_mul_f32_e32 v97, v79, v177
	v_fmac_f32_e32 v96, v86, v174
	v_fmac_f32_e32 v97, v78, v176
	ds_read_b128 v[174:177], v99 offset:5120
	v_add_f32_e32 v96, v96, v97
	v_add_f32_e32 v47, v96, v47
	s_waitcnt lgkmcnt(1)
	v_mul_f32_e32 v96, v77, v171
	v_mul_f32_e32 v97, v75, v173
	v_fmac_f32_e32 v96, v76, v170
	v_fmac_f32_e32 v97, v74, v172
	ds_read_b128 v[170:173], v99 offset:6144
	v_add_f32_e32 v96, v96, v97
	v_add_f32_e32 v47, v96, v47
	s_waitcnt lgkmcnt(1)
	v_mul_f32_e32 v96, v81, v175
	v_mul_f32_e32 v97, v73, v177
	v_fmac_f32_e32 v96, v80, v174
	v_fmac_f32_e32 v97, v72, v176
	ds_read_b128 v[174:177], v99 offset:7168
	v_add_f32_e32 v96, v96, v97
	v_add_f32_e32 v47, v96, v47
	s_waitcnt lgkmcnt(1)
	v_mul_f32_e32 v96, v69, v171
	v_mul_f32_e32 v97, v65, v173
	v_fmac_f32_e32 v96, v68, v170
	v_fmac_f32_e32 v97, v64, v172
	v_add_f32_e32 v96, v96, v97
	ds_read_b128 v[170:173], v99 offset:8192
	v_add_f32_e32 v47, v96, v47
	s_waitcnt lgkmcnt(1)
	v_mul_f32_e32 v96, v71, v175
	v_mul_f32_e32 v97, v67, v177
	v_fmac_f32_e32 v96, v70, v174
	v_fmac_f32_e32 v97, v66, v176
	ds_read_b128 v[174:177], v99 offset:9216
	v_add_f32_e32 v96, v96, v97
	v_add_f32_e32 v47, v96, v47
	s_waitcnt lgkmcnt(1)
	v_mul_f32_e32 v96, v93, v171
	v_mul_f32_e32 v97, v91, v173
	v_fmac_f32_e32 v96, v92, v170
	v_fmac_f32_e32 v97, v90, v172
	ds_read_b128 v[170:173], v99 offset:10240
	v_add_f32_e32 v96, v96, v97
	s_waitcnt lgkmcnt(1)
	v_mul_f32_e32 v97, v95, v175
	v_fmac_f32_e32 v97, v94, v174
	v_mul_f32_e32 v174, v89, v177
	v_fmac_f32_e32 v174, v88, v176
	v_add_f32_e32 v96, 0, v96
	v_add_f32_e32 v97, v97, v174
	ds_read_b128 v[174:177], v99 offset:11264
	v_add_f32_e32 v96, v96, v97
	s_waitcnt lgkmcnt(1)
; #define LAS __attribute__((address_space(3)))
; template <int MODE, bool SB  > DI void norm_phase(const Params& P, const Frame& F, int L, const void* src_, const float* gain, bool combine) {
;     ...
;             for (int q = 0; q < 16; ++q) { float t = 0.f;
; #pragma unroll
;                 for (int j = 0; j < 8; ++j) { const f32x4 w = *(const LAS f32x4*)(F.lds + (size_t)(q * D + 256 * j + 4 * F.lane) * 4); t += (v[j][0] * w[0] + v[j][1] * w[1]) + (v[j][2] * w[2] + v[j][3] * w[3]); }
;                 s[q] = t; if ((q & 3) == 3) asm volatile("" ::: "memory"); }
	v_mul_f32_e32 v97, v85, v171
	v_fmac_f32_e32 v97, v84, v170
	v_mul_f32_e32 v170, v83, v173
	v_fmac_f32_e32 v170, v82, v172
	v_add_f32_e32 v97, v97, v170
	ds_read_b128 v[170:173], v99 offset:12288
	v_add_f32_e32 v96, v96, v97
	s_waitcnt lgkmcnt(1)
	v_mul_f32_e32 v97, v87, v175
	v_fmac_f32_e32 v97, v86, v174
	v_mul_f32_e32 v174, v79, v177
	v_fmac_f32_e32 v174, v78, v176
	v_add_f32_e32 v97, v97, v174
	ds_read_b128 v[174:177], v99 offset:13312
	v_add_f32_e32 v96, v96, v97
	s_waitcnt lgkmcnt(1)
	v_mul_f32_e32 v97, v77, v171
	v_fmac_f32_e32 v97, v76, v170
	v_mul_f32_e32 v170, v75, v173
	v_fmac_f32_e32 v170, v74, v172
	v_add_f32_e32 v97, v97, v170
	ds_read_b128 v[170:173], v99 offset:14336
	v_add_f32_e32 v96, v96, v97
	s_waitcnt lgkmcnt(1)
	v_mul_f32_e32 v97, v81, v175
	v_fmac_f32_e32 v97, v80, v174
	v_mul_f32_e32 v174, v73, v177
	v_fmac_f32_e32 v174, v72, v176
	v_add_f32_e32 v97, v97, v174
	ds_read_b128 v[174:177], v99 offset:15360
	v_add_f32_e32 v96, v96, v97
	s_waitcnt lgkmcnt(1)
	v_mul_f32_e32 v97, v69, v171
	v_fmac_f32_e32 v97, v68, v170
	v_mul_f32_e32 v170, v65, v173
	v_fmac_f32_e32 v170, v64, v172
	v_add_f32_e32 v97, v97, v170
	v_add_f32_e32 v96, v96, v97
	s_waitcnt lgkmcnt(0)
	v_mul_f32_e32 v97, v71, v175
	v_fmac_f32_e32 v97, v70, v174
	v_mul_f32_e32 v174, v67, v177
	ds_read_b128 v[170:173], v99 offset:16384
	v_fmac_f32_e32 v174, v66, v176
	v_add_f32_e32 v97, v97, v174
	ds_read_b128 v[174:177], v99 offset:17408
	v_add_f32_e32 v96, v96, v97
	s_waitcnt lgkmcnt(1)
	v_mul_f32_e32 v97, v93, v171
	v_fmac_f32_e32 v97, v92, v170
	v_mul_f32_e32 v170, v91, v173
	v_fmac_f32_e32 v170, v90, v172
	s_waitcnt lgkmcnt(0)
	v_mul_f32_e32 v175, v95, v175
	v_add_f32_e32 v97, v97, v170
	v_fmac_f32_e32 v175, v94, v174
	v_mul_f32_e32 v174, v89, v177
	ds_read_b128 v[170:173], v99 offset:18432
	v_fmac_f32_e32 v174, v88, v176
	v_add_f32_e32 v97, 0, v97
	v_add_f32_e32 v174, v175, v174
	v_add_f32_e32 v97, v97, v174
	ds_read_b128 v[174:177], v99 offset:19456
	s_waitcnt lgkmcnt(1)
	v_mul_f32_e32 v171, v85, v171
	v_fmac_f32_e32 v171, v84, v170
	v_mul_f32_e32 v170, v83, v173
	v_fmac_f32_e32 v170, v82, v172
	v_add_f32_e32 v170, v171, v170
	s_waitcnt lgkmcnt(0)
	v_mul_f32_e32 v175, v87, v175
	v_add_f32_e32 v97, v97, v170
	v_fmac_f32_e32 v175, v86, v174
	v_mul_f32_e32 v174, v79, v177
	ds_read_b128 v[170:173], v99 offset:20480
	v_fmac_f32_e32 v174, v78, v176
	v_add_f32_e32 v174, v175, v174
	v_add_f32_e32 v97, v97, v174
	ds_read_b128 v[174:177], v99 offset:21504
	s_waitcnt lgkmcnt(1)
	v_mul_f32_e32 v171, v77, v171
	v_fmac_f32_e32 v171, v76, v170
	v_mul_f32_e32 v170, v75, v173
	v_fmac_f32_e32 v170, v74, v172
	v_add_f32_e32 v170, v171, v170
	s_waitcnt lgkmcnt(0)
	v_mul_f32_e32 v175, v81, v175
	v_add_f32_e32 v97, v97, v170
	v_fmac_f32_e32 v175, v80, v174
	v_mul_f32_e32 v174, v73, v177
	ds_read_b128 v[170:173], v99 offset:22528
	v_fmac_f32_e32 v174, v72, v176
	v_add_f32_e32 v174, v175, v174
	v_add_f32_e32 v97, v97, v174
	ds_read_b128 v[174:177], v99 offset:23552
	s_waitcnt lgkmcnt(1)
	v_mul_f32_e32 v171, v69, v171
	v_fmac_f32_e32 v171, v68, v170
	v_mul_f32_e32 v170, v65, v173
	v_fmac_f32_e32 v170, v64, v172
	v_add_f32_e32 v170, v171, v170
	s_waitcnt lgkmcnt(0)
	v_mul_f32_e32 v175, v71, v175
	v_add_f32_e32 v97, v97, v170
	v_fmac_f32_e32 v175, v70, v174
	v_mul_f32_e32 v174, v67, v177
	ds_read_b128 v[170:173], v99 offset:24576
	v_fmac_f32_e32 v174, v66, v176
	v_add_f32_e32 v174, v175, v174
	v_add_f32_e32 v97, v97, v174
	ds_read_b128 v[174:177], v99 offset:25600
	s_waitcnt lgkmcnt(1)
	v_mul_f32_e32 v171, v93, v171
	v_fmac_f32_e32 v171, v92, v170
	v_mul_f32_e32 v170, v91, v173
	v_fmac_f32_e32 v170, v90, v172
	v_add_f32_e32 v170, v171, v170
	s_waitcnt lgkmcnt(0)
	v_mul_f32_e32 v175, v95, v175
	v_add_f32_e32 v178, 0, v170
	v_fmac_f32_e32 v175, v94, v174
	v_mul_f32_e32 v174, v89, v177
	ds_read_b128 v[170:173], v99 offset:26624
	v_fmac_f32_e32 v174, v88, v176
	v_add_f32_e32 v174, v175, v174
	v_add_f32_e32 v178, v178, v174
	ds_read_b128 v[174:177], v99 offset:27648
	s_waitcnt lgkmcnt(1)
	v_mul_f32_e32 v171, v85, v171
	v_fmac_f32_e32 v171, v84, v170
	v_mul_f32_e32 v170, v83, v173
	v_fmac_f32_e32 v170, v82, v172
	v_add_f32_e32 v170, v171, v170
	s_waitcnt lgkmcnt(0)
	v_mul_f32_e32 v175, v87, v175
	v_add_f32_e32 v178, v178, v170
	v_fmac_f32_e32 v175, v86, v174
	v_mul_f32_e32 v174, v79, v177
	ds_read_b128 v[170:173], v99 offset:28672
	v_fmac_f32_e32 v174, v78, v176
	v_add_f32_e32 v174, v175, v174
	v_add_f32_e32 v178, v178, v174
	ds_read_b128 v[174:177], v99 offset:29696
	s_waitcnt lgkmcnt(1)
	v_mul_f32_e32 v171, v77, v171
	v_fmac_f32_e32 v171, v76, v170
	v_mul_f32_e32 v170, v75, v173
	v_fmac_f32_e32 v170, v74, v172
	v_add_f32_e32 v170, v171, v170
	s_waitcnt lgkmcnt(0)
	v_mul_f32_e32 v175, v81, v175
	v_add_f32_e32 v178, v178, v170
	v_fmac_f32_e32 v175, v80, v174
	v_mul_f32_e32 v174, v73, v177
	ds_read_b128 v[170:173], v99 offset:30720
	v_fmac_f32_e32 v174, v72, v176
	v_add_f32_e32 v174, v175, v174
	v_add_f32_e32 v178, v178, v174
	ds_read_b128 v[174:177], v99 offset:31744
	s_waitcnt lgkmcnt(1)
	v_mul_f32_e32 v171, v69, v171
	v_fmac_f32_e32 v171, v68, v170
	v_mul_f32_e32 v170, v65, v173
	v_fmac_f32_e32 v170, v64, v172
	v_add_f32_e32 v170, v171, v170
	s_waitcnt lgkmcnt(0)
	v_mul_f32_e32 v171, v71, v175
	v_fmac_f32_e32 v171, v70, v174
	v_mul_f32_e32 v177, v67, v177
	ds_read_b128 v[172:175], v99 offset:32768
	v_fmac_f32_e32 v177, v66, v176
	v_add_f32_e32 v170, v178, v170
	v_add_f32_e32 v171, v171, v177
	ds_read_b128 v[176:179], v99 offset:33792
	v_add_f32_e32 v170, v170, v171
	s_waitcnt lgkmcnt(1)
	v_mul_f32_e32 v171, v93, v173
	v_fmac_f32_e32 v171, v92, v172
	v_mul_f32_e32 v172, v91, v175
	v_fmac_f32_e32 v172, v90, v174
	s_waitcnt lgkmcnt(0)
; #define LAS __attribute__((address_space(3)))
; template <int MODE, bool SB  > DI void norm_phase(const Params& P, const Frame& F, int L, const void* src_, const float* gain, bool combine) {
;     ...
;             for (int q = 0; q < 16; ++q) { float t = 0.f;
; #pragma unroll
;                 for (int j = 0; j < 8; ++j) { const f32x4 w = *(const LAS f32x4*)(F.lds + (size_t)(q * D + 256 * j + 4 * F.lane) * 4); t += (v[j][0] * w[0] + v[j][1] * w[1]) + (v[j][2] * w[2] + v[j][3] * w[3]); }
;                 s[q] = t; if ((q & 3) == 3) asm volatile("" ::: "memory"); }
	v_mul_f32_e32 v177, v95, v177
	v_add_f32_e32 v171, v171, v172
	v_fmac_f32_e32 v177, v94, v176
	v_mul_f32_e32 v176, v89, v179
	ds_read_b128 v[172:175], v99 offset:34816
	v_fmac_f32_e32 v176, v88, v178
	v_add_f32_e32 v171, 0, v171
	v_add_f32_e32 v176, v177, v176
	v_add_f32_e32 v171, v171, v176
	ds_read_b128 v[176:179], v99 offset:35840
	s_waitcnt lgkmcnt(1)
	v_mul_f32_e32 v173, v85, v173
	v_fmac_f32_e32 v173, v84, v172
	v_mul_f32_e32 v172, v83, v175
	v_fmac_f32_e32 v172, v82, v174
	v_add_f32_e32 v172, v173, v172
	s_waitcnt lgkmcnt(0)
	v_mul_f32_e32 v177, v87, v177
	v_add_f32_e32 v171, v171, v172
	v_fmac_f32_e32 v177, v86, v176
	v_mul_f32_e32 v176, v79, v179
	ds_read_b128 v[172:175], v99 offset:36864
	v_fmac_f32_e32 v176, v78, v178
	v_add_f32_e32 v176, v177, v176
	v_add_f32_e32 v171, v171, v176
	ds_read_b128 v[176:179], v99 offset:37888
	s_waitcnt lgkmcnt(1)
	v_mul_f32_e32 v173, v77, v173
	v_fmac_f32_e32 v173, v76, v172
	v_mul_f32_e32 v172, v75, v175
	v_fmac_f32_e32 v172, v74, v174
	v_add_f32_e32 v172, v173, v172
	s_waitcnt lgkmcnt(0)
	v_mul_f32_e32 v177, v81, v177
	v_add_f32_e32 v171, v171, v172
	v_fmac_f32_e32 v177, v80, v176
	v_mul_f32_e32 v176, v73, v179
	ds_read_b128 v[172:175], v99 offset:38912
	v_fmac_f32_e32 v176, v72, v178
	v_add_f32_e32 v176, v177, v176
	v_add_f32_e32 v171, v171, v176
	ds_read_b128 v[176:179], v99 offset:39936
	s_waitcnt lgkmcnt(1)
	v_mul_f32_e32 v173, v69, v173
	v_fmac_f32_e32 v173, v68, v172
	v_mul_f32_e32 v172, v65, v175
	v_fmac_f32_e32 v172, v64, v174
	v_add_f32_e32 v172, v173, v172
	s_waitcnt lgkmcnt(0)
	v_mul_f32_e32 v177, v71, v177
	v_add_f32_e32 v171, v171, v172
	v_fmac_f32_e32 v177, v70, v176
	v_mul_f32_e32 v176, v67, v179
	ds_read_b128 v[172:175], v99 offset:40960
	v_fmac_f32_e32 v176, v66, v178
	v_add_f32_e32 v176, v177, v176
	v_add_f32_e32 v171, v171, v176
	ds_read_b128 v[176:179], v99 offset:41984
	s_waitcnt lgkmcnt(1)
	v_mul_f32_e32 v173, v93, v173
	v_fmac_f32_e32 v173, v92, v172
	v_mul_f32_e32 v172, v91, v175
	v_fmac_f32_e32 v172, v90, v174
	v_add_f32_e32 v172, v173, v172
	s_waitcnt lgkmcnt(0)
	v_mul_f32_e32 v177, v95, v177
	v_add_f32_e32 v180, 0, v172
	v_fmac_f32_e32 v177, v94, v176
	v_mul_f32_e32 v176, v89, v179
	ds_read_b128 v[172:175], v99 offset:43008
	v_fmac_f32_e32 v176, v88, v178
	v_add_f32_e32 v176, v177, v176
	v_add_f32_e32 v180, v180, v176
	ds_read_b128 v[176:179], v99 offset:44032
	s_waitcnt lgkmcnt(1)
	v_mul_f32_e32 v173, v85, v173
	v_fmac_f32_e32 v173, v84, v172
	v_mul_f32_e32 v172, v83, v175
	v_fmac_f32_e32 v172, v82, v174
	v_add_f32_e32 v172, v173, v172
	s_waitcnt lgkmcnt(0)
	v_mul_f32_e32 v177, v87, v177
	v_add_f32_e32 v180, v180, v172
	v_fmac_f32_e32 v177, v86, v176
	v_mul_f32_e32 v176, v79, v179
	ds_read_b128 v[172:175], v99 offset:45056
	v_fmac_f32_e32 v176, v78, v178
	v_add_f32_e32 v176, v177, v176
	v_add_f32_e32 v180, v180, v176
	ds_read_b128 v[176:179], v99 offset:46080
	s_waitcnt lgkmcnt(1)
	v_mul_f32_e32 v173, v77, v173
	v_fmac_f32_e32 v173, v76, v172
	v_mul_f32_e32 v172, v75, v175
	v_fmac_f32_e32 v172, v74, v174
	v_add_f32_e32 v172, v173, v172
	s_waitcnt lgkmcnt(0)
	v_mul_f32_e32 v177, v81, v177
	v_add_f32_e32 v180, v180, v172
	v_fmac_f32_e32 v177, v80, v176
	v_mul_f32_e32 v176, v73, v179
	ds_read_b128 v[172:175], v99 offset:47104
	v_fmac_f32_e32 v176, v72, v178
	v_add_f32_e32 v176, v177, v176
	v_add_f32_e32 v180, v180, v176
	ds_read_b128 v[176:179], v99 offset:48128
	s_waitcnt lgkmcnt(1)
	v_mul_f32_e32 v173, v69, v173
	v_fmac_f32_e32 v173, v68, v172
	v_mul_f32_e32 v172, v65, v175
	v_fmac_f32_e32 v172, v64, v174
	v_add_f32_e32 v172, v173, v172
	s_waitcnt lgkmcnt(0)
	v_mul_f32_e32 v173, v71, v177
	v_fmac_f32_e32 v173, v70, v176
	v_mul_f32_e32 v179, v67, v179
	ds_read_b128 v[174:177], v99 offset:49152
	v_fmac_f32_e32 v179, v66, v178
	v_add_f32_e32 v172, v180, v172
	v_add_f32_e32 v173, v173, v179
	ds_read_b128 v[178:181], v99 offset:50176
	v_add_f32_e32 v172, v172, v173
	s_waitcnt lgkmcnt(1)
	v_mul_f32_e32 v173, v93, v175
	v_fmac_f32_e32 v173, v92, v174
	v_mul_f32_e32 v174, v91, v177
	v_fmac_f32_e32 v174, v90, v176
	s_waitcnt lgkmcnt(0)
	v_mul_f32_e32 v179, v95, v179
	v_add_f32_e32 v173, v173, v174
	v_fmac_f32_e32 v179, v94, v178
	v_mul_f32_e32 v178, v89, v181
	ds_read_b128 v[174:177], v99 offset:51200
	v_fmac_f32_e32 v178, v88, v180
	v_add_f32_e32 v173, 0, v173
	v_add_f32_e32 v178, v179, v178
	v_add_f32_e32 v173, v173, v178
	ds_read_b128 v[178:181], v99 offset:52224
	s_waitcnt lgkmcnt(1)
	v_mul_f32_e32 v175, v85, v175
	v_fmac_f32_e32 v175, v84, v174
	v_mul_f32_e32 v174, v83, v177
	v_fmac_f32_e32 v174, v82, v176
	v_add_f32_e32 v174, v175, v174
	s_waitcnt lgkmcnt(0)
	v_mul_f32_e32 v179, v87, v179
	v_add_f32_e32 v173, v173, v174
	v_fmac_f32_e32 v179, v86, v178
	v_mul_f32_e32 v178, v79, v181
	ds_read_b128 v[174:177], v99 offset:53248
	v_fmac_f32_e32 v178, v78, v180
	v_add_f32_e32 v178, v179, v178
	v_add_f32_e32 v173, v173, v178
	ds_read_b128 v[178:181], v99 offset:54272
	s_waitcnt lgkmcnt(1)
	v_mul_f32_e32 v175, v77, v175
	v_fmac_f32_e32 v175, v76, v174
	v_mul_f32_e32 v174, v75, v177
	v_fmac_f32_e32 v174, v74, v176
	v_add_f32_e32 v174, v175, v174
	s_waitcnt lgkmcnt(0)
	v_mul_f32_e32 v179, v81, v179
	v_add_f32_e32 v173, v173, v174
	v_fmac_f32_e32 v179, v80, v178
	v_mul_f32_e32 v178, v73, v181
	ds_read_b128 v[174:177], v99 offset:55296
	v_fmac_f32_e32 v178, v72, v180
	v_add_f32_e32 v178, v179, v178
	v_add_f32_e32 v173, v173, v178
	ds_read_b128 v[178:181], v99 offset:56320
	s_waitcnt lgkmcnt(1)
	v_mul_f32_e32 v175, v69, v175
	v_fmac_f32_e32 v175, v68, v174
	v_mul_f32_e32 v174, v65, v177
	v_fmac_f32_e32 v174, v64, v176
	v_add_f32_e32 v174, v175, v174
	s_waitcnt lgkmcnt(0)
; #define LAS __attribute__((address_space(3)))
; template <int MODE, bool SB  > DI void norm_phase(const Params& P, const Frame& F, int L, const void* src_, const float* gain, bool combine) {
;     ...
;             for (int q = 0; q < 16; ++q) { float t = 0.f;
; #pragma unroll
;                 for (int j = 0; j < 8; ++j) { const f32x4 w = *(const LAS f32x4*)(F.lds + (size_t)(q * D + 256 * j + 4 * F.lane) * 4); t += (v[j][0] * w[0] + v[j][1] * w[1]) + (v[j][2] * w[2] + v[j][3] * w[3]); }
;                 s[q] = t; if ((q & 3) == 3) asm volatile("" ::: "memory"); }
	v_mul_f32_e32 v179, v71, v179
	v_add_f32_e32 v173, v173, v174
	v_fmac_f32_e32 v179, v70, v178
	v_mul_f32_e32 v178, v67, v181
	ds_read_b128 v[174:177], v99 offset:57344
	v_fmac_f32_e32 v178, v66, v180
	v_add_f32_e32 v178, v179, v178
	v_add_f32_e32 v173, v173, v178
	ds_read_b128 v[178:181], v99 offset:58368
	s_waitcnt lgkmcnt(1)
	v_mul_f32_e32 v175, v93, v175
	v_fmac_f32_e32 v175, v92, v174
	v_mul_f32_e32 v174, v91, v177
	v_fmac_f32_e32 v174, v90, v176
	v_add_f32_e32 v174, v175, v174
	s_waitcnt lgkmcnt(0)
	v_mul_f32_e32 v179, v95, v179
	v_add_f32_e32 v182, 0, v174
	v_fmac_f32_e32 v179, v94, v178
	v_mul_f32_e32 v178, v89, v181
	ds_read_b128 v[174:177], v99 offset:59392
	v_fmac_f32_e32 v178, v88, v180
	v_add_f32_e32 v178, v179, v178
	v_add_f32_e32 v182, v182, v178
	ds_read_b128 v[178:181], v99 offset:60416
	s_waitcnt lgkmcnt(1)
	v_mul_f32_e32 v175, v85, v175
	v_fmac_f32_e32 v175, v84, v174
	v_mul_f32_e32 v174, v83, v177
	v_fmac_f32_e32 v174, v82, v176
	v_add_f32_e32 v174, v175, v174
	s_waitcnt lgkmcnt(0)
	v_mul_f32_e32 v179, v87, v179
	v_add_f32_e32 v182, v182, v174
	v_fmac_f32_e32 v179, v86, v178
	v_mul_f32_e32 v178, v79, v181
	ds_read_b128 v[174:177], v99 offset:61440
	v_fmac_f32_e32 v178, v78, v180
	v_add_f32_e32 v178, v179, v178
	v_add_f32_e32 v182, v182, v178
	ds_read_b128 v[178:181], v99 offset:62464
	s_waitcnt lgkmcnt(1)
	v_mul_f32_e32 v175, v77, v175
	v_fmac_f32_e32 v175, v76, v174
	v_mul_f32_e32 v174, v75, v177
	v_fmac_f32_e32 v174, v74, v176
	v_add_f32_e32 v174, v175, v174
	s_waitcnt lgkmcnt(0)
	v_mul_f32_e32 v179, v81, v179
	v_add_f32_e32 v182, v182, v174
	v_fmac_f32_e32 v179, v80, v178
	v_mul_f32_e32 v178, v73, v181
	ds_read_b128 v[174:177], v99 offset:63488
	v_fmac_f32_e32 v178, v72, v180
	v_add_f32_e32 v178, v179, v178
	v_add_f32_e32 v182, v182, v178
	ds_read_b128 v[178:181], v99 offset:64512
	s_waitcnt lgkmcnt(1)
	v_mul_f32_e32 v175, v69, v175
	v_fmac_f32_e32 v175, v68, v174
	v_mul_f32_e32 v174, v65, v177
	v_fmac_f32_e32 v174, v64, v176
	v_add_f32_e32 v174, v175, v174
	s_waitcnt lgkmcnt(0)
	v_mul_f32_e32 v175, v71, v179
	v_fmac_f32_e32 v175, v70, v178
	v_mul_f32_e32 v181, v67, v181
	ds_read_b128 v[176:179], v100
	v_fmac_f32_e32 v181, v66, v180
	v_add_f32_e32 v174, v182, v174
	v_add_f32_e32 v175, v175, v181
	ds_read_b128 v[180:183], v101
	v_add_f32_e32 v174, v174, v175
	s_waitcnt lgkmcnt(1)
	v_mul_f32_e32 v175, v93, v177
	v_fmac_f32_e32 v175, v92, v176
	v_mul_f32_e32 v176, v91, v179
	v_fmac_f32_e32 v176, v90, v178
	s_waitcnt lgkmcnt(0)
	v_mul_f32_e32 v181, v95, v181
	v_add_f32_e32 v175, v175, v176
	v_fmac_f32_e32 v181, v94, v180
	v_mul_f32_e32 v180, v89, v183
	ds_read_b128 v[176:179], v102
	v_fmac_f32_e32 v180, v88, v182
	v_add_f32_e32 v175, 0, v175
	v_add_f32_e32 v180, v181, v180
	v_add_f32_e32 v175, v175, v180
	ds_read_b128 v[180:183], v103
	s_waitcnt lgkmcnt(1)
	v_mul_f32_e32 v177, v85, v177
	v_fmac_f32_e32 v177, v84, v176
	v_mul_f32_e32 v176, v83, v179
	v_fmac_f32_e32 v176, v82, v178
	v_add_f32_e32 v176, v177, v176
	s_waitcnt lgkmcnt(0)
	v_mul_f32_e32 v181, v87, v181
	v_add_f32_e32 v175, v175, v176
	v_fmac_f32_e32 v181, v86, v180
	v_mul_f32_e32 v180, v79, v183
	ds_read_b128 v[176:179], v104
	v_fmac_f32_e32 v180, v78, v182
	v_add_f32_e32 v180, v181, v180
	v_add_f32_e32 v175, v175, v180
	ds_read_b128 v[180:183], v105
	s_waitcnt lgkmcnt(1)
	v_mul_f32_e32 v177, v77, v177
	v_fmac_f32_e32 v177, v76, v176
	v_mul_f32_e32 v176, v75, v179
	v_fmac_f32_e32 v176, v74, v178
	v_add_f32_e32 v176, v177, v176
	s_waitcnt lgkmcnt(0)
	v_mul_f32_e32 v181, v81, v181
	v_add_f32_e32 v175, v175, v176
	v_fmac_f32_e32 v181, v80, v180
	v_mul_f32_e32 v180, v73, v183
	ds_read_b128 v[176:179], v106
	v_fmac_f32_e32 v180, v72, v182
	v_add_f32_e32 v180, v181, v180
	v_add_f32_e32 v175, v175, v180
	ds_read_b128 v[180:183], v107
	s_waitcnt lgkmcnt(1)
	v_mul_f32_e32 v177, v69, v177
	v_fmac_f32_e32 v177, v68, v176
	v_mul_f32_e32 v176, v65, v179
	v_fmac_f32_e32 v176, v64, v178
	v_add_f32_e32 v176, v177, v176
	s_waitcnt lgkmcnt(0)
	v_mul_f32_e32 v181, v71, v181
	v_add_f32_e32 v175, v175, v176
	v_fmac_f32_e32 v181, v70, v180
	v_mul_f32_e32 v180, v67, v183
	ds_read_b128 v[176:179], v108
	v_fmac_f32_e32 v180, v66, v182
	v_add_f32_e32 v180, v181, v180
	v_add_f32_e32 v175, v175, v180
	ds_read_b128 v[180:183], v109
	s_waitcnt lgkmcnt(1)
	v_mul_f32_e32 v177, v93, v177
	v_fmac_f32_e32 v177, v92, v176
	v_mul_f32_e32 v176, v91, v179
	v_fmac_f32_e32 v176, v90, v178
	v_add_f32_e32 v176, v177, v176
	s_waitcnt lgkmcnt(0)
	v_mul_f32_e32 v181, v95, v181
	v_add_f32_e32 v184, 0, v176
	v_fmac_f32_e32 v181, v94, v180
	v_mul_f32_e32 v180, v89, v183
	ds_read_b128 v[176:179], v110
	v_fmac_f32_e32 v180, v88, v182
	v_add_f32_e32 v180, v181, v180
	v_add_f32_e32 v184, v184, v180
	ds_read_b128 v[180:183], v111
	s_waitcnt lgkmcnt(1)
	v_mul_f32_e32 v177, v85, v177
	v_fmac_f32_e32 v177, v84, v176
	v_mul_f32_e32 v176, v83, v179
	v_fmac_f32_e32 v176, v82, v178
	v_add_f32_e32 v176, v177, v176
	s_waitcnt lgkmcnt(0)
	v_mul_f32_e32 v181, v87, v181
	v_add_f32_e32 v184, v184, v176
	v_fmac_f32_e32 v181, v86, v180
	v_mul_f32_e32 v180, v79, v183
	ds_read_b128 v[176:179], v112
	v_fmac_f32_e32 v180, v78, v182
	v_add_f32_e32 v180, v181, v180
	v_add_f32_e32 v184, v184, v180
	ds_read_b128 v[180:183], v113
	s_waitcnt lgkmcnt(1)
	v_mul_f32_e32 v177, v77, v177
	v_fmac_f32_e32 v177, v76, v176
	v_mul_f32_e32 v176, v75, v179
	v_fmac_f32_e32 v176, v74, v178
	v_add_f32_e32 v176, v177, v176
	s_waitcnt lgkmcnt(0)
	v_mul_f32_e32 v181, v81, v181
	v_add_f32_e32 v184, v184, v176
	v_fmac_f32_e32 v181, v80, v180
	v_mul_f32_e32 v180, v73, v183
	ds_read_b128 v[176:179], v114
	v_fmac_f32_e32 v180, v72, v182
	v_add_f32_e32 v180, v181, v180
	v_add_f32_e32 v184, v184, v180
	ds_read_b128 v[180:183], v115
	s_waitcnt lgkmcnt(1)
; #define LAS __attribute__((address_space(3)))
; template <int MODE, bool SB  > DI void norm_phase(const Params& P, const Frame& F, int L, const void* src_, const float* gain, bool combine) {
;     ...
;             for (int q = 0; q < 16; ++q) { float t = 0.f;
; #pragma unroll
;                 for (int j = 0; j < 8; ++j) { const f32x4 w = *(const LAS f32x4*)(F.lds + (size_t)(q * D + 256 * j + 4 * F.lane) * 4); t += (v[j][0] * w[0] + v[j][1] * w[1]) + (v[j][2] * w[2] + v[j][3] * w[3]); }
;                 s[q] = t; if ((q & 3) == 3) asm volatile("" ::: "memory"); }
	v_mul_f32_e32 v177, v69, v177
	v_fmac_f32_e32 v177, v68, v176
	v_mul_f32_e32 v176, v65, v179
	v_fmac_f32_e32 v176, v64, v178
	v_add_f32_e32 v176, v177, v176
	s_waitcnt lgkmcnt(0)
	v_mul_f32_e32 v177, v71, v181
	v_mul_f32_e32 v183, v67, v183
	v_fmac_f32_e32 v177, v70, v180
	ds_read_b128 v[178:181], v116
	v_fmac_f32_e32 v183, v66, v182
	v_add_f32_e32 v176, v184, v176
	v_add_f32_e32 v177, v177, v183
	ds_read_b128 v[182:185], v117
	v_add_f32_e32 v176, v176, v177
	s_waitcnt lgkmcnt(1)
	v_mul_f32_e32 v177, v93, v179
	v_fmac_f32_e32 v177, v92, v178
	v_mul_f32_e32 v178, v91, v181
	s_waitcnt lgkmcnt(0)
	v_mul_f32_e32 v183, v95, v183
	v_fmac_f32_e32 v178, v90, v180
	v_fmac_f32_e32 v183, v94, v182
	v_mul_f32_e32 v182, v89, v185
	v_add_f32_e32 v177, v177, v178
	ds_read_b128 v[178:181], v118
	v_fmac_f32_e32 v182, v88, v184
	v_add_f32_e32 v177, 0, v177
	v_add_f32_e32 v182, v183, v182
	v_add_f32_e32 v177, v177, v182
	ds_read_b128 v[182:185], v119
	s_waitcnt lgkmcnt(1)
	v_mul_f32_e32 v179, v85, v179
	v_fmac_f32_e32 v179, v84, v178
	v_mul_f32_e32 v178, v83, v181
	v_fmac_f32_e32 v178, v82, v180
	s_waitcnt lgkmcnt(0)
	v_mul_f32_e32 v183, v87, v183
	v_add_f32_e32 v178, v179, v178
	v_fmac_f32_e32 v183, v86, v182
	v_mul_f32_e32 v182, v79, v185
	v_add_f32_e32 v177, v177, v178
	ds_read_b128 v[178:181], v120
	v_fmac_f32_e32 v182, v78, v184
	v_add_f32_e32 v182, v183, v182
	v_add_f32_e32 v177, v177, v182
	ds_read_b128 v[182:185], v121
	s_waitcnt lgkmcnt(1)
	v_mul_f32_e32 v179, v77, v179
	v_fmac_f32_e32 v179, v76, v178
	v_mul_f32_e32 v178, v75, v181
	v_fmac_f32_e32 v178, v74, v180
	s_waitcnt lgkmcnt(0)
	v_mul_f32_e32 v183, v81, v183
	v_add_f32_e32 v178, v179, v178
	v_fmac_f32_e32 v183, v80, v182
	v_mul_f32_e32 v182, v73, v185
	v_add_f32_e32 v177, v177, v178
	ds_read_b128 v[178:181], v122
	v_fmac_f32_e32 v182, v72, v184
	v_add_f32_e32 v182, v183, v182
	v_add_f32_e32 v177, v177, v182
	ds_read_b128 v[182:185], v123
	s_waitcnt lgkmcnt(1)
	v_mul_f32_e32 v179, v69, v179
	v_fmac_f32_e32 v179, v68, v178
	v_mul_f32_e32 v178, v65, v181
	v_fmac_f32_e32 v178, v64, v180
	s_waitcnt lgkmcnt(0)
	v_mul_f32_e32 v183, v71, v183
	v_add_f32_e32 v178, v179, v178
	v_fmac_f32_e32 v183, v70, v182
	v_mul_f32_e32 v182, v67, v185
	v_add_f32_e32 v177, v177, v178
	ds_read_b128 v[178:181], v124
	v_fmac_f32_e32 v182, v66, v184
	v_add_f32_e32 v182, v183, v182
	v_add_f32_e32 v177, v177, v182
	ds_read_b128 v[182:185], v125
	s_waitcnt lgkmcnt(1)
	v_mul_f32_e32 v179, v93, v179
	v_fmac_f32_e32 v179, v92, v178
	v_mul_f32_e32 v178, v91, v181
	v_fmac_f32_e32 v178, v90, v180
	s_waitcnt lgkmcnt(0)
	v_mul_f32_e32 v183, v95, v183
	v_add_f32_e32 v178, v179, v178
	v_fmac_f32_e32 v183, v94, v182
	v_mul_f32_e32 v182, v89, v185
	v_add_f32_e32 v186, 0, v178
	ds_read_b128 v[178:181], v126
	v_fmac_f32_e32 v182, v88, v184
	v_add_f32_e32 v182, v183, v182
	v_add_f32_e32 v186, v186, v182
	ds_read_b128 v[182:185], v127
	s_waitcnt lgkmcnt(1)
	v_mul_f32_e32 v179, v85, v179
	v_fmac_f32_e32 v179, v84, v178
	v_mul_f32_e32 v178, v83, v181
	v_fmac_f32_e32 v178, v82, v180
	s_waitcnt lgkmcnt(0)
	v_mul_f32_e32 v183, v87, v183
	v_add_f32_e32 v178, v179, v178
	v_fmac_f32_e32 v183, v86, v182
	v_mul_f32_e32 v182, v79, v185
	v_add_f32_e32 v186, v186, v178
	ds_read_b128 v[178:181], v128
	v_fmac_f32_e32 v182, v78, v184
	v_add_f32_e32 v182, v183, v182
	v_add_f32_e32 v186, v186, v182
	ds_read_b128 v[182:185], v129
	s_waitcnt lgkmcnt(1)
	v_mul_f32_e32 v179, v77, v179
	v_fmac_f32_e32 v179, v76, v178
	v_mul_f32_e32 v178, v75, v181
	v_fmac_f32_e32 v178, v74, v180
	s_waitcnt lgkmcnt(0)
	v_mul_f32_e32 v183, v81, v183
	v_add_f32_e32 v178, v179, v178
	v_fmac_f32_e32 v183, v80, v182
	v_mul_f32_e32 v182, v73, v185
	v_add_f32_e32 v186, v186, v178
	ds_read_b128 v[178:181], v130
	v_fmac_f32_e32 v182, v72, v184
	v_add_f32_e32 v182, v183, v182
	v_add_f32_e32 v186, v186, v182
	ds_read_b128 v[182:185], v131
	s_waitcnt lgkmcnt(1)
	v_mul_f32_e32 v179, v69, v179
	v_fmac_f32_e32 v179, v68, v178
	v_mul_f32_e32 v178, v65, v181
	v_fmac_f32_e32 v178, v64, v180
	s_waitcnt lgkmcnt(0)
	v_mul_f32_e32 v183, v71, v183
	v_add_f32_e32 v178, v179, v178
	v_fmac_f32_e32 v183, v70, v182
	v_mul_f32_e32 v182, v67, v185
	v_add_f32_e32 v186, v186, v178
	ds_read_b128 v[178:181], v132
	v_fmac_f32_e32 v182, v66, v184
	v_add_f32_e32 v182, v183, v182
	v_add_f32_e32 v186, v186, v182
	ds_read_b128 v[182:185], v133
	s_waitcnt lgkmcnt(1)
	v_mul_f32_e32 v179, v93, v179
	v_fmac_f32_e32 v179, v92, v178
	v_mul_f32_e32 v178, v91, v181
	v_fmac_f32_e32 v178, v90, v180
	s_waitcnt lgkmcnt(0)
	v_mul_f32_e32 v183, v95, v183
	v_add_f32_e32 v178, v179, v178
	v_fmac_f32_e32 v183, v94, v182
	v_mul_f32_e32 v182, v89, v185
	v_add_f32_e32 v187, 0, v178
	ds_read_b128 v[178:181], v134
	v_fmac_f32_e32 v182, v88, v184
	v_add_f32_e32 v182, v183, v182
	v_add_f32_e32 v187, v187, v182
	ds_read_b128 v[182:185], v135
	s_waitcnt lgkmcnt(1)
	v_mul_f32_e32 v179, v85, v179
	v_fmac_f32_e32 v179, v84, v178
	v_mul_f32_e32 v178, v83, v181
	v_fmac_f32_e32 v178, v82, v180
	s_waitcnt lgkmcnt(0)
	v_mul_f32_e32 v183, v87, v183
	v_add_f32_e32 v178, v179, v178
	v_fmac_f32_e32 v183, v86, v182
	v_mul_f32_e32 v182, v79, v185
	v_add_f32_e32 v187, v187, v178
	ds_read_b128 v[178:181], v136
	v_fmac_f32_e32 v182, v78, v184
	v_add_f32_e32 v182, v183, v182
	v_add_f32_e32 v187, v187, v182
	ds_read_b128 v[182:185], v137
	s_waitcnt lgkmcnt(1)
	v_mul_f32_e32 v179, v77, v179
	v_fmac_f32_e32 v179, v76, v178
	v_mul_f32_e32 v178, v75, v181
	v_fmac_f32_e32 v178, v74, v180
	s_waitcnt lgkmcnt(0)
; #define LAS __attribute__((address_space(3)))
; template <int MODE, bool SB  > DI void norm_phase(const Params& P, const Frame& F, int L, const void* src_, const float* gain, bool combine) {
;     ...
;             for (int q = 0; q < 16; ++q) { float t = 0.f;
; #pragma unroll
;                 for (int j = 0; j < 8; ++j) { const f32x4 w = *(const LAS f32x4*)(F.lds + (size_t)(q * D + 256 * j + 4 * F.lane) * 4); t += (v[j][0] * w[0] + v[j][1] * w[1]) + (v[j][2] * w[2] + v[j][3] * w[3]); }
;                 s[q] = t; if ((q & 3) == 3) asm volatile("" ::: "memory"); }
	v_mul_f32_e32 v183, v81, v183
	v_add_f32_e32 v178, v179, v178
	v_fmac_f32_e32 v183, v80, v182
	v_mul_f32_e32 v182, v73, v185
	v_add_f32_e32 v187, v187, v178
	ds_read_b128 v[178:181], v138
	v_fmac_f32_e32 v182, v72, v184
	v_add_f32_e32 v182, v183, v182
	v_add_f32_e32 v187, v187, v182
	ds_read_b128 v[182:185], v139
	s_waitcnt lgkmcnt(1)
	v_mul_f32_e32 v179, v69, v179
	v_fmac_f32_e32 v179, v68, v178
	v_mul_f32_e32 v178, v65, v181
	v_fmac_f32_e32 v178, v64, v180
	s_waitcnt lgkmcnt(0)
	v_mul_f32_e32 v183, v71, v183
	v_add_f32_e32 v178, v179, v178
	v_fmac_f32_e32 v183, v70, v182
	v_mul_f32_e32 v182, v67, v185
	v_add_f32_e32 v187, v187, v178
	ds_read_b128 v[178:181], v140
	v_fmac_f32_e32 v182, v66, v184
	v_add_f32_e32 v182, v183, v182
	v_add_f32_e32 v187, v187, v182
	ds_read_b128 v[182:185], v141
	s_waitcnt lgkmcnt(1)
	v_mul_f32_e32 v179, v93, v179
	v_fmac_f32_e32 v179, v92, v178
	v_mul_f32_e32 v178, v91, v181
	v_fmac_f32_e32 v178, v90, v180
	s_waitcnt lgkmcnt(0)
	v_mul_f32_e32 v183, v95, v183
	v_add_f32_e32 v178, v179, v178
	v_fmac_f32_e32 v183, v94, v182
	v_mul_f32_e32 v182, v89, v185
	v_add_f32_e32 v188, 0, v178
	ds_read_b128 v[178:181], v142
	v_fmac_f32_e32 v182, v88, v184
	v_add_f32_e32 v182, v183, v182
	v_add_f32_e32 v188, v188, v182
	ds_read_b128 v[182:185], v143
	s_waitcnt lgkmcnt(1)
	v_mul_f32_e32 v179, v85, v179
	v_fmac_f32_e32 v179, v84, v178
	v_mul_f32_e32 v178, v83, v181
	v_fmac_f32_e32 v178, v82, v180
	s_waitcnt lgkmcnt(0)
	v_mul_f32_e32 v183, v87, v183
	v_add_f32_e32 v178, v179, v178
	v_fmac_f32_e32 v183, v86, v182
	v_mul_f32_e32 v182, v79, v185
	v_add_f32_e32 v188, v188, v178
	ds_read_b128 v[178:181], v144
	v_fmac_f32_e32 v182, v78, v184
	v_add_f32_e32 v182, v183, v182
	v_add_f32_e32 v188, v188, v182
	ds_read_b128 v[182:185], v145
	s_waitcnt lgkmcnt(1)
	v_mul_f32_e32 v179, v77, v179
	v_fmac_f32_e32 v179, v76, v178
	v_mul_f32_e32 v178, v75, v181
	v_fmac_f32_e32 v178, v74, v180
	s_waitcnt lgkmcnt(0)
	v_mul_f32_e32 v183, v81, v183
	v_add_f32_e32 v178, v179, v178
	v_fmac_f32_e32 v183, v80, v182
	v_mul_f32_e32 v182, v73, v185
	v_add_f32_e32 v188, v188, v178
	ds_read_b128 v[178:181], v146
	v_fmac_f32_e32 v182, v72, v184
	v_add_f32_e32 v182, v183, v182
	v_add_f32_e32 v188, v188, v182
	ds_read_b128 v[182:185], v147
	s_waitcnt lgkmcnt(1)
	v_mul_f32_e32 v179, v69, v179
	v_fmac_f32_e32 v179, v68, v178
	v_mul_f32_e32 v178, v65, v181
	v_fmac_f32_e32 v178, v64, v180
	s_waitcnt lgkmcnt(0)
	v_mul_f32_e32 v183, v71, v183
	v_add_f32_e32 v178, v179, v178
	v_fmac_f32_e32 v183, v70, v182
	v_mul_f32_e32 v182, v67, v185
	v_add_f32_e32 v188, v188, v178
	ds_read_b128 v[178:181], v148
	v_fmac_f32_e32 v182, v66, v184
	v_add_f32_e32 v182, v183, v182
	v_add_f32_e32 v188, v188, v182
	ds_read_b128 v[182:185], v149
	s_waitcnt lgkmcnt(1)
	v_mul_f32_e32 v179, v93, v179
	v_fmac_f32_e32 v179, v92, v178
	v_mul_f32_e32 v178, v91, v181
	v_fmac_f32_e32 v178, v90, v180
	s_waitcnt lgkmcnt(0)
	v_mul_f32_e32 v183, v95, v183
	v_add_f32_e32 v178, v179, v178
	v_fmac_f32_e32 v183, v94, v182
	v_mul_f32_e32 v182, v89, v185
	v_add_f32_e32 v189, 0, v178
	ds_read_b128 v[178:181], v150
	v_fmac_f32_e32 v182, v88, v184
	v_add_f32_e32 v182, v183, v182
	v_add_f32_e32 v189, v189, v182
	ds_read_b128 v[182:185], v151
	s_waitcnt lgkmcnt(1)
	v_mul_f32_e32 v179, v85, v179
	v_fmac_f32_e32 v179, v84, v178
	v_mul_f32_e32 v178, v83, v181
	v_fmac_f32_e32 v178, v82, v180
	s_waitcnt lgkmcnt(0)
	v_mul_f32_e32 v183, v87, v183
	v_add_f32_e32 v178, v179, v178
	v_fmac_f32_e32 v183, v86, v182
	v_mul_f32_e32 v182, v79, v185
	v_add_f32_e32 v189, v189, v178
	ds_read_b128 v[178:181], v152
	v_fmac_f32_e32 v182, v78, v184
	v_add_f32_e32 v182, v183, v182
	v_add_f32_e32 v189, v189, v182
	ds_read_b128 v[182:185], v153
	s_waitcnt lgkmcnt(1)
	v_mul_f32_e32 v179, v77, v179
	v_fmac_f32_e32 v179, v76, v178
	v_mul_f32_e32 v178, v75, v181
	v_fmac_f32_e32 v178, v74, v180
	s_waitcnt lgkmcnt(0)
	v_mul_f32_e32 v183, v81, v183
	v_add_f32_e32 v178, v179, v178
	v_fmac_f32_e32 v183, v80, v182
	v_mul_f32_e32 v182, v73, v185
	v_add_f32_e32 v189, v189, v178
	ds_read_b128 v[178:181], v154
	v_fmac_f32_e32 v182, v72, v184
	v_add_f32_e32 v182, v183, v182
	v_add_f32_e32 v189, v189, v182
	ds_read_b128 v[182:185], v155
	s_waitcnt lgkmcnt(1)
	v_mul_f32_e32 v179, v69, v179
	v_fmac_f32_e32 v179, v68, v178
	v_mul_f32_e32 v178, v65, v181
	v_fmac_f32_e32 v178, v64, v180
	s_waitcnt lgkmcnt(0)
	v_mul_f32_e32 v183, v71, v183
	v_add_f32_e32 v178, v179, v178
	v_fmac_f32_e32 v183, v70, v182
	v_mul_f32_e32 v182, v67, v185
	v_add_f32_e32 v189, v189, v178
	ds_read_b128 v[178:181], v156
	v_fmac_f32_e32 v182, v66, v184
	v_add_f32_e32 v182, v183, v182
	v_add_f32_e32 v189, v189, v182
	ds_read_b128 v[182:185], v157
	s_waitcnt lgkmcnt(1)
	v_mul_f32_e32 v93, v93, v179
	v_mul_f32_e32 v91, v91, v181
	v_fmac_f32_e32 v93, v92, v178
	v_fmac_f32_e32 v91, v90, v180
	v_add_f32_e32 v90, v93, v91
	s_waitcnt lgkmcnt(0)
; #define LAS __attribute__((address_space(3)))
; DI float sigmoidf_(float x) { return __builtin_amdgcn_rcpf(1.0f + __expf(-x)); }
; template <int MODE, bool SB  > DI void norm_phase(const Params& P, const Frame& F, int L, const void* src_, const float* gain, bool combine) {
;     ...
;             for (int q = 0; q < 16; ++q) { float t = 0.f;
; #pragma unroll
;                 for (int j = 0; j < 8; ++j) { const f32x4 w = *(const LAS f32x4*)(F.lds + (size_t)(q * D + 256 * j + 4 * F.lane) * 4); t += (v[j][0] * w[0] + v[j][1] * w[1]) + (v[j][2] * w[2] + v[j][3] * w[3]); }
;                 s[q] = t; if ((q & 3) == 3) asm volatile("" ::: "memory"); }
; #pragma unroll
;             for (int i = 0; i < 8; ++i) { const bool hi = (F.lane & 32) != 0; const float send = hi ? s[i] : s[i + 8], keep = hi ? s[i + 8] : s[i]; s[i] = keep + shx<32>(send); }
; #pragma unroll
;             for (int i = 0; i < 4; ++i) { const bool hi = (F.lane & 16) != 0; const float send = hi ? s[i] : s[i + 4], keep = hi ? s[i + 4] : s[i]; s[i] = keep + shx<16>(send); }
; #pragma unroll
;             for (int i = 0; i < 2; ++i) { const bool hi = (F.lane & 8) != 0; const float send = hi ? s[i] : s[i + 2], keep = hi ? s[i + 2] : s[i]; s[i] = keep + shx<8>(send); }
;             { const bool hi = (F.lane & 4) != 0; const float send = hi ? s[0] : s[1], keep = hi ? s[1] : s[0]; s[0] = keep + shx<4>(send); }
;             float mine = s[0]; mine += shx<2>(mine); mine += shx<1>(mine);
;             if ((F.lane & 3) == 0) { const int gi = ((F.lane >> 5) & 1) * 8 + ((F.lane >> 4) & 1) * 4 + ((F.lane >> 3) & 1) * 2 + ((F.lane >> 2) & 1), h = gi & 3; float r;
;                 if (gi < 4) r = sigmoidf_(mine);
	v_mul_f32_e32 v95, v95, v183
	v_mul_f32_e32 v89, v89, v185
	v_add_f32_e32 v178, 0, v90
	v_fmac_f32_e32 v95, v94, v182
	ds_read_b128 v[90:93], v158
	v_fmac_f32_e32 v89, v88, v184
	v_add_f32_e32 v88, v95, v89
	v_add_f32_e32 v88, v178, v88
	ds_read_b128 v[178:181], v159
	s_waitcnt lgkmcnt(1)
	v_mul_f32_e32 v85, v85, v91
	v_mul_f32_e32 v83, v83, v93
	v_fmac_f32_e32 v85, v84, v90
	v_fmac_f32_e32 v83, v82, v92
	v_add_f32_e32 v82, v85, v83
	s_waitcnt lgkmcnt(0)
	v_mul_f32_e32 v87, v87, v179
	v_mul_f32_e32 v79, v79, v181
	v_add_f32_e32 v88, v88, v82
	v_fmac_f32_e32 v87, v86, v178
	ds_read_b128 v[82:85], v160
	v_fmac_f32_e32 v79, v78, v180
	v_add_f32_e32 v78, v87, v79
	v_add_f32_e32 v78, v88, v78
	ds_read_b128 v[86:89], v161
	s_waitcnt lgkmcnt(1)
	v_mul_f32_e32 v77, v77, v83
	v_mul_f32_e32 v75, v75, v85
	v_fmac_f32_e32 v77, v76, v82
	v_fmac_f32_e32 v75, v74, v84
	v_add_f32_e32 v74, v77, v75
	s_waitcnt lgkmcnt(0)
	v_mul_f32_e32 v79, v81, v87
	v_mul_f32_e32 v73, v73, v89
	v_add_f32_e32 v78, v78, v74
	v_fmac_f32_e32 v79, v80, v86
	ds_read_b128 v[74:77], v162
	v_fmac_f32_e32 v73, v72, v88
	v_add_f32_e32 v72, v79, v73
	v_add_f32_e32 v72, v78, v72
	ds_read_b128 v[78:81], v163
	s_waitcnt lgkmcnt(1)
	v_mul_f32_e32 v69, v69, v75
	v_mul_f32_e32 v65, v65, v77
	v_fmac_f32_e32 v69, v68, v74
	v_fmac_f32_e32 v65, v64, v76
	v_add_f32_e32 v64, v69, v65
	s_waitcnt lgkmcnt(0)
	v_mul_f32_e32 v65, v71, v79
	v_mul_f32_e32 v67, v67, v81
	v_fmac_f32_e32 v65, v70, v78
	v_fmac_f32_e32 v67, v66, v80
	v_add_f32_e32 v64, v72, v64
	v_add_f32_e32 v65, v65, v67
	v_add_f32_e32 v64, v64, v65
	v_cndmask_b32_e64 v65, v47, v175, s[4:5]
	ds_bpermute_b32 v65, v98, v65
	v_cndmask_b32_e64 v66, v96, v176, s[4:5]
	ds_bpermute_b32 v66, v98, v66
	v_cndmask_b32_e64 v67, v97, v177, s[4:5]
	ds_bpermute_b32 v67, v98, v67
	v_cndmask_b32_e64 v47, v175, v47, s[4:5]
	s_waitcnt lgkmcnt(2)
	v_add_f32_e32 v47, v47, v65
	v_cndmask_b32_e64 v65, v176, v96, s[4:5]
	s_waitcnt lgkmcnt(1)
	v_add_f32_e32 v65, v65, v66
	v_cndmask_b32_e64 v66, v177, v97, s[4:5]
	s_waitcnt lgkmcnt(0)
	v_add_f32_e32 v66, v66, v67
	v_cndmask_b32_e64 v67, v170, v186, s[4:5]
	ds_bpermute_b32 v67, v98, v67
	v_cndmask_b32_e64 v69, v171, v187, s[4:5]
	ds_bpermute_b32 v69, v98, v69
	v_cndmask_b32_e64 v70, v172, v188, s[4:5]
	ds_bpermute_b32 v70, v98, v70
	v_cndmask_b32_e64 v68, v186, v170, s[4:5]
	s_waitcnt lgkmcnt(2)
	v_add_f32_e32 v67, v68, v67
	v_cndmask_b32_e64 v68, v187, v171, s[4:5]
	s_waitcnt lgkmcnt(1)
	v_add_f32_e32 v68, v68, v69
	v_cndmask_b32_e64 v69, v188, v172, s[4:5]
	s_waitcnt lgkmcnt(0)
	v_add_f32_e32 v69, v69, v70
	v_cndmask_b32_e64 v70, v173, v189, s[4:5]
	v_cndmask_b32_e64 v72, v174, v64, s[4:5]
	ds_bpermute_b32 v70, v98, v70
	ds_bpermute_b32 v72, v98, v72
	v_cndmask_b32_e64 v71, v189, v173, s[4:5]
	v_cndmask_b32_e64 v64, v64, v174, s[4:5]
	v_cndmask_b32_e64 v73, v47, v68, s[8:9]
	s_waitcnt lgkmcnt(1)
	v_add_f32_e32 v70, v71, v70
	s_waitcnt lgkmcnt(0)
	v_add_f32_e32 v64, v64, v72
	v_cndmask_b32_e64 v47, v68, v47, s[8:9]
	v_cndmask_b32_e64 v68, v65, v69, s[8:9]
	v_cndmask_b32_e64 v65, v69, v65, s[8:9]
	v_cndmask_b32_e64 v69, v66, v70, s[8:9]
	v_cndmask_b32_e64 v71, v67, v64, s[8:9]
	ds_swizzle_b32 v73, v73 offset:swizzle(SWAP,16)
	ds_swizzle_b32 v68, v68 offset:swizzle(SWAP,16)
	ds_swizzle_b32 v69, v69 offset:swizzle(SWAP,16)
	ds_swizzle_b32 v71, v71 offset:swizzle(SWAP,16)
	v_cndmask_b32_e64 v66, v70, v66, s[8:9]
	v_cndmask_b32_e64 v64, v64, v67, s[8:9]
	s_waitcnt lgkmcnt(3)
	v_add_f32_e32 v47, v47, v73
	s_waitcnt lgkmcnt(2)
	v_add_f32_e32 v65, v65, v68
	s_waitcnt lgkmcnt(1)
	v_add_f32_e32 v66, v66, v69
	s_waitcnt lgkmcnt(0)
	v_add_f32_e32 v64, v64, v71
	v_cndmask_b32_e64 v67, v47, v66, s[10:11]
	v_cndmask_b32_e64 v68, v65, v64, s[10:11]
	ds_swizzle_b32 v67, v67 offset:swizzle(SWAP,8)
	ds_swizzle_b32 v68, v68 offset:swizzle(SWAP,8)
	v_cndmask_b32_e64 v47, v66, v47, s[10:11]
	v_cndmask_b32_e64 v64, v64, v65, s[10:11]
	s_waitcnt lgkmcnt(1)
	v_add_f32_e32 v47, v47, v67
	s_waitcnt lgkmcnt(0)
	v_add_f32_e32 v64, v64, v68
	v_cndmask_b32_e64 v65, v47, v64, s[12:13]
	ds_swizzle_b32 v65, v65 offset:swizzle(SWAP,4)
	v_cndmask_b32_e64 v47, v64, v47, s[12:13]
	s_waitcnt lgkmcnt(0)
	v_add_f32_e32 v47, v47, v65
	s_nop 1
	v_add_f32_dpp v47, v47, v47 quad_perm:[2,3,0,1] row_mask:0xf bank_mask:0xf bound_ctrl:1
	s_nop 1
	v_mov_b32_dpp v64, v47 quad_perm:[1,0,3,2] row_mask:0xf bank_mask:0xf bound_ctrl:1
	s_and_saveexec_b64 s[20:21], s[14:15]
	s_cbranch_execz .LBB0_1647
	v_add_f32_e32 v47, v47, v64
	s_and_saveexec_b64 s[24:25], s[16:17]
	s_xor_b64 s[24:25], exec, s[24:25]
	s_cbranch_execz .LBB0_1659
	s_and_saveexec_b64 s[26:27], s[6:7]
	s_xor_b64 s[26:27], exec, s[26:27]
	s_cbranch_execz .LBB0_1656
	s_and_saveexec_b64 s[28:29], s[18:19]
	s_xor_b64 s[28:29], exec, s[28:29]
	s_cbranch_execz .LBB0_1653
	v_mov_b32_e32 v64, v190
	v_add_f32_e32 v64, v47, v64

.LBB0_1704:
	global_load_dword v1, v0, s[10:11] sc1
	s_waitcnt vmcnt(0)
	v_cmp_eq_u32_e32 vcc, 0, v1
	s_cbranch_vccnz .LBB0_1706
	s_mov_b64 s[18:19], -1
	s_mov_b64 s[22:23], -1
	s_branch .LBB0_1700
	s_nop 0
	s_nop 0
	s_nop 0
	s_nop 0
	s_nop 0
	s_nop 0
	s_nop 0
	s_nop 0
	s_nop 0
	s_nop 0
	s_nop 0
	s_nop 0
	s_nop 0
	s_nop 0
	s_nop 0
	s_nop 0
	s_nop 0
	s_nop 0
	s_nop 0
	s_nop 0
	s_nop 0
	s_nop 0
	s_nop 0
	s_nop 0
	s_nop 0
	s_nop 0
	s_nop 0
	s_nop 0
	s_nop 0
	s_nop 0
	s_nop 0
	s_nop 0
	s_nop 0
	s_nop 0
	s_nop 0
	s_nop 0
	s_nop 0
	s_nop 0
	s_nop 0
	s_nop 0
	s_nop 0
	s_nop 0
	s_nop 0
	s_nop 0
	s_nop 0
	s_nop 0
	s_nop 0
	s_nop 0
	s_nop 0
	s_nop 0
	s_nop 0
	s_nop 0
	s_nop 0
	s_nop 0
	s_nop 0
	s_nop 0
	s_nop 0
	s_nop 0
	s_nop 0
	s_nop 0
	s_nop 0
	s_nop 0

; DI void attn_block(const Params& P, const Frame& F, int L, int b, int h, int qb, float lam, float oml) {
;     ...
;     const float* nw = P.in[I_DIFF_NORM] + L * 128;
;     f32x4 nwv[8];
; #pragma unroll
;     for (int d = 0; d < 8; ++d) nwv[d] = *(const f32x4*)(nw + 16 * d + 4 * rq);
;     float inv[2];
; #pragma unroll
;     for (int j = 0; j < 2; ++j) { float l = lrun[j]; l += shx<16>(l); l += shx<32>(l); inv[j] = __builtin_amdgcn_rcpf(l); }
;     const float inv1l = lam * inv[1];
;     float ss = 0.f;
; #pragma unroll
;     for (int d = 0; d < 8; ++d)
; #pragma unroll
;         for (int e = 0; e < 4; ++e) { const float o = O[0][d][e] * inv[0] - O[1][d][e] * inv1l; O[0][d][e] = o; ss += o * o; }
;     ss += shx<16>(ss); ss += shx<32>(ss);
;     const float r = oml * __builtin_amdgcn_rsqf(ss * (1.0f / 128.0f) + EPS);
.LBB0_2611:
	global_load_dwordx4 v[0:3], v[110:111], off offset:512
	global_load_dwordx4 v[4:7], v[110:111], off offset:576
	ds_swizzle_b32 v8, v202 offset:swizzle(SWAP,16)
	ds_swizzle_b32 v9, v203 offset:swizzle(SWAP,16)
	s_lshl_b32 s40, s68, 1
	v_readlane_b32 s68, v254, 37
	s_mov_b64 s[6:7], 0
	s_waitcnt vmcnt(2) lgkmcnt(1)
	s_mov_b64 s[6:7], exec
	s_and_b64 exec, exec, s[4:5]
	v_mov_b32_e32 v252, 1
	global_atomic_add v252, v97, v252, s[0:1] sc0
	s_mov_b64 exec, s[6:7]
	s_mov_b64 s[6:7], 0
	v_add_f32_e32 v24, v202, v8
	s_waitcnt lgkmcnt(0)
	v_add_f32_e32 v25, v203, v9
	ds_bpermute_b32 v26, v190, v24
	ds_bpermute_b32 v27, v190, v25
	global_load_dwordx4 v[8:11], v[110:111], off offset:640
	global_load_dwordx4 v[12:15], v[110:111], off offset:704
	global_load_dwordx4 v[16:19], v[110:111], off offset:768
	global_load_dwordx4 v[20:23], v[110:111], off offset:832
	v_readlane_b32 s70, v254, 39
	v_readlane_b32 s71, v254, 40
	s_waitcnt lgkmcnt(1)
	v_add_f32_e32 v24, v24, v26
	s_waitcnt lgkmcnt(0)
	v_add_f32_e32 v25, v25, v27
	v_rcp_f32_e32 v128, v25
	v_rcp_f32_e32 v96, v24
	global_load_dwordx4 v[24:27], v[110:111], off offset:896
	global_load_dwordx4 v[28:31], v[110:111], off offset:960
	v_readlane_b32 s69, v254, 38
	v_mul_f32_e32 v128, v197, v128
	v_pk_mul_f32 v[36:37], v[36:37], v[128:129] op_sel_hi:[1,0]
	v_pk_mul_f32 v[38:39], v[38:39], v[128:129] op_sel_hi:[1,0]
	v_pk_fma_f32 v[32:33], v[32:33], v[96:97], v[36:37] op_sel_hi:[1,0,1] neg_lo:[0,0,1] neg_hi:[0,0,1]
	v_pk_fma_f32 v[34:35], v[34:35], v[96:97], v[38:39] op_sel_hi:[1,0,1] neg_lo:[0,0,1] neg_hi:[0,0,1]
	v_pk_mul_f32 v[36:37], v[32:33], v[32:33]
	v_pk_mul_f32 v[44:45], v[44:45], v[128:129] op_sel_hi:[1,0]
	v_pk_mul_f32 v[38:39], v[34:35], v[34:35]
	v_add_f32_e32 v36, v36, v37
	v_pk_fma_f32 v[40:41], v[40:41], v[96:97], v[44:45] op_sel_hi:[1,0,1] neg_lo:[0,0,1] neg_hi:[0,0,1]
	v_add_f32_e32 v36, v38, v36
	v_pk_mul_f32 v[46:47], v[46:47], v[128:129] op_sel_hi:[1,0]
	v_pk_mul_f32 v[44:45], v[40:41], v[40:41]
	v_add_f32_e32 v36, v39, v36
	v_pk_fma_f32 v[42:43], v[42:43], v[96:97], v[46:47] op_sel_hi:[1,0,1] neg_lo:[0,0,1] neg_hi:[0,0,1]
	v_add_f32_e32 v36, v44, v36
	v_pk_mul_f32 v[56:57], v[56:57], v[128:129] op_sel_hi:[1,0]
	v_pk_mul_f32 v[46:47], v[42:43], v[42:43]
	v_add_f32_e32 v36, v45, v36
	v_pk_fma_f32 v[48:49], v[48:49], v[96:97], v[56:57] op_sel_hi:[1,0,1] neg_lo:[0,0,1] neg_hi:[0,0,1]
	v_add_f32_e32 v36, v46, v36
	v_pk_mul_f32 v[58:59], v[58:59], v[128:129] op_sel_hi:[1,0]
	v_pk_mul_f32 v[56:57], v[48:49], v[48:49]
	v_add_f32_e32 v36, v47, v36
	v_pk_fma_f32 v[50:51], v[50:51], v[96:97], v[58:59] op_sel_hi:[1,0,1] neg_lo:[0,0,1] neg_hi:[0,0,1]
	v_add_f32_e32 v36, v56, v36
	v_pk_mul_f32 v[64:65], v[64:65], v[128:129] op_sel_hi:[1,0]
	v_pk_mul_f32 v[58:59], v[50:51], v[50:51]
	v_add_f32_e32 v36, v57, v36
	v_pk_fma_f32 v[52:53], v[52:53], v[96:97], v[64:65] op_sel_hi:[1,0,1] neg_lo:[0,0,1] neg_hi:[0,0,1]
	v_add_f32_e32 v36, v58, v36
	v_pk_mul_f32 v[66:67], v[66:67], v[128:129] op_sel_hi:[1,0]
	v_pk_mul_f32 v[64:65], v[52:53], v[52:53]
	v_add_f32_e32 v36, v59, v36
	v_pk_fma_f32 v[54:55], v[54:55], v[96:97], v[66:67] op_sel_hi:[1,0,1] neg_lo:[0,0,1] neg_hi:[0,0,1]
	v_add_f32_e32 v36, v64, v36
	v_pk_mul_f32 v[68:69], v[68:69], v[128:129] op_sel_hi:[1,0]
	v_pk_mul_f32 v[66:67], v[54:55], v[54:55]
	v_add_f32_e32 v36, v65, v36
	v_pk_fma_f32 v[60:61], v[60:61], v[96:97], v[68:69] op_sel_hi:[1,0,1] neg_lo:[0,0,1] neg_hi:[0,0,1]
	v_add_f32_e32 v36, v66, v36
	v_pk_mul_f32 v[70:71], v[70:71], v[128:129] op_sel_hi:[1,0]
	v_pk_mul_f32 v[68:69], v[60:61], v[60:61]
	v_add_f32_e32 v36, v67, v36
	v_pk_fma_f32 v[62:63], v[62:63], v[96:97], v[70:71] op_sel_hi:[1,0,1] neg_lo:[0,0,1] neg_hi:[0,0,1]
	v_add_f32_e32 v36, v68, v36
	v_pk_mul_f32 v[76:77], v[76:77], v[128:129] op_sel_hi:[1,0]
	v_pk_mul_f32 v[70:71], v[62:63], v[62:63]
	v_add_f32_e32 v36, v69, v36
	v_pk_fma_f32 v[72:73], v[72:73], v[96:97], v[76:77] op_sel_hi:[1,0,1] neg_lo:[0,0,1] neg_hi:[0,0,1]
	v_add_f32_e32 v36, v70, v36
	v_pk_mul_f32 v[78:79], v[78:79], v[128:129] op_sel_hi:[1,0]
	v_pk_mul_f32 v[76:77], v[72:73], v[72:73]
	v_add_f32_e32 v36, v71, v36
	v_pk_fma_f32 v[74:75], v[74:75], v[96:97], v[78:79] op_sel_hi:[1,0,1] neg_lo:[0,0,1] neg_hi:[0,0,1]
	v_add_f32_e32 v36, v76, v36
	v_pk_mul_f32 v[84:85], v[84:85], v[128:129] op_sel_hi:[1,0]
	v_pk_mul_f32 v[78:79], v[74:75], v[74:75]
	v_add_f32_e32 v36, v77, v36
	v_pk_fma_f32 v[80:81], v[80:81], v[96:97], v[84:85] op_sel_hi:[1,0,1] neg_lo:[0,0,1] neg_hi:[0,0,1]
	v_add_f32_e32 v36, v78, v36
	v_pk_mul_f32 v[86:87], v[86:87], v[128:129] op_sel_hi:[1,0]
	v_pk_mul_f32 v[84:85], v[80:81], v[80:81]
	v_add_f32_e32 v36, v79, v36
	v_pk_fma_f32 v[82:83], v[82:83], v[96:97], v[86:87] op_sel_hi:[1,0,1] neg_lo:[0,0,1] neg_hi:[0,0,1]
	v_add_f32_e32 v36, v84, v36
	v_pk_mul_f32 v[92:93], v[92:93], v[128:129] op_sel_hi:[1,0]
	v_pk_mul_f32 v[86:87], v[82:83], v[82:83]
	v_add_f32_e32 v36, v85, v36
	v_pk_fma_f32 v[88:89], v[88:89], v[96:97], v[92:93] op_sel_hi:[1,0,1] neg_lo:[0,0,1] neg_hi:[0,0,1]
	v_add_f32_e32 v36, v86, v36
	v_pk_mul_f32 v[94:95], v[94:95], v[128:129] op_sel_hi:[1,0]
	v_pk_mul_f32 v[92:93], v[88:89], v[88:89]
	v_add_f32_e32 v36, v87, v36
	v_pk_fma_f32 v[90:91], v[90:91], v[96:97], v[94:95] op_sel_hi:[1,0,1] neg_lo:[0,0,1] neg_hi:[0,0,1]
	v_add_f32_e32 v36, v92, v36
	v_pk_mul_f32 v[94:95], v[90:91], v[90:91]
	v_add_f32_e32 v36, v93, v36
	v_add_f32_e32 v36, v94, v36
	v_add_f32_e32 v36, v95, v36
	v_mov_b32_e32 v37, v36
	v_readlane_b32 s72, v254, 41
	v_readlane_b32 s73, v254, 42
	v_readlane_b32 s74, v254, 43
	v_readlane_b32 s75, v254, 44
	s_waitcnt lgkmcnt(0)
; DI unsigned pk2(float lo, float hi) { const f32x2 v = {lo, hi}; return __builtin_bit_cast(unsigned, __builtin_convertvector(v, bf16x2_t)); }
; DI void attn_block(const Params& P, const Frame& F, int L, int b, int h, int qb, float lam, float oml) {
;     ...
;     const float r = oml * __builtin_amdgcn_rsqf(ss * (1.0f / 128.0f) + EPS);
;     unsigned long long ov[8];
; #pragma unroll
;     for (int d = 0; d < 8; ++d) ov[d] = (unsigned long long)pk2(O[0][d][0] * r * nwv[d][0], O[0][d][1] * r * nwv[d][1]) | ((unsigned long long)pk2(O[0][d][2] * r * nwv[d][2], O[0][d][3] * r * nwv[d][3]) << 32);
; #pragma unroll
;     for (int d = 0; d < 8; ++d) *(unsigned long long*)(MIX + (rowbase + qrow) * D + 512 + h * 128 + 16 * d + 4 * rq) = ov[d];
	s_nop 1
	v_permlane16_swap_b32_e32 v36, v37
	v_add_f32_e32 v36, v36, v37
	ds_bpermute_b32 v37, v190, v36
	v_readlane_b32 s76, v254, 45
	v_readlane_b32 s77, v254, 46
	v_readlane_b32 s78, v254, 47
	v_readlane_b32 s79, v254, 48
	s_waitcnt lgkmcnt(0)
	v_add_f32_e32 v36, v36, v37
	v_fmamk_f32 v36, v36, 0x3c000000, v163
	v_rsq_f32_e32 v36, v36
	v_readlane_b32 s80, v254, 49
	v_readlane_b32 s81, v254, 50
	v_readlane_b32 s82, v254, 51
	v_mul_f32_e32 v36, 0x3f24fd5c, v36
	v_pk_mul_f32 v[32:33], v[32:33], v[36:37] op_sel_hi:[1,0]
	v_readlane_b32 s83, v254, 52
	s_waitcnt vmcnt(7)
	v_pk_mul_f32 v[0:1], v[0:1], v[32:33]
	v_pk_mul_f32 v[32:33], v[34:35], v[36:37] op_sel_hi:[1,0]
	v_cvt_pk_bf16_f32 v0, v0, v1
	v_pk_mul_f32 v[2:3], v[2:3], v[32:33]
	s_nop 0
	v_cvt_pk_bf16_f32 v1, v2, v3
	v_pk_mul_f32 v[2:3], v[40:41], v[36:37] op_sel_hi:[1,0]
	s_waitcnt vmcnt(6)
	v_pk_mul_f32 v[2:3], v[4:5], v[2:3]
	v_pk_mul_f32 v[4:5], v[42:43], v[36:37] op_sel_hi:[1,0]
	v_cvt_pk_bf16_f32 v2, v2, v3
	v_pk_mul_f32 v[4:5], v[6:7], v[4:5]
	v_pk_mul_f32 v[6:7], v[50:51], v[36:37] op_sel_hi:[1,0]
	v_cvt_pk_bf16_f32 v3, v4, v5
	v_pk_mul_f32 v[4:5], v[48:49], v[36:37] op_sel_hi:[1,0]
	s_waitcnt vmcnt(5)
	v_pk_mul_f32 v[6:7], v[10:11], v[6:7]
	v_pk_mul_f32 v[4:5], v[8:9], v[4:5]
	v_pk_mul_f32 v[8:9], v[54:55], v[36:37] op_sel_hi:[1,0]
	v_cvt_pk_bf16_f32 v4, v4, v5
	v_cvt_pk_bf16_f32 v5, v6, v7
	v_pk_mul_f32 v[6:7], v[52:53], v[36:37] op_sel_hi:[1,0]
	s_waitcnt vmcnt(4)
	v_pk_mul_f32 v[8:9], v[14:15], v[8:9]
	v_pk_mul_f32 v[6:7], v[12:13], v[6:7]
	v_pk_mul_f32 v[10:11], v[62:63], v[36:37] op_sel_hi:[1,0]
	v_cvt_pk_bf16_f32 v6, v6, v7
	v_cvt_pk_bf16_f32 v7, v8, v9
	v_pk_mul_f32 v[8:9], v[60:61], v[36:37] op_sel_hi:[1,0]
	s_waitcnt vmcnt(3)
	v_pk_mul_f32 v[10:11], v[18:19], v[10:11]
	v_pk_mul_f32 v[8:9], v[16:17], v[8:9]
	v_pk_mul_f32 v[12:13], v[74:75], v[36:37] op_sel_hi:[1,0]
	v_cvt_pk_bf16_f32 v8, v8, v9
	v_cvt_pk_bf16_f32 v9, v10, v11
	v_pk_mul_f32 v[10:11], v[72:73], v[36:37] op_sel_hi:[1,0]
	s_waitcnt vmcnt(2)
	v_pk_mul_f32 v[12:13], v[22:23], v[12:13]
	v_pk_mul_f32 v[10:11], v[20:21], v[10:11]
	v_pk_mul_f32 v[14:15], v[82:83], v[36:37] op_sel_hi:[1,0]
	v_cvt_pk_bf16_f32 v10, v10, v11
	v_cvt_pk_bf16_f32 v11, v12, v13
	v_pk_mul_f32 v[12:13], v[80:81], v[36:37] op_sel_hi:[1,0]
	s_waitcnt vmcnt(1)
	v_pk_mul_f32 v[14:15], v[26:27], v[14:15]
	v_pk_mul_f32 v[12:13], v[24:25], v[12:13]
	v_pk_mul_f32 v[16:17], v[90:91], v[36:37] op_sel_hi:[1,0]
	v_cvt_pk_bf16_f32 v12, v12, v13
	v_cvt_pk_bf16_f32 v13, v14, v15
	v_pk_mul_f32 v[14:15], v[88:89], v[36:37] op_sel_hi:[1,0]
	s_waitcnt vmcnt(0)
	v_pk_mul_f32 v[16:17], v[30:31], v[16:17]
	v_pk_mul_f32 v[14:15], v[28:29], v[14:15]
	s_nop 0
	v_cvt_pk_bf16_f32 v14, v14, v15
	v_cvt_pk_bf16_f32 v15, v16, v17
	v_lshlrev_b64 v[16:17], 12, v[126:127]
	v_lshl_add_u64 v[16:17], s[54:55], 0, v[16:17]
	v_lshl_add_u64 v[16:17], v[16:17], 0, s[40:41]
	v_lshl_add_u64 v[16:17], v[106:107], 1, v[16:17]
	v_lshl_add_u64 v[18:19], v[16:17], 0, s[48:49]
	v_add_co_u32_e32 v16, vcc, s65, v16
	s_nop 1
	v_addc_co_u32_e32 v17, vcc, 0, v17, vcc
	global_store_dwordx2 v[16:17], v[0:1], off offset:1024
	global_store_dwordx2 v[18:19], v[2:3], off offset:32
	global_store_dwordx2 v[18:19], v[4:5], off offset:64
	global_store_dwordx2 v[18:19], v[6:7], off offset:96
	global_store_dwordx2 v[18:19], v[8:9], off offset:128
	global_store_dwordx2 v[18:19], v[10:11], off offset:160
	global_store_dwordx2 v[18:19], v[12:13], off offset:192
	global_store_dwordx2 v[18:19], v[14:15], off offset:224

; DI void attn_block(const Params& P, const Frame& F, int L, int b, int h, int qb, float lam, float oml) {
;     ...
;                 for (int i = 0; i < 8; ++i) { mx = fmaxf(mx, x2[i].x); mx = fmaxf(mx, x2[i].y); }
;                 mx += base2;
;                 mx = fmaxf(mx, shx<16>(mx)); mx = fmaxf(mx, shx<32>(mx));
;                 const float mnew = fmaxf(mrun[j], mx), alpha = __builtin_amdgcn_exp2f(mrun[j] - mnew), msub = mnew - base2;
;                 const f32x2 ms2 = (f32x2){msub, msub}; f32x2 ps2 = (f32x2){0.f, 0.f};
; #pragma unroll
;                 for (int i = 0; i < 8; ++i) { const f32x2 t = x2[i] - ms2; x2[i] = (f32x2){__builtin_amdgcn_exp2f(t.x), __builtin_amdgcn_exp2f(t.y)}; ps2 = ps2 + x2[i]; }
;                 lrun[j] = lrun[j] * alpha + (ps2.x + ps2.y); mrun[j] = mnew;
;                 if (__builtin_amdgcn_ballot_w64(alpha != 1.0f) != 0ull) {
; #pragma unroll
;                     for (int d = 0; d < 8; ++d) O[j][d] = O[j][d] * alpha; }
.LBB0_2624:
	v_max3_f32 v165, v160, s64, v161
	v_max3_f32 v165, v165, v158, v159
	v_max3_f32 v165, v165, v156, v157
	v_max3_f32 v165, v165, v154, v155
	v_cvt_f32_i32_e32 v205, v201
	v_max3_f32 v165, v165, v152, v153
	v_max3_f32 v165, v165, v150, v151
	v_max3_f32 v165, v165, v148, v149
	v_max3_f32 v165, v165, v146, v147
	v_fmac_f32_e32 v165, v199, v205
	v_mov_b32_e32 v166, v165
	s_waitcnt lgkmcnt(0)
	v_max_f32_e32 v166, v166, v166
	s_nop 1
	v_permlane16_swap_b32_e32 v165, v166
	v_max_f32_e32 v165, v165, v166
	v_mov_b32_e32 v166, v165
	s_waitcnt lgkmcnt(0)
	s_nop 1
	v_permlane32_swap_b32_e32 v165, v166
	v_max3_f32 v204, v144, v165, v166
	v_sub_f32_e32 v144, v144, v204
	v_exp_f32_e32 v144, v144
	s_nop 0
	v_cmp_neq_f32_e32 vcc, 1.0, v144
	s_cbranch_vccz .LBB0_2626
	v_pk_mul_f32 v[34:35], v[34:35], v[144:145] op_sel_hi:[1,0]
	v_pk_mul_f32 v[32:33], v[32:33], v[144:145] op_sel_hi:[1,0]
	v_pk_mul_f32 v[42:43], v[42:43], v[144:145] op_sel_hi:[1,0]
	v_pk_mul_f32 v[40:41], v[40:41], v[144:145] op_sel_hi:[1,0]
	v_pk_mul_f32 v[50:51], v[50:51], v[144:145] op_sel_hi:[1,0]
	v_pk_mul_f32 v[48:49], v[48:49], v[144:145] op_sel_hi:[1,0]
	v_pk_mul_f32 v[54:55], v[54:55], v[144:145] op_sel_hi:[1,0]
	v_pk_mul_f32 v[52:53], v[52:53], v[144:145] op_sel_hi:[1,0]
	v_pk_mul_f32 v[62:63], v[62:63], v[144:145] op_sel_hi:[1,0]
	v_pk_mul_f32 v[60:61], v[60:61], v[144:145] op_sel_hi:[1,0]
	v_pk_mul_f32 v[74:75], v[74:75], v[144:145] op_sel_hi:[1,0]
	v_pk_mul_f32 v[72:73], v[72:73], v[144:145] op_sel_hi:[1,0]
	v_pk_mul_f32 v[82:83], v[82:83], v[144:145] op_sel_hi:[1,0]
	v_pk_mul_f32 v[80:81], v[80:81], v[144:145] op_sel_hi:[1,0]
	v_pk_mul_f32 v[90:91], v[90:91], v[144:145] op_sel_hi:[1,0]
	v_pk_mul_f32 v[88:89], v[88:89], v[144:145] op_sel_hi:[1,0]

; DI void attn_block(const Params& P, const Frame& F, int L, int b, int h, int qb, float lam, float oml) {
;     ...
;                 for (int i = 0; i < 8; ++i) { mx = fmaxf(mx, x2[i].x); mx = fmaxf(mx, x2[i].y); }
;                 mx += base2;
;                 mx = fmaxf(mx, shx<16>(mx)); mx = fmaxf(mx, shx<32>(mx));
;                 const float mnew = fmaxf(mrun[j], mx), alpha = __builtin_amdgcn_exp2f(mrun[j] - mnew), msub = mnew - base2;
;                 const f32x2 ms2 = (f32x2){msub, msub}; f32x2 ps2 = (f32x2){0.f, 0.f};
; #pragma unroll
;                 for (int i = 0; i < 8; ++i) { const f32x2 t = x2[i] - ms2; x2[i] = (f32x2){__builtin_amdgcn_exp2f(t.x), __builtin_amdgcn_exp2f(t.y)}; ps2 = ps2 + x2[i]; }
;                 lrun[j] = lrun[j] * alpha + (ps2.x + ps2.y); mrun[j] = mnew;
;                 if (__builtin_amdgcn_ballot_w64(alpha != 1.0f) != 0ull) {
; #pragma unroll
;                     for (int d = 0; d < 8; ++d) O[j][d] = O[j][d] * alpha; }
.LBB0_2628:
	v_max3_f32 v192, v172, s64, v173
	v_max3_f32 v192, v192, v174, v175
	v_max3_f32 v192, v192, v176, v177
	v_max3_f32 v192, v192, v178, v179
	v_max3_f32 v192, v192, v170, v171
	v_max3_f32 v192, v192, v168, v169
	v_max3_f32 v192, v192, v166, v167
	v_mul_f32_e32 v206, v199, v205
	v_max3_f32 v192, v192, v164, v165
	v_add_f32_e32 v192, v206, v192
	v_mov_b32_e32 v205, v192
	s_waitcnt lgkmcnt(0)
	v_max_f32_e32 v205, v205, v205
	s_nop 1
	v_permlane16_swap_b32_e32 v192, v205
	v_max_f32_e32 v192, v192, v205
	v_mov_b32_e32 v205, v192
	s_waitcnt lgkmcnt(0)
	s_nop 1
	v_permlane32_swap_b32_e32 v192, v205
	v_max3_f32 v205, v162, v192, v205
	v_sub_f32_e32 v162, v162, v205
	v_exp_f32_e32 v162, v162
	s_nop 0
	v_cmp_neq_f32_e32 vcc, 1.0, v162
	s_cbranch_vccz .LBB0_2630
	v_pk_mul_f32 v[38:39], v[38:39], v[162:163] op_sel_hi:[1,0]
	v_pk_mul_f32 v[36:37], v[36:37], v[162:163] op_sel_hi:[1,0]
	v_pk_mul_f32 v[46:47], v[46:47], v[162:163] op_sel_hi:[1,0]
	v_pk_mul_f32 v[44:45], v[44:45], v[162:163] op_sel_hi:[1,0]
	v_pk_mul_f32 v[58:59], v[58:59], v[162:163] op_sel_hi:[1,0]
	v_pk_mul_f32 v[56:57], v[56:57], v[162:163] op_sel_hi:[1,0]
	v_pk_mul_f32 v[66:67], v[66:67], v[162:163] op_sel_hi:[1,0]
	v_pk_mul_f32 v[64:65], v[64:65], v[162:163] op_sel_hi:[1,0]
	v_pk_mul_f32 v[70:71], v[70:71], v[162:163] op_sel_hi:[1,0]
	v_pk_mul_f32 v[68:69], v[68:69], v[162:163] op_sel_hi:[1,0]
	v_pk_mul_f32 v[78:79], v[78:79], v[162:163] op_sel_hi:[1,0]
	v_pk_mul_f32 v[76:77], v[76:77], v[162:163] op_sel_hi:[1,0]
	v_pk_mul_f32 v[86:87], v[86:87], v[162:163] op_sel_hi:[1,0]
	v_pk_mul_f32 v[84:85], v[84:85], v[162:163] op_sel_hi:[1,0]
	v_pk_mul_f32 v[94:95], v[94:95], v[162:163] op_sel_hi:[1,0]
	v_pk_mul_f32 v[92:93], v[92:93], v[162:163] op_sel_hi:[1,0]

.LBB0_2680:
	s_cmp_lt_u32 s3, 0x40001
	s_mov_b64 s[18:19], 0
	s_cselect_b64 s[20:21], -1, 0
	s_mov_b64 s[22:23], -1
	s_and_b64 vcc, exec, s[20:21]
	s_cbranch_vccnz .LBB0_2677
	s_branch .LBB0_2674
	s_nop 0
	s_nop 0
	s_nop 0
	s_nop 0
	s_nop 0
	s_nop 0
	s_nop 0
	s_nop 0
	s_nop 0
	s_nop 0
	s_nop 0
	s_nop 0
	s_nop 0
	s_nop 0
	s_nop 0
	s_nop 0
	s_nop 0
	s_nop 0
	s_nop 0
	s_nop 0
	s_nop 0
	s_nop 0
	s_nop 0
	s_nop 0
	s_nop 0
	s_nop 0
	s_nop 0
	s_nop 0
	s_nop 0
	s_nop 0
	s_nop 0
	s_nop 0
	s_nop 0
	s_nop 0
	s_nop 0
	s_nop 0
	s_nop 0
	s_nop 0
	s_nop 0
.LBB0_2681:
	s_or_b64 exec, exec, s[14:15]
	s_and_b64 s[14:15], s[16:17], exec

; DI unsigned pk2(float lo, float hi) { const f32x2 v = {lo, hi}; return __builtin_bit_cast(unsigned, __builtin_convertvector(v, bf16x2_t)); }
; template <int MODE, bool SB  > DI void norm_phase(const Params& P, const Frame& F, int L, const void* src_, const float* gain, bool combine) {
;     ...
;     for (int row = r_lo + F.wave; row < r_hi; row += NWAVES) {
;         f32x4 v[8];
; #pragma unroll
;         for (int j = 0; j < 8; ++j) { if constexpr (SB) v[j] = (f32x4){bflo(vb[j].x), bfhi(vb[j].x), bflo(vb[j].y), bfhi(vb[j].y)}; else v[j] = vn[j]; }
;         { const int rnx = (row + NWAVES < r_hi) ? row + NWAVES : row;
; #pragma unroll
;           for (int j = 0; j < 8; ++j) { if constexpr (SB) vb[j] = *(const u32x2*)(srcb + (size_t)rnx * D + 4 * F.lane + 256 * j); else vn[j] = *(const f32x4*)(src + (size_t)rnx * D + 4 * F.lane + 256 * j); } }
;         if (MODE == 3 && combine) {
;             const int* SLOT = (const int*)(ws + WS_SLOT); const float* TOPW = (const float*)(ws + WS_TOPW); const bf16* Y = (const bf16*)(ws + WS_T + T_YPERM);
;             const int s1 = SLOT[row * 2], s2 = SLOT[row * 2 + 1]; const float w1 = TOPW[row * 2], w2 = TOPW[row * 2 + 1];
;             u32x2 ya[8], yb[8];
; #pragma unroll
;             for (int j = 0; j < 8; ++j) { ya[j] = *(const u32x2*)(Y + (size_t)s1 * D + 4 * F.lane + 256 * j); yb[j] = *(const u32x2*)(Y + (size_t)s2 * D + 4 * F.lane + 256 * j); }
; #pragma unroll
;             for (int j = 0; j < 8; ++j) { const f32x4 y1 = (f32x4){bflo(ya[j].x), bfhi(ya[j].x), bflo(ya[j].y), bfhi(ya[j].y)}, y2 = (f32x4){bflo(yb[j].x), bfhi(yb[j].x), bflo(yb[j].y), bfhi(yb[j].y)};
;                 v[j] = v[j] + w1 * y1 + w2 * y2;
;                 const u32x2 hb = {pk2(v[j][0], v[j][1]), pk2(v[j][2], v[j][3])}; *(u32x2*)(const_cast<bf16*>(srcb) + (size_t)row * D + 4 * F.lane + 256 * j) = hb;
;                 v[j] = (f32x4){bflo(hb.x), bfhi(hb.x), bflo(hb.y), bfhi(hb.y)}; }
;         }
;         float ss = 0.f;
; #pragma unroll
;         for (int j = 0; j < 8; ++j) ss += (v[j][0] * v[j][0] + v[j][1] * v[j][1]) + (v[j][2] * v[j][2] + v[j][3] * v[j][3]);
;         const float rstd = 1.0f / sqrtf(wave_sum(ss) * (1.0f / D) + EPS);
; #pragma unroll
;         for (int j = 0; j < 8; ++j) v[j] = v[j] * rstd * g[j];
.LBB0_2879:
	s_waitcnt vmcnt(0)
	v_and_b32_e32 v57, 0xffff0000, v46
	v_and_b32_e32 v56, 0xffff0000, v44
	v_and_b32_e32 v61, 0xffff0000, v47
	v_and_b32_e32 v60, 0xffff0000, v45
	v_lshlrev_b32_e32 v80, 16, v38
	v_and_b32_e32 v98, 0xffff0000, v38
	v_lshlrev_b32_e32 v78, 16, v39
	v_and_b32_e32 v79, 0xffff0000, v39
	v_lshlrev_b32_e32 v55, 16, v46
	v_lshlrev_b32_e32 v54, 16, v44
	v_lshlrev_b32_e32 v59, 16, v47
	v_lshlrev_b32_e32 v58, 16, v45
	v_pk_mul_f32 v[38:39], v[56:57], v[56:57]
	v_pk_mul_f32 v[44:45], v[60:61], v[60:61]
	v_pk_fma_f32 v[38:39], v[54:55], v[54:55], v[38:39]
	v_pk_fma_f32 v[44:45], v[58:59], v[58:59], v[44:45]
	v_and_b32_e32 v71, 0xffff0000, v43
	v_pk_add_f32 v[38:39], v[38:39], v[44:45]
	v_and_b32_e32 v70, 0xffff0000, v42
	v_lshlrev_b32_e32 v62, 16, v40
	v_and_b32_e32 v63, 0xffff0000, v40
	v_lshlrev_b32_e32 v66, 16, v48
	v_pk_add_f32 v[38:39], v[38:39], v[38:39] op_sel_hi:[0,1]
	v_lshlrev_b32_e32 v65, 16, v43
	v_lshlrev_b32_e32 v64, 16, v42
	v_pk_mul_f32 v[42:43], v[70:71], v[70:71]
	v_lshlrev_b32_e32 v72, 16, v41
	v_pk_fma_f32 v[42:43], v[64:65], v[64:65], v[42:43]
	v_mul_f32_e32 v67, v62, v62
	v_mul_f32_e32 v45, v63, v63
	v_and_b32_e32 v73, 0xffff0000, v41
	v_mul_f32_e32 v38, v72, v72
	v_mov_b32_e32 v44, v66
	v_and_b32_e32 v93, 0xffff0000, v48
	v_lshlrev_b32_e32 v68, 16, v49
	v_and_b32_e32 v69, 0xffff0000, v49
	v_pk_add_f32 v[42:43], v[42:43], v[42:43] op_sel_hi:[0,1]
	v_pk_fma_f32 v[40:41], v[72:73], v[72:73], v[38:39] op_sel_hi:[1,1,0]
	v_pk_add_f32 v[44:45], v[66:67], v[44:45]
	v_mul_f32_e32 v40, v93, v93
	v_mul_f32_e32 v42, v68, v68
	v_mul_f32_e32 v38, v69, v69
	v_mul_f32_e32 v46, v66, v66
	v_mov_b32_e32 v47, v45
	v_pk_add_f32 v[40:41], v[46:47], v[40:41]
	v_pk_add_f32 v[38:39], v[42:43], v[38:39]
	v_and_b32_e32 v83, 0xffff0000, v53
	v_pk_add_f32 v[38:39], v[40:41], v[38:39]
	v_and_b32_e32 v82, 0xffff0000, v52
	v_lshlrev_b32_e32 v74, 16, v50
	v_and_b32_e32 v75, 0xffff0000, v50
	v_pk_add_f32 v[38:39], v[38:39], v[38:39] op_sel_hi:[0,1]
	v_lshlrev_b32_e32 v77, 16, v53
	v_lshlrev_b32_e32 v76, 16, v52
	v_pk_mul_f32 v[40:41], v[82:83], v[82:83]
	v_lshlrev_b32_e32 v84, 16, v51
	v_pk_fma_f32 v[40:41], v[76:77], v[76:77], v[40:41]
	v_mul_f32_e32 v81, v74, v74
	v_mul_f32_e32 v43, v75, v75
	v_and_b32_e32 v85, 0xffff0000, v51
	v_mul_f32_e32 v38, v84, v84
	v_mov_b32_e32 v42, v80
	v_pk_add_f32 v[40:41], v[40:41], v[40:41] op_sel_hi:[0,1]
	v_pk_fma_f32 v[44:45], v[84:85], v[84:85], v[38:39] op_sel_hi:[1,1,0]
	v_pk_add_f32 v[42:43], v[80:81], v[42:43]
	v_mul_f32_e32 v44, v98, v98
	v_mul_f32_e32 v40, v78, v78
	v_mul_f32_e32 v38, v79, v79
	v_mul_f32_e32 v46, v80, v80
	v_mov_b32_e32 v47, v43
	v_pk_add_f32 v[42:43], v[46:47], v[44:45]
	v_pk_add_f32 v[38:39], v[40:41], v[38:39]
	s_mov_b32 s12, s0
	v_pk_add_f32 v[38:39], v[42:43], v[38:39]
	s_add_i32 s0, s0, 8
	v_add_f32_e32 v38, v38, v39
	s_cmp_ge_i32 s0, s3
	s_cselect_b64 s[10:11], -1, 0
	v_add_f32_dpp v38, v38, v38 quad_perm:[1,0,3,2] row_mask:0xf bank_mask:0xf bound_ctrl:1
	s_cmp_lt_i32 s0, s3
	s_cselect_b32 s8, s0, s12
	v_add_f32_dpp v38, v38, v38 quad_perm:[2,3,0,1] row_mask:0xf bank_mask:0xf bound_ctrl:1
	ds_swizzle_b32 v39, v38 offset:swizzle(SWAP,4)
	s_ashr_i32 s9, s8, 31
	s_lshl_b64 s[8:9], s[8:9], 12
	v_lshl_add_u64 v[86:87], v[34:35], 0, s[8:9]
	global_load_dwordx2 v[46:47], v[86:87], off
	global_load_dwordx2 v[44:45], v[86:87], off offset:512
	global_load_dwordx2 v[42:43], v[86:87], off offset:1024
	global_load_dwordx2 v[40:41], v[86:87], off offset:1536
	s_waitcnt lgkmcnt(0)
	v_add_f32_e32 v38, v38, v39
	ds_swizzle_b32 v39, v38 offset:swizzle(SWAP,8)
	v_mov_b32_e32 v96, v59
	v_mov_b32_e32 v59, v60
	v_mov_b32_e32 v97, v61
	v_mov_b32_e32 v99, 0
	s_waitcnt lgkmcnt(0)
	v_add_f32_e32 v38, v38, v39
	v_mov_b32_e32 v39, v38
	v_mov_b32_e32 v100, 0
	s_ashr_i32 s13, s12, 31
	s_waitcnt lgkmcnt(0)
	s_nop 1
	v_permlane16_swap_b32_e32 v38, v39
	v_add_f32_e32 v38, v38, v39
	v_mov_b32_e32 v39, v38
	s_waitcnt lgkmcnt(0)
	s_nop 1
	v_permlane32_swap_b32_e32 v38, v39
	v_add_f32_e32 v38, v38, v39
	v_fmamk_f32 v38, v38, 0x3a000000, v89
	v_mul_f32_e32 v39, 0x4f800000, v38
	v_cmp_gt_f32_e32 vcc, s19, v38
	s_nop 1
	v_cndmask_b32_e32 v38, v38, v39, vcc
	v_sqrt_f32_e32 v39, v38
	s_nop 0
	v_add_u32_e32 v48, -1, v39
	v_fma_f32 v49, -v48, v39, v38
	v_cmp_ge_f32_e64 s[8:9], 0, v49
	v_add_u32_e32 v49, 1, v39
	s_nop 0
	v_cndmask_b32_e64 v48, v39, v48, s[8:9]
	v_fma_f32 v39, -v49, v39, v38
	v_cmp_lt_f32_e64 s[8:9], 0, v39
	s_nop 1
	v_cndmask_b32_e64 v39, v48, v49, s[8:9]
	v_mul_f32_e32 v48, 0x37800000, v39
	v_cndmask_b32_e32 v39, v39, v48, vcc
	v_cmp_class_f32_e32 vcc, v38, v90
	s_nop 1
	v_cndmask_b32_e32 v67, v39, v38, vcc
	global_load_dwordx2 v[48:49], v[86:87], off offset:2048
	global_load_dwordx2 v[52:53], v[86:87], off offset:2560
	global_load_dwordx2 v[50:51], v[86:87], off offset:3072
	global_load_dwordx2 v[38:39], v[86:87], off offset:3584
	v_div_scale_f32 v81, s[8:9], v67, v67, 1.0
	v_rcp_f32_e32 v94, v81
	s_lshl_b64 s[8:9], s[12:13], 11
	s_mov_b32 s13, 0
	v_fma_f32 v86, -v81, v94, 1.0
	v_fmac_f32_e32 v94, v86, v94
	v_div_scale_f32 v86, vcc, 1.0, v67, 1.0
	v_mul_f32_e32 v87, v86, v94
	v_fma_f32 v95, -v81, v87, v86
	v_fmac_f32_e32 v87, v95, v94
	v_fma_f32 v81, -v81, v87, v86
	v_div_fmas_f32 v81, v81, v94, v87
	v_div_fixup_f32 v86, v81, v67, 1.0
	v_mov_b32_e32 v94, v55
	v_mov_b32_e32 v95, v57
	v_mov_b32_e32 v55, v56
	v_pk_mul_f32 v[94:95], v[94:95], v[86:87] op_sel_hi:[1,0]
	v_pk_mul_f32 v[56:57], v[54:55], v[86:87] op_sel_hi:[1,0]
	v_pk_mul_f32 v[54:55], v[58:59], v[86:87] op_sel_hi:[1,0]
	v_mov_b32_e32 v58, v64
	v_mov_b32_e32 v59, v70
	v_mov_b32_e32 v70, v65
	v_mov_b32_e32 v67, v93
; DI unsigned pk4_fp8(float a, float b, float c, float d) { unsigned w = 0u; w = __builtin_amdgcn_cvt_pk_fp8_f32(a, b, w, false); w = __builtin_amdgcn_cvt_pk_fp8_f32(c, d, w, true); return w; }
; DI float wave_sum(float v) { v += shx<1>(v); v += shx<2>(v); v += shx<4>(v); v += shx<8>(v); v += shx<16>(v); v += shx<32>(v); return v; }
; template <int MODE, bool SB  > DI void norm_phase(const Params& P, const Frame& F, int L, const void* src_, const float* gain, bool combine) {
;     ...
;         const float rstd = 1.0f / sqrtf(wave_sum(ss) * (1.0f / D) + EPS);
; #pragma unroll
;         for (int j = 0; j < 8; ++j) v[j] = v[j] * rstd * g[j];
;         if (MODE == 4) {
; #pragma unroll
;             for (int j = 0; j < 8; ++j) *(f32x4*)(P.out + (size_t)row * D + 4 * F.lane + 256 * j) = v[j];
;         } else if (MODE == 0 || MODE == 2 || (MODE == 3 && L == 1)) {
;             unsigned* o4 = (unsigned*)((unsigned char*)HN + (size_t)row * D) + F.lane; const float hs = (float)(1 << LS_HN);
; #pragma unroll
;             for (int j = 0; j < 8; ++j) o4[64 * j] = pk4_fp8(v[j][0] * hs, v[j][1] * hs, v[j][2] * hs, v[j][3] * hs);
;     ...
;             int e1 = 0, e2 = 0; float l1 = -INFINITY, l2 = -INFINITY;
	v_pk_mul_f32 v[94:95], v[8:9], v[94:95]
	v_pk_mul_f32 v[60:61], v[86:87], v[58:59] op_sel_hi:[0,1]
	v_pk_mul_f32 v[58:59], v[86:87], v[70:71] op_sel_hi:[0,1]
	v_pk_mul_f32 v[70:71], v[66:67], v[86:87] op_sel_hi:[1,0]
	v_pk_mul_f32 v[56:57], v[0:1], v[56:57]
	v_pk_mul_f32 v[66:67], v[68:69], v[86:87] op_sel_hi:[1,0]
	v_pk_mul_f32 v[68:69], v[16:17], v[70:71]
	v_mov_b32_e32 v70, v76
	v_mov_b32_e32 v71, v82
	v_mov_b32_e32 v82, v77
	v_pk_mul_f32 v[76:77], v[74:75], v[86:87] op_sel_hi:[1,0]
	v_pk_mul_f32 v[74:75], v[84:85], v[86:87] op_sel_hi:[1,0]
	v_mul_f32_e32 v84, 4.0, v94
	v_mul_f32_e32 v85, 4.0, v95
	v_mov_b32_e32 v93, 0
	v_mov_b32_e32 v81, v98
	v_cvt_pk_fp8_f32 v93, v84, v85
	v_mul_f32_e32 v84, 4.0, v56
	v_mul_f32_e32 v85, 4.0, v57
	v_mov_b32_e32 v98, 0
	v_cvt_pk_fp8_f32 v98, v84, v85
	v_pk_mul_f32 v[54:55], v[2:3], v[54:55]
	v_pk_mul_f32 v[60:61], v[4:5], v[60:61]
	v_pk_mul_f32 v[64:65], v[62:63], v[86:87] op_sel_hi:[1,0]
	v_mul_f32_e32 v84, 4.0, v54
	v_mul_f32_e32 v85, 4.0, v55
	v_pk_mul_f32 v[96:97], v[96:97], v[86:87] op_sel_hi:[1,0]
	v_pk_mul_f32 v[64:65], v[12:13], v[64:65]
	v_cvt_pk_fp8_f32 v98, v84, v85 op_sel:[0,0,1]
	v_mul_f32_e32 v84, 4.0, v60
	v_mul_f32_e32 v85, 4.0, v61
	v_pk_mul_f32 v[96:97], v[10:11], v[96:97]
	v_cvt_pk_fp8_f32 v99, v84, v85
	v_mul_f32_e32 v84, 4.0, v64
	v_mul_f32_e32 v85, 4.0, v65
	v_pk_mul_f32 v[62:63], v[72:73], v[86:87] op_sel_hi:[1,0]
	v_pk_mul_f32 v[72:73], v[86:87], v[70:71] op_sel_hi:[0,1]
	v_pk_mul_f32 v[70:71], v[86:87], v[82:83] op_sel_hi:[0,1]
	v_pk_mul_f32 v[80:81], v[80:81], v[86:87] op_sel_hi:[1,0]
	v_pk_mul_f32 v[78:79], v[78:79], v[86:87] op_sel_hi:[1,0]
	v_mul_f32_e32 v86, 4.0, v96
	v_mul_f32_e32 v87, 4.0, v97
	v_cvt_pk_fp8_f32 v100, v84, v85
	v_pk_mul_f32 v[58:59], v[6:7], v[58:59]
	v_cvt_pk_fp8_f32 v93, v86, v87 op_sel:[0,0,1]
	v_pk_mul_f32 v[62:63], v[14:15], v[62:63]
	v_mul_f32_e32 v86, 4.0, v58
	v_mul_f32_e32 v87, 4.0, v59
	v_cvt_pk_fp8_f32 v99, v86, v87 op_sel:[0,0,1]
	v_mul_f32_e32 v84, 4.0, v62
	v_mul_f32_e32 v85, 4.0, v63
	v_lshl_add_u64 v[82:83], v[36:37], 0, s[8:9]
	v_cvt_pk_fp8_f32 v100, v84, v85 op_sel:[0,0,1]
	v_pk_mul_f32 v[72:73], v[20:21], v[72:73]
	global_store_dword v[82:83], v93, off
	global_store_dword v[82:83], v98, off offset:256
	global_store_dword v[82:83], v99, off offset:512
	global_store_dword v[82:83], v100, off offset:768
	v_mul_f32_e32 v84, 4.0, v68
	v_mul_f32_e32 v85, 4.0, v69
	v_mov_b32_e32 v93, 0
	v_cvt_pk_fp8_f32 v93, v84, v85
	v_mul_f32_e32 v84, 4.0, v72
	v_mul_f32_e32 v85, 4.0, v73
	v_mov_b32_e32 v98, 0
	v_cvt_pk_fp8_f32 v98, v84, v85
	v_pk_mul_f32 v[70:71], v[22:23], v[70:71]
	v_pk_mul_f32 v[76:77], v[24:25], v[76:77]
	v_mul_f32_e32 v84, 4.0, v70
	v_mul_f32_e32 v85, 4.0, v71
	v_pk_mul_f32 v[80:81], v[28:29], v[80:81]
	v_cvt_pk_fp8_f32 v98, v84, v85 op_sel:[0,0,1]
	v_mul_f32_e32 v84, 4.0, v76
	v_mul_f32_e32 v85, 4.0, v77
	v_mov_b32_e32 v99, 0
	v_pk_mul_f32 v[66:67], v[18:19], v[66:67]
	v_cvt_pk_fp8_f32 v99, v84, v85
	v_mul_f32_e32 v84, 4.0, v80
	v_mul_f32_e32 v85, 4.0, v81
	v_mov_b32_e32 v100, 0
	v_mul_f32_e32 v86, 4.0, v66
	v_mul_f32_e32 v87, 4.0, v67
	v_cvt_pk_fp8_f32 v100, v84, v85
	v_pk_mul_f32 v[74:75], v[26:27], v[74:75]
	v_cvt_pk_fp8_f32 v93, v86, v87 op_sel:[0,0,1]
	v_pk_mul_f32 v[78:79], v[30:31], v[78:79]
	v_mul_f32_e32 v86, 4.0, v74
	v_mul_f32_e32 v87, 4.0, v75
	v_cvt_pk_fp8_f32 v99, v86, v87 op_sel:[0,0,1]
	v_mul_f32_e32 v84, 4.0, v78
	v_mul_f32_e32 v85, 4.0, v79
	v_cvt_pk_fp8_f32 v100, v84, v85 op_sel:[0,0,1]
	global_store_dword v[82:83], v93, off offset:1024
	global_store_dword v[82:83], v98, off offset:1280
	global_store_dword v[82:83], v99, off offset:1536
	global_store_dword v[82:83], v100, off offset:1792
	v_mov_b32_e32 v84, v94
	v_mov_b32_e32 v85, v56
	v_mov_b32_e32 v56, v95
	v_mov_b32_e32 v86, v96
	v_mov_b32_e32 v87, v54
	v_mov_b32_e32 v54, v97
	v_mov_b32_e32 v95, 0xff800000
	v_mov_b32_e32 v94, v88
	v_mov_b32_e32 v93, 0xff800000
	v_mov_b32_e32 v96, 0
	v_mov_b32_e32 v83, 0
; #define LAS __attribute__((address_space(3)))
; DI float wave_sum(float v) { v += shx<1>(v); v += shx<2>(v); v += shx<4>(v); v += shx<8>(v); v += shx<16>(v); v += shx<32>(v); return v; }
; template <int MODE, bool SB  > DI void norm_phase(const Params& P, const Frame& F, int L, const void* src_, const float* gain, bool combine) {
;     ...
;             for (int q = 0; q < 8; ++q) { float s = 0.f;
; #pragma unroll
;                 for (int j = 0; j < 8; ++j) { const f32x4 w = *(const LAS f32x4*)(F.lds + (size_t)(q * D + 256 * j + 4 * F.lane) * 4); s += (v[j][0] * w[0] + v[j][1] * w[1]) + (v[j][2] * w[2] + v[j][3] * w[3]); }
;                 s = wave_sum(s);
;                 if (s > l1) { l2 = l1; e2 = e1; l1 = s; e1 = q; } else if (s > l2) { l2 = s; e2 = q; } }
.LBB0_2880:
	ds_read_b128 v[98:101], v94
	ds_read_b128 v[102:105], v94 offset:1024
	s_waitcnt lgkmcnt(1)
	v_mov_b32_e32 v106, v98
	s_waitcnt lgkmcnt(0)
	v_mov_b32_e32 v107, v102
	v_mov_b32_e32 v102, v99
	v_mov_b32_e32 v99, v104
	v_mov_b32_e32 v104, v101
	v_mov_b32_e32 v98, v100
	v_pk_mul_f32 v[100:101], v[54:55], v[104:105]
	v_pk_mul_f32 v[102:103], v[56:57], v[102:103]
	v_pk_fma_f32 v[104:105], v[86:87], v[98:99], v[100:101]
	ds_read_b128 v[98:101], v94 offset:2048
	v_pk_fma_f32 v[102:103], v[84:85], v[106:107], v[102:103]
	s_nop 0
	v_pk_add_f32 v[102:103], v[102:103], v[104:105]
	s_nop 0
	v_add_f32_e32 v82, 0, v102
	v_add_f32_e32 v110, v82, v103
	ds_read_b128 v[102:105], v94 offset:3072
	s_waitcnt lgkmcnt(1)
	v_pk_mul_f32 v[106:107], v[58:59], v[100:101]
	v_pk_mul_f32 v[108:109], v[60:61], v[98:99]
	ds_read_b128 v[98:101], v94 offset:4096
	v_pk_mov_b32 v[112:113], v[108:109], v[106:107] op_sel:[1,0]
	v_mov_b32_e32 v109, v107
	v_pk_add_f32 v[112:113], v[112:113], v[108:109]
	ds_read_b128 v[106:109], v94 offset:5120
	s_waitcnt lgkmcnt(1)
	v_mul_f32_e32 v111, v68, v98
	v_mul_f32_e32 v82, v69, v99
	v_pk_add_f32 v[98:99], v[112:113], v[112:113] op_sel:[0,1] op_sel_hi:[1,0]
	v_mul_f32_e32 v97, v66, v100
	v_mov_b32_e32 v99, v82
	v_mul_f32_e32 v82, v65, v103
	v_mul_f32_e32 v114, v67, v101
	v_pk_fma_f32 v[100:101], v[64:65], v[102:103], v[82:83] op_sel_hi:[1,1,0]
	v_mul_f32_e32 v82, v63, v105
	v_pk_fma_f32 v[102:103], v[62:63], v[104:105], v[82:83] op_sel_hi:[1,1,0]
	v_mov_b32_e32 v101, v97
	v_mov_b32_e32 v103, v114
	v_pk_add_f32 v[98:99], v[110:111], v[98:99]
	v_pk_add_f32 v[100:101], v[100:101], v[102:103]
	s_waitcnt lgkmcnt(0)
	v_pk_mul_f32 v[108:109], v[70:71], v[108:109]
	v_pk_add_f32 v[110:111], v[98:99], v[100:101]
	ds_read_b128 v[98:101], v94 offset:6144
	ds_read_b128 v[102:105], v94 offset:7168
	v_pk_mul_f32 v[106:107], v[72:73], v[106:107]
	s_waitcnt lgkmcnt(0)
	v_mul_f32_e32 v82, v80, v102
	v_mul_f32_e32 v97, v81, v103
	v_pk_add_f32 v[102:103], v[110:111], v[110:111] op_sel:[0,1] op_sel_hi:[1,0]
	v_pk_mov_b32 v[112:113], v[106:107], v[108:109] op_sel:[1,0]
	v_mov_b32_e32 v107, v109
	v_mov_b32_e32 v103, v82
	v_mul_f32_e32 v82, v77, v99
	v_pk_add_f32 v[106:107], v[112:113], v[106:107]
	v_pk_fma_f32 v[98:99], v[76:77], v[98:99], v[82:83] op_sel_hi:[1,1,0]
	v_mul_f32_e32 v82, v75, v101
	v_mul_f32_e32 v108, v78, v104
	v_mul_f32_e32 v109, v79, v105
	v_pk_add_f32 v[104:105], v[106:107], v[106:107] op_sel:[0,1] op_sel_hi:[1,0]
	v_pk_fma_f32 v[100:101], v[74:75], v[100:101], v[82:83] op_sel_hi:[1,1,0]
	v_mov_b32_e32 v105, v97
	v_mov_b32_e32 v99, v108
	v_mov_b32_e32 v101, v109
	v_pk_add_f32 v[102:103], v[102:103], v[104:105]
	v_pk_add_f32 v[98:99], v[98:99], v[100:101]
	s_nop 0
	v_pk_add_f32 v[98:99], v[102:103], v[98:99]
	s_nop 0
	v_add_f32_e32 v82, v98, v99
	s_nop 1
	v_add_f32_dpp v82, v82, v82 quad_perm:[1,0,3,2] row_mask:0xf bank_mask:0xf bound_ctrl:1
	s_nop 1
	v_add_f32_dpp v82, v82, v82 quad_perm:[2,3,0,1] row_mask:0xf bank_mask:0xf bound_ctrl:1
	ds_swizzle_b32 v97, v82 offset:swizzle(SWAP,4)
	s_waitcnt lgkmcnt(0)
	v_add_f32_e32 v82, v82, v97
	ds_swizzle_b32 v97, v82 offset:swizzle(SWAP,8)
	s_waitcnt lgkmcnt(0)
	v_add_f32_e32 v82, v82, v97
	v_mov_b32_e32 v97, v82
	s_waitcnt lgkmcnt(0)
	s_nop 1
	v_permlane16_swap_b32_e32 v82, v97
	v_add_f32_e32 v82, v82, v97
	v_mov_b32_e32 v97, v82
	s_waitcnt lgkmcnt(0)
	s_nop 1
	v_permlane32_swap_b32_e32 v82, v97
	v_add_f32_e32 v97, v82, v97
	v_cmp_ngt_f32_e32 vcc, v97, v93
	v_mov_b32_e32 v82, s13
	s_and_saveexec_b64 s[8:9], vcc
	s_cbranch_execz .LBB0_2884
	v_cmp_gt_f32_e32 vcc, v97, v95
	s_and_saveexec_b64 s[14:15], vcc
	v_mov_b32_e32 v96, s13
	v_mov_b32_e32 v95, v97
	s_or_b64 exec, exec, s[14:15]
	v_mov_b32_e32 v82, v83
	v_mov_b32_e32 v83, v96
	v_mov_b32_e32 v97, v93
	v_mov_b32_e32 v93, v95

.LBB0_2933:
	global_load_dword v1, v0, s[10:11] sc1
	s_waitcnt vmcnt(0)
	v_cmp_eq_u32_e32 vcc, 0, v1
	s_cbranch_vccnz .LBB0_2935
	s_mov_b64 s[18:19], -1
	s_mov_b64 s[22:23], -1
	s_branch .LBB0_2929
	s_nop 0
	s_nop 0
	s_nop 0
	s_nop 0
	s_nop 0
	s_nop 0
	s_nop 0
	s_nop 0
	s_nop 0
	s_nop 0
	s_nop 0
	s_nop 0
	s_nop 0
	s_nop 0
	s_nop 0
	s_nop 0
	s_nop 0
	s_nop 0
	s_nop 0
	s_nop 0
	s_nop 0
	s_nop 0
	s_nop 0
	s_nop 0
	s_nop 0
	s_nop 0
	s_nop 0
	s_nop 0
	s_nop 0
	s_nop 0
	s_nop 0
	s_nop 0
	s_nop 0
	s_nop 0
	s_nop 0
	s_nop 0
	s_nop 0
	s_nop 0
	s_nop 0
	s_nop 0
	s_nop 0
	s_nop 0
	s_nop 0
	s_nop 0
	s_nop 0
	s_nop 0
	s_nop 0
	s_nop 0
	s_nop 0
	s_nop 0
	s_nop 0
	s_nop 0
	s_nop 0
	s_nop 0
	s_nop 0
	s_nop 0
	s_nop 0
	s_nop 0
	s_nop 0
	s_nop 0

; template <int MODE, bool SB  > DI void norm_phase(const Params& P, const Frame& F, int L, const void* src_, const float* gain, bool combine) {
;     ...
;     for (int row = r_lo + F.wave; row < r_hi; row += NWAVES) {
;         f32x4 v[8];
; #pragma unroll
;         for (int j = 0; j < 8; ++j) { if constexpr (SB) v[j] = (f32x4){bflo(vb[j].x), bfhi(vb[j].x), bflo(vb[j].y), bfhi(vb[j].y)}; else v[j] = vn[j]; }
;         { const int rnx = (row + NWAVES < r_hi) ? row + NWAVES : row;
; #pragma unroll
;           for (int j = 0; j < 8; ++j) { if constexpr (SB) vb[j] = *(const u32x2*)(srcb + (size_t)rnx * D + 4 * F.lane + 256 * j); else vn[j] = *(const f32x4*)(src + (size_t)rnx * D + 4 * F.lane + 256 * j); } }
;         if (MODE == 3 && combine) {
;             const int* SLOT = (const int*)(ws + WS_SLOT); const float* TOPW = (const float*)(ws + WS_TOPW); const bf16* Y = (const bf16*)(ws + WS_T + T_YPERM);
;             const int s1 = SLOT[row * 2], s2 = SLOT[row * 2 + 1]; const float w1 = TOPW[row * 2], w2 = TOPW[row * 2 + 1];
;             u32x2 ya[8], yb[8];
; #pragma unroll
;             for (int j = 0; j < 8; ++j) { ya[j] = *(const u32x2*)(Y + (size_t)s1 * D + 4 * F.lane + 256 * j); yb[j] = *(const u32x2*)(Y + (size_t)s2 * D + 4 * F.lane + 256 * j); }
; #pragma unroll
;             for (int j = 0; j < 8; ++j) { const f32x4 y1 = (f32x4){bflo(ya[j].x), bfhi(ya[j].x), bflo(ya[j].y), bfhi(ya[j].y)}, y2 = (f32x4){bflo(yb[j].x), bfhi(yb[j].x), bflo(yb[j].y), bfhi(yb[j].y)};
.LBB0_3245:
	s_add_i32 s23, s4, 8
	s_cmp_lt_i32 s23, s3
	s_cselect_b64 s[14:15], -1, 0
	s_and_b64 s[24:25], s[14:15], exec
	s_cselect_b32 s4, s23, s4
	s_waitcnt vmcnt(7)
	v_lshlrev_b32_e32 v72, 16, v76
	v_and_b32_e32 v73, 0xffff0000, v76
	v_lshlrev_b32_e32 v74, 16, v77
	v_and_b32_e32 v75, 0xffff0000, v77
	v_lshl_add_u64 v[76:77], s[54:55], 0, v[42:43]
	s_ashr_i32 s7, s6, 31
	s_ashr_i32 s5, s4, 31
	v_add_co_u32_e32 v98, vcc, s20, v76
	s_lshl_b64 s[24:25], s[6:7], 2
	s_lshl_b64 s[4:5], s[4:5], 12
	s_waitcnt vmcnt(6)
	v_lshlrev_b32_e32 v68, 16, v78
	v_and_b32_e32 v69, 0xffff0000, v78
	v_lshlrev_b32_e32 v70, 16, v79
	v_and_b32_e32 v71, 0xffff0000, v79
	v_lshl_add_u64 v[78:79], s[54:55], 0, v[40:41]
	v_addc_co_u32_e32 v99, vcc, 0, v77, vcc
	v_lshl_add_u64 v[100:101], v[32:33], 0, s[4:5]
	s_add_u32 s4, s16, s24
	v_add_co_u32_e32 v92, vcc, s22, v78
	s_addc_u32 s5, s17, s25
	s_waitcnt vmcnt(0)
	v_lshlrev_b32_e32 v44, 16, v90
	v_and_b32_e32 v45, 0xffff0000, v90
	v_lshlrev_b32_e32 v46, 16, v91
	v_and_b32_e32 v47, 0xffff0000, v91
	v_lshlrev_b32_e32 v48, 16, v88
	v_and_b32_e32 v49, 0xffff0000, v88
	v_lshlrev_b32_e32 v50, 16, v89
	v_and_b32_e32 v51, 0xffff0000, v89
	v_lshlrev_b32_e32 v52, 16, v86
	v_and_b32_e32 v53, 0xffff0000, v86
	v_lshlrev_b32_e32 v54, 16, v87
	v_and_b32_e32 v55, 0xffff0000, v87
	v_lshlrev_b32_e32 v56, 16, v84
	v_and_b32_e32 v57, 0xffff0000, v84
	v_lshlrev_b32_e32 v58, 16, v85
	v_and_b32_e32 v59, 0xffff0000, v85
	v_lshlrev_b32_e32 v60, 16, v82
	v_and_b32_e32 v61, 0xffff0000, v82
	v_lshlrev_b32_e32 v62, 16, v83
	v_and_b32_e32 v63, 0xffff0000, v83
	v_lshlrev_b32_e32 v64, 16, v80
	v_and_b32_e32 v65, 0xffff0000, v80
	v_lshlrev_b32_e32 v66, 16, v81
	v_and_b32_e32 v67, 0xffff0000, v81
	v_addc_co_u32_e32 v93, vcc, 0, v79, vcc
	global_load_dwordx2 v[90:91], v[100:101], off
	global_load_dwordx2 v[88:89], v[100:101], off offset:512
	global_load_dwordx2 v[86:87], v[100:101], off offset:1024
	global_load_dwordx2 v[84:85], v[100:101], off offset:1536
	global_load_dwordx2 v[82:83], v[100:101], off offset:2048
	global_load_dwordx2 v[80:81], v[100:101], off offset:2560
	global_load_dwordx2 v[78:79], v[100:101], off offset:3072
	global_load_dwordx2 v[76:77], v[100:101], off offset:3584
	s_add_i32 s26, s6, 1
	global_load_dwordx2 v[100:101], v95, s[4:5]
	s_ashr_i32 s27, s26, 31
	s_add_u32 s4, s18, s24
	s_addc_u32 s5, s19, s25
	s_lshl_b64 s[24:25], s[26:27], 2
	global_load_dword v102, v95, s[4:5]
	s_add_u32 s4, s18, s24
	s_addc_u32 s5, s19, s25
	global_load_dword v104, v95, s[4:5]
	v_mov_b32_e32 v168, 0
	v_mov_b32_e32 v169, 0
	v_mov_b32_e32 v170, 0
	v_mov_b32_e32 v171, 0
	v_mov_b32_e32 v172, 0
	v_mov_b32_e32 v173, 0
	v_mov_b32_e32 v174, 0
	v_mov_b32_e32 v175, 0
	v_lshl_add_u64 v[40:41], v[40:41], 0, s[10:11]
	v_lshl_add_u64 v[42:43], v[42:43], 0, s[12:13]
	s_add_i32 s6, s6, 16
	s_waitcnt vmcnt(2)
	v_ashrrev_i32_e32 v107, 31, v100
	v_mov_b32_e32 v106, v100
	v_ashrrev_i32_e32 v109, 31, v101
	v_mov_b32_e32 v108, v101
	v_lshlrev_b64 v[100:101], 12, v[106:107]
	v_lshlrev_b64 v[106:107], 12, v[108:109]
	v_lshl_add_u64 v[100:101], v[34:35], 0, v[100:101]
	v_lshl_add_u64 v[106:107], v[34:35], 0, v[106:107]
	global_load_dwordx2 v[108:109], v[100:101], off
	global_load_dwordx2 v[110:111], v[106:107], off
	global_load_dwordx2 v[112:113], v[100:101], off offset:512
	global_load_dwordx2 v[114:115], v[106:107], off offset:512
	global_load_dwordx2 v[116:117], v[100:101], off offset:1024
	global_load_dwordx2 v[118:119], v[106:107], off offset:1024
	global_load_dwordx2 v[120:121], v[100:101], off offset:1536
	global_load_dwordx2 v[122:123], v[106:107], off offset:1536
	global_load_dwordx2 v[124:125], v[100:101], off offset:2048
	global_load_dwordx2 v[126:127], v[106:107], off offset:2048
	global_load_dwordx2 v[128:129], v[100:101], off offset:2560
	global_load_dwordx2 v[130:131], v[106:107], off offset:2560
	global_load_dwordx2 v[132:133], v[100:101], off offset:3072
	global_load_dwordx2 v[134:135], v[106:107], off offset:3072
	s_nop 0
	global_load_dwordx2 v[100:101], v[100:101], off offset:3584
	s_nop 0
	global_load_dwordx2 v[106:107], v[106:107], off offset:3584
	s_waitcnt vmcnt(15)
	v_lshlrev_b32_e32 v136, 16, v108
	v_and_b32_e32 v137, 0xffff0000, v108
	v_lshlrev_b32_e32 v108, 16, v109
	v_and_b32_e32 v109, 0xffff0000, v109
	s_waitcnt vmcnt(13)
	v_lshlrev_b32_e32 v140, 16, v112
	v_and_b32_e32 v141, 0xffff0000, v112
	v_lshlrev_b32_e32 v112, 16, v113
	v_and_b32_e32 v113, 0xffff0000, v113
	v_lshlrev_b32_e32 v138, 16, v110
	v_and_b32_e32 v139, 0xffff0000, v110
	v_lshlrev_b32_e32 v110, 16, v111
	v_and_b32_e32 v111, 0xffff0000, v111
	s_waitcnt vmcnt(12)
	v_lshlrev_b32_e32 v142, 16, v114
	v_and_b32_e32 v143, 0xffff0000, v114
	v_lshlrev_b32_e32 v114, 16, v115
	v_and_b32_e32 v115, 0xffff0000, v115
	s_waitcnt vmcnt(11)
	v_lshlrev_b32_e32 v144, 16, v116
	v_and_b32_e32 v145, 0xffff0000, v116
	v_lshlrev_b32_e32 v116, 16, v117
	v_and_b32_e32 v117, 0xffff0000, v117
	s_waitcnt vmcnt(9)
	v_lshlrev_b32_e32 v148, 16, v120
	v_and_b32_e32 v149, 0xffff0000, v120
	v_lshlrev_b32_e32 v120, 16, v121
	v_and_b32_e32 v121, 0xffff0000, v121
	s_waitcnt vmcnt(3)
	v_lshlrev_b32_e32 v160, 16, v132
	v_and_b32_e32 v161, 0xffff0000, v132
	v_lshlrev_b32_e32 v132, 16, v133
	v_and_b32_e32 v133, 0xffff0000, v133
	s_waitcnt vmcnt(1)
; DI unsigned pk2(float lo, float hi) { const f32x2 v = {lo, hi}; return __builtin_bit_cast(unsigned, __builtin_convertvector(v, bf16x2_t)); }
; template <int MODE, bool SB  > DI void norm_phase(const Params& P, const Frame& F, int L, const void* src_, const float* gain, bool combine) {
;     ...
;             for (int j = 0; j < 8; ++j) { const f32x4 y1 = (f32x4){bflo(ya[j].x), bfhi(ya[j].x), bflo(ya[j].y), bfhi(ya[j].y)}, y2 = (f32x4){bflo(yb[j].x), bfhi(yb[j].x), bflo(yb[j].y), bfhi(yb[j].y)};
;                 v[j] = v[j] + w1 * y1 + w2 * y2;
;                 const u32x2 hb = {pk2(v[j][0], v[j][1]), pk2(v[j][2], v[j][3])}; *(u32x2*)(const_cast<bf16*>(srcb) + (size_t)row * D + 4 * F.lane + 256 * j) = hb;
;                 v[j] = (f32x4){bflo(hb.x), bfhi(hb.x), bflo(hb.y), bfhi(hb.y)}; }
;         }
;         float ss = 0.f;
; #pragma unroll
;         for (int j = 0; j < 8; ++j) ss += (v[j][0] * v[j][0] + v[j][1] * v[j][1]) + (v[j][2] * v[j][2] + v[j][3] * v[j][3]);
	v_lshlrev_b32_e32 v164, 16, v100
	v_and_b32_e32 v165, 0xffff0000, v100
	v_pk_fma_f32 v[44:45], v[102:103], v[136:137], v[44:45] op_sel_hi:[0,1,1]
	v_pk_fma_f32 v[46:47], v[102:103], v[108:109], v[46:47] op_sel_hi:[0,1,1]
	v_pk_fma_f32 v[48:49], v[102:103], v[140:141], v[48:49] op_sel_hi:[0,1,1]
	v_pk_fma_f32 v[50:51], v[102:103], v[112:113], v[50:51] op_sel_hi:[0,1,1]
	v_lshlrev_b32_e32 v146, 16, v118
	v_and_b32_e32 v147, 0xffff0000, v118
	v_lshlrev_b32_e32 v118, 16, v119
	v_and_b32_e32 v119, 0xffff0000, v119
	v_lshlrev_b32_e32 v150, 16, v122
	v_and_b32_e32 v151, 0xffff0000, v122
	v_lshlrev_b32_e32 v122, 16, v123
	v_and_b32_e32 v123, 0xffff0000, v123
	v_lshlrev_b32_e32 v152, 16, v124
	v_and_b32_e32 v153, 0xffff0000, v124
	v_lshlrev_b32_e32 v156, 16, v128
	v_and_b32_e32 v157, 0xffff0000, v128
	v_lshlrev_b32_e32 v162, 16, v134
	v_and_b32_e32 v163, 0xffff0000, v134
	v_lshlrev_b32_e32 v134, 16, v135
	v_and_b32_e32 v135, 0xffff0000, v135
	s_waitcnt vmcnt(0)
	v_lshlrev_b32_e32 v166, 16, v106
	v_and_b32_e32 v167, 0xffff0000, v106
	v_pk_fma_f32 v[52:53], v[102:103], v[144:145], v[52:53] op_sel_hi:[0,1,1]
	v_pk_fma_f32 v[54:55], v[102:103], v[116:117], v[54:55] op_sel_hi:[0,1,1]
	v_pk_fma_f32 v[56:57], v[102:103], v[148:149], v[56:57] op_sel_hi:[0,1,1]
	v_pk_fma_f32 v[58:59], v[102:103], v[120:121], v[58:59] op_sel_hi:[0,1,1]
	v_pk_fma_f32 v[68:69], v[102:103], v[160:161], v[68:69] op_sel_hi:[0,1,1]
	v_pk_fma_f32 v[70:71], v[102:103], v[132:133], v[70:71] op_sel_hi:[0,1,1]
	v_pk_fma_f32 v[72:73], v[102:103], v[164:165], v[72:73] op_sel_hi:[0,1,1]
	v_pk_fma_f32 v[46:47], v[104:105], v[110:111], v[46:47] op_sel_hi:[0,1,1]
	v_pk_fma_f32 v[44:45], v[104:105], v[138:139], v[44:45] op_sel_hi:[0,1,1]
	v_pk_fma_f32 v[50:51], v[104:105], v[114:115], v[50:51] op_sel_hi:[0,1,1]
	v_pk_fma_f32 v[48:49], v[104:105], v[142:143], v[48:49] op_sel_hi:[0,1,1]
	v_lshlrev_b32_e32 v154, 16, v126
	v_and_b32_e32 v155, 0xffff0000, v126
	v_lshlrev_b32_e32 v158, 16, v130
	v_and_b32_e32 v159, 0xffff0000, v130
	v_pk_fma_f32 v[60:61], v[102:103], v[152:153], v[60:61] op_sel_hi:[0,1,1]
	v_pk_fma_f32 v[64:65], v[102:103], v[156:157], v[64:65] op_sel_hi:[0,1,1]
	v_pk_fma_f32 v[54:55], v[104:105], v[118:119], v[54:55] op_sel_hi:[0,1,1]
	v_pk_fma_f32 v[52:53], v[104:105], v[146:147], v[52:53] op_sel_hi:[0,1,1]
	v_pk_fma_f32 v[58:59], v[104:105], v[122:123], v[58:59] op_sel_hi:[0,1,1]
	v_pk_fma_f32 v[56:57], v[104:105], v[150:151], v[56:57] op_sel_hi:[0,1,1]
	v_pk_fma_f32 v[70:71], v[104:105], v[134:135], v[70:71] op_sel_hi:[0,1,1]
	v_pk_fma_f32 v[68:69], v[104:105], v[162:163], v[68:69] op_sel_hi:[0,1,1]
	v_pk_fma_f32 v[72:73], v[104:105], v[166:167], v[72:73] op_sel_hi:[0,1,1]
	v_cvt_pk_bf16_f32 v44, v44, v45
	v_cvt_pk_bf16_f32 v45, v46, v47
	v_cvt_pk_bf16_f32 v46, v48, v49
	v_cvt_pk_bf16_f32 v47, v50, v51
	v_lshlrev_b32_e32 v124, 16, v125
	v_and_b32_e32 v125, 0xffff0000, v125
	v_lshlrev_b32_e32 v128, 16, v129
	v_and_b32_e32 v129, 0xffff0000, v129
	v_lshlrev_b32_e32 v100, 16, v101
	v_and_b32_e32 v101, 0xffff0000, v101
	v_pk_fma_f32 v[60:61], v[104:105], v[154:155], v[60:61] op_sel_hi:[0,1,1]
	v_pk_fma_f32 v[64:65], v[104:105], v[158:159], v[64:65] op_sel_hi:[0,1,1]
	v_cvt_pk_bf16_f32 v48, v52, v53
	v_cvt_pk_bf16_f32 v49, v54, v55
	v_cvt_pk_bf16_f32 v50, v56, v57
	v_cvt_pk_bf16_f32 v51, v58, v59
	v_cvt_pk_bf16_f32 v56, v68, v69
	v_cvt_pk_bf16_f32 v57, v70, v71
	v_cvt_pk_bf16_f32 v58, v72, v73
	global_store_dwordx2 v[98:99], v[44:45], off
	global_store_dwordx2 v[98:99], v[46:47], off offset:512
	global_store_dwordx2 v[98:99], v[48:49], off offset:1024
	global_store_dwordx2 v[98:99], v[50:51], off offset:1536
	v_lshlrev_b32_e32 v68, 16, v44
	v_and_b32_e32 v69, 0xffff0000, v44
	v_lshlrev_b32_e32 v44, 16, v45
	v_and_b32_e32 v45, 0xffff0000, v45
	v_lshlrev_b32_e32 v71, 16, v47
	v_lshlrev_b32_e32 v70, 16, v46
	v_and_b32_e32 v47, 0xffff0000, v47
	v_and_b32_e32 v46, 0xffff0000, v46
	v_lshlrev_b32_e32 v126, 16, v127
	v_and_b32_e32 v127, 0xffff0000, v127
	v_lshlrev_b32_e32 v130, 16, v131
	v_and_b32_e32 v131, 0xffff0000, v131
	v_lshlrev_b32_e32 v106, 16, v107
	v_and_b32_e32 v107, 0xffff0000, v107
	v_pk_fma_f32 v[62:63], v[102:103], v[124:125], v[62:63] op_sel_hi:[0,1,1]
	v_pk_fma_f32 v[66:67], v[102:103], v[128:129], v[66:67] op_sel_hi:[0,1,1]
	v_pk_fma_f32 v[74:75], v[102:103], v[100:101], v[74:75] op_sel_hi:[0,1,1]
	v_cvt_pk_bf16_f32 v52, v60, v61
	v_cvt_pk_bf16_f32 v54, v64, v65
	v_lshlrev_b32_e32 v61, 16, v50
	v_lshlrev_b32_e32 v65, 16, v58
	v_and_b32_e32 v73, 0xffff0000, v48
	v_mul_f32_e32 v60, v45, v45
	v_pk_mul_f32 v[102:103], v[46:47], v[46:47]
	v_mul_f32_e32 v64, v69, v69
	v_pk_fma_f32 v[62:63], v[104:105], v[126:127], v[62:63] op_sel_hi:[0,1,1]
	v_pk_fma_f32 v[66:67], v[104:105], v[130:131], v[66:67] op_sel_hi:[0,1,1]
	v_pk_fma_f32 v[74:75], v[104:105], v[106:107], v[74:75] op_sel_hi:[0,1,1]
	v_lshlrev_b32_e32 v72, 16, v48
	v_lshlrev_b32_e32 v48, 16, v49
	v_and_b32_e32 v49, 0xffff0000, v49
	v_mov_b32_e32 v105, v61
	v_mul_f32_e32 v104, v73, v73
	v_mov_b32_e32 v116, v70
	v_mov_b32_e32 v117, v46
	v_mov_b32_e32 v46, v71
	v_pk_fma_f32 v[122:123], v[44:45], v[44:45], v[60:61] op_sel_hi:[1,1,0]
	v_pk_fma_f32 v[70:71], v[70:71], v[70:71], v[102:103]
	v_pk_fma_f32 v[102:103], v[68:69], v[68:69], v[64:65] op_sel_hi:[1,1,0]
	v_cvt_pk_bf16_f32 v53, v62, v63
	v_and_b32_e32 v63, 0xffff0000, v50
	v_lshlrev_b32_e32 v50, 16, v51
	v_and_b32_e32 v51, 0xffff0000, v51
	v_mul_f32_e32 v106, v49, v49
	v_mov_b32_e32 v107, v65
	v_pk_fma_f32 v[124:125], v[72:73], v[72:73], v[104:105] op_sel_hi:[1,1,0]
	v_mov_b32_e32 v60, v102
	v_mov_b32_e32 v104, v122
	v_mul_f32_e32 v113, v63, v63
	v_mul_f32_e32 v115, v50, v50
; DI unsigned pk2(float lo, float hi) { const f32x2 v = {lo, hi}; return __builtin_bit_cast(unsigned, __builtin_convertvector(v, bf16x2_t)); }
; DI float wave_sum(float v) { v += shx<1>(v); v += shx<2>(v); v += shx<4>(v); v += shx<8>(v); v += shx<16>(v); v += shx<32>(v); return v; }
; template <int MODE, bool SB  > DI void norm_phase(const Params& P, const Frame& F, int L, const void* src_, const float* gain, bool combine) {
;     ...
;                 const u32x2 hb = {pk2(v[j][0], v[j][1]), pk2(v[j][2], v[j][3])}; *(u32x2*)(const_cast<bf16*>(srcb) + (size_t)row * D + 4 * F.lane + 256 * j) = hb;
;                 v[j] = (f32x4){bflo(hb.x), bfhi(hb.x), bflo(hb.y), bfhi(hb.y)}; }
;         }
;         float ss = 0.f;
; #pragma unroll
;         for (int j = 0; j < 8; ++j) ss += (v[j][0] * v[j][0] + v[j][1] * v[j][1]) + (v[j][2] * v[j][2] + v[j][3] * v[j][3]);
;         const float rstd = 1.0f / sqrtf(wave_sum(ss) * (1.0f / D) + EPS);
	v_mul_f32_e32 v128, v51, v51
	v_mov_b32_e32 v62, v61
	v_pk_fma_f32 v[126:127], v[48:49], v[48:49], v[106:107] op_sel_hi:[1,1,0]
	v_pk_add_f32 v[102:103], v[102:103], v[122:123]
	v_pk_add_f32 v[70:71], v[70:71], v[70:71] op_sel:[0,1] op_sel_hi:[1,0]
	v_pk_mul_f32 v[60:61], v[60:61], v[104:105]
	v_cvt_pk_bf16_f32 v55, v66, v67
	v_cvt_pk_bf16_f32 v59, v74, v75
	global_store_dwordx2 v[98:99], v[52:53], off offset:2048
	global_store_dwordx2 v[98:99], v[54:55], off offset:2560
	global_store_dwordx2 v[98:99], v[56:57], off offset:3072
	global_store_dwordx2 v[98:99], v[58:59], off offset:3584
	v_lshlrev_b32_e32 v75, 16, v53
	v_lshlrev_b32_e32 v74, 16, v52
	v_and_b32_e32 v53, 0xffff0000, v53
	v_and_b32_e32 v52, 0xffff0000, v52
	v_mov_b32_e32 v125, v115
	v_mov_b32_e32 v127, v128
	v_mov_b32_e32 v71, v113
	v_mov_b32_e32 v103, v61
	v_pk_mul_f32 v[108:109], v[52:53], v[52:53]
	v_pk_add_f32 v[104:105], v[124:125], v[126:127]
	v_pk_add_f32 v[60:61], v[102:103], v[70:71]
	v_lshlrev_b32_e32 v99, 16, v55
	v_lshlrev_b32_e32 v98, 16, v54
	v_and_b32_e32 v55, 0xffff0000, v55
	v_and_b32_e32 v54, 0xffff0000, v54
	v_mov_b32_e32 v118, v74
	v_mov_b32_e32 v119, v52
	v_mov_b32_e32 v52, v75
	v_pk_fma_f32 v[74:75], v[74:75], v[74:75], v[108:109]
	v_pk_add_f32 v[60:61], v[60:61], v[104:105]
	v_lshlrev_b32_e32 v100, 16, v56
	v_and_b32_e32 v101, 0xffff0000, v56
	v_lshlrev_b32_e32 v56, 16, v57
	v_and_b32_e32 v57, 0xffff0000, v57
	v_pk_mul_f32 v[110:111], v[54:55], v[54:55]
	v_pk_add_f32 v[74:75], v[74:75], v[74:75] op_sel:[0,1] op_sel_hi:[1,0]
	v_pk_add_f32 v[60:61], v[60:61], v[60:61] op_sel:[0,1] op_sel_hi:[1,0]
	v_and_b32_e32 v67, 0xffff0000, v58
	v_lshlrev_b32_e32 v58, 16, v59
	v_and_b32_e32 v59, 0xffff0000, v59
	v_mul_f32_e32 v112, v101, v101
	v_mul_f32_e32 v114, v57, v57
	v_mov_b32_e32 v120, v98
	v_mov_b32_e32 v121, v54
	v_mov_b32_e32 v54, v99
	v_pk_fma_f32 v[98:99], v[98:99], v[98:99], v[110:111]
	v_mov_b32_e32 v106, v74
	v_mov_b32_e32 v64, v60
	v_mul_f32_e32 v129, v67, v67
	v_mul_f32_e32 v130, v58, v58
	v_mul_f32_e32 v131, v59, v59
	v_mov_b32_e32 v66, v65
	v_pk_fma_f32 v[108:109], v[100:101], v[100:101], v[112:113] op_sel_hi:[1,1,0]
	v_pk_fma_f32 v[110:111], v[56:57], v[56:57], v[114:115] op_sel_hi:[1,1,0]
	v_pk_add_f32 v[98:99], v[98:99], v[98:99] op_sel:[0,1] op_sel_hi:[1,0]
	v_pk_add_f32 v[60:61], v[60:61], v[74:75]
	v_pk_mul_f32 v[64:65], v[64:65], v[106:107]
	v_mov_b32_e32 v109, v130
	v_mov_b32_e32 v111, v131
	v_mov_b32_e32 v99, v129
	v_mov_b32_e32 v61, v65
	v_pk_add_f32 v[108:109], v[108:109], v[110:111]
	v_pk_add_f32 v[60:61], v[60:61], v[98:99]
	s_nop 0
	v_pk_add_f32 v[60:61], v[60:61], v[108:109]
	s_nop 0
	v_add_f32_e32 v60, v60, v61
	s_nop 1
	v_add_f32_dpp v60, v60, v60 quad_perm:[1,0,3,2] row_mask:0xf bank_mask:0xf bound_ctrl:1
	s_nop 1
	v_add_f32_dpp v60, v60, v60 quad_perm:[2,3,0,1] row_mask:0xf bank_mask:0xf bound_ctrl:1
	ds_swizzle_b32 v61, v60 offset:swizzle(SWAP,4)
	s_waitcnt lgkmcnt(0)
	v_add_f32_e32 v60, v60, v61
	ds_swizzle_b32 v61, v60 offset:swizzle(SWAP,8)
	s_waitcnt lgkmcnt(0)
	v_add_f32_e32 v60, v60, v61
	v_mov_b32_e32 v61, v60
	s_waitcnt lgkmcnt(0)
	s_nop 1
	v_permlane16_swap_b32_e32 v60, v61
	v_add_f32_e32 v60, v60, v61
	v_mov_b32_e32 v61, v60
	s_waitcnt lgkmcnt(0)
; DI unsigned pk2(float lo, float hi) { const f32x2 v = {lo, hi}; return __builtin_bit_cast(unsigned, __builtin_convertvector(v, bf16x2_t)); }
; DI unsigned pk4_fp8(float a, float b, float c, float d) { unsigned w = 0u; w = __builtin_amdgcn_cvt_pk_fp8_f32(a, b, w, false); w = __builtin_amdgcn_cvt_pk_fp8_f32(c, d, w, true); return w; }
; DI float wave_sum(float v) { v += shx<1>(v); v += shx<2>(v); v += shx<4>(v); v += shx<8>(v); v += shx<16>(v); v += shx<32>(v); return v; }
; template <int MODE, bool SB  > DI void norm_phase(const Params& P, const Frame& F, int L, const void* src_, const float* gain, bool combine) {
;     ...
;         const float rstd = 1.0f / sqrtf(wave_sum(ss) * (1.0f / D) + EPS);
; #pragma unroll
;         for (int j = 0; j < 8; ++j) v[j] = v[j] * rstd * g[j];
;         if (MODE == 4) {
; #pragma unroll
;             for (int j = 0; j < 8; ++j) *(f32x4*)(P.out + (size_t)row * D + 4 * F.lane + 256 * j) = v[j];
;         } else if (MODE == 0 || MODE == 2 || (MODE == 3 && L == 1)) {
;             unsigned* o4 = (unsigned*)((unsigned char*)HN + (size_t)row * D) + F.lane; const float hs = (float)(1 << LS_HN);
; #pragma unroll
;             for (int j = 0; j < 8; ++j) o4[64 * j] = pk4_fp8(v[j][0] * hs, v[j][1] * hs, v[j][2] * hs, v[j][3] * hs);
;     ...
;         if (MODE == 3) { const f32x4 pv = *(const f32x4*)(P.in[I_P] + ((size_t)L * M + row) * PLE + 4 * F.lane);
;             *((unsigned long long*)((bf16*)(ws + WS_T + T_PB) + (size_t)row * PLE) + F.lane) = (unsigned long long)pk2(pv[0], pv[1]) | ((unsigned long long)pk2(pv[2], pv[3]) << 32); }
	s_nop 1
	v_permlane32_swap_b32_e32 v60, v61
	v_add_f32_e32 v60, v60, v61
	v_fmamk_f32 v60, v60, 0x3a000000, v96
	v_mul_f32_e32 v61, 0x4f800000, v60
	v_cmp_gt_f32_e32 vcc, s21, v60
	s_nop 1
	v_cndmask_b32_e32 v60, v60, v61, vcc
	v_sqrt_f32_e32 v61, v60
	s_nop 0
	v_add_u32_e32 v64, -1, v61
	v_add_u32_e32 v65, 1, v61
	v_fma_f32 v70, -v64, v61, v60
	v_fma_f32 v71, -v65, v61, v60
	v_cmp_ge_f32_e64 s[4:5], 0, v70
	s_nop 1
	v_cndmask_b32_e64 v61, v61, v64, s[4:5]
	v_cmp_lt_f32_e64 s[4:5], 0, v71
	s_nop 1
	v_cndmask_b32_e64 v61, v61, v65, s[4:5]
	v_mul_f32_e32 v64, 0x37800000, v61
	v_cndmask_b32_e32 v61, v61, v64, vcc
	v_cmp_class_f32_e32 vcc, v60, v97
	s_nop 1
	v_cndmask_b32_e32 v60, v61, v60, vcc
	v_div_scale_f32 v61, s[4:5], v60, v60, 1.0
	v_rcp_f32_e32 v65, v61
	v_div_scale_f32 v64, vcc, 1.0, v60, 1.0
	s_mov_b32 s4, s23
	v_fma_f32 v70, -v61, v65, 1.0
	v_fmac_f32_e32 v65, v70, v65
	v_mul_f32_e32 v70, v64, v65
	v_fma_f32 v71, -v61, v70, v64
	v_fmac_f32_e32 v70, v71, v65
	v_fma_f32 v61, -v61, v70, v64
	v_div_fmas_f32 v61, v61, v65, v70
	v_div_fixup_f32 v60, v61, v60, 1.0
	v_pk_mul_f32 v[64:65], v[60:61], v[68:69] op_sel_hi:[0,1]
	v_pk_mul_f32 v[44:45], v[60:61], v[44:45] op_sel_hi:[0,1]
	v_pk_mul_f32 v[68:69], v[60:61], v[116:117] op_sel_hi:[0,1]
	v_pk_mul_f32 v[46:47], v[60:61], v[46:47] op_sel_hi:[0,1]
	v_pk_mul_f32 v[70:71], v[60:61], v[72:73] op_sel_hi:[0,1]
	v_pk_mul_f32 v[48:49], v[60:61], v[48:49] op_sel_hi:[0,1]
	v_pk_mul_f32 v[62:63], v[62:63], v[60:61] op_sel_hi:[1,0]
	v_pk_mul_f32 v[50:51], v[50:51], v[60:61] op_sel_hi:[1,0]
	v_pk_mul_f32 v[72:73], v[60:61], v[118:119] op_sel_hi:[0,1]
	v_pk_mul_f32 v[52:53], v[60:61], v[52:53] op_sel_hi:[0,1]
	v_pk_mul_f32 v[74:75], v[60:61], v[120:121] op_sel_hi:[0,1]
	v_pk_mul_f32 v[54:55], v[60:61], v[54:55] op_sel_hi:[0,1]
	v_pk_mul_f32 v[98:99], v[60:61], v[100:101] op_sel_hi:[0,1]
	v_pk_mul_f32 v[56:57], v[60:61], v[56:57] op_sel_hi:[0,1]
	v_pk_mul_f32 v[66:67], v[66:67], v[60:61] op_sel_hi:[1,0]
	v_pk_mul_f32 v[58:59], v[58:59], v[60:61] op_sel_hi:[1,0]
	v_pk_mul_f32 v[60:61], v[8:9], v[64:65]
	v_pk_mul_f32 v[64:65], v[0:1], v[68:69]
	v_mul_f32_e32 v60, 4.0, v60
	v_mul_f32_e32 v61, 4.0, v61
	v_pk_mul_f32 v[68:69], v[4:5], v[70:71]
	v_mul_f32_e32 v64, 4.0, v64
	v_mul_f32_e32 v65, 4.0, v65
	v_cvt_pk_fp8_f32 v168, v60, v61
	v_pk_mul_f32 v[62:63], v[12:13], v[62:63]
	v_mul_f32_e32 v68, 4.0, v68
	v_mul_f32_e32 v69, 4.0, v69
	v_cvt_pk_fp8_f32 v169, v64, v65
	v_pk_mul_f32 v[44:45], v[10:11], v[44:45]
	v_pk_mul_f32 v[70:71], v[16:17], v[72:73]
	v_pk_mul_f32 v[72:73], v[20:21], v[74:75]
	v_pk_mul_f32 v[74:75], v[24:25], v[98:99]
	v_pk_mul_f32 v[66:67], v[28:29], v[66:67]
	v_mul_f32_e32 v62, 4.0, v62
	v_mul_f32_e32 v63, 4.0, v63
	v_cvt_pk_fp8_f32 v170, v68, v69
	v_pk_mul_f32 v[46:47], v[2:3], v[46:47]
	v_mul_f32_e32 v44, 4.0, v44
	v_mul_f32_e32 v45, 4.0, v45
	v_mul_f32_e32 v70, 4.0, v70
	v_mul_f32_e32 v71, 4.0, v71
	v_mul_f32_e32 v72, 4.0, v72
	v_mul_f32_e32 v73, 4.0, v73
	v_mul_f32_e32 v74, 4.0, v74
	v_mul_f32_e32 v75, 4.0, v75
	v_mul_f32_e32 v66, 4.0, v66
	v_mul_f32_e32 v67, 4.0, v67
	v_cvt_pk_fp8_f32 v171, v62, v63
	v_pk_mul_f32 v[48:49], v[6:7], v[48:49]
	v_mul_f32_e32 v46, 4.0, v46
	v_mul_f32_e32 v47, 4.0, v47
	v_cvt_pk_fp8_f32 v172, v70, v71
	v_cvt_pk_fp8_f32 v173, v72, v73
	v_cvt_pk_fp8_f32 v174, v74, v75
	v_cvt_pk_fp8_f32 v175, v66, v67
	v_cvt_pk_fp8_f32 v168, v44, v45 op_sel:[0,0,1]
	v_pk_mul_f32 v[50:51], v[14:15], v[50:51]
	v_mul_f32_e32 v48, 4.0, v48
	v_mul_f32_e32 v49, 4.0, v49
	v_cvt_pk_fp8_f32 v169, v46, v47 op_sel:[0,0,1]
	v_pk_mul_f32 v[52:53], v[18:19], v[52:53]
	v_pk_mul_f32 v[54:55], v[22:23], v[54:55]
	v_pk_mul_f32 v[56:57], v[26:27], v[56:57]
	v_pk_mul_f32 v[58:59], v[30:31], v[58:59]
	v_mul_f32_e32 v50, 4.0, v50
	v_mul_f32_e32 v51, 4.0, v51
	v_cvt_pk_fp8_f32 v170, v48, v49 op_sel:[0,0,1]
	v_mul_f32_e32 v52, 4.0, v52
	v_mul_f32_e32 v53, 4.0, v53
	v_mul_f32_e32 v54, 4.0, v54
	v_mul_f32_e32 v55, 4.0, v55
	v_mul_f32_e32 v56, 4.0, v56
	v_mul_f32_e32 v57, 4.0, v57
	v_mul_f32_e32 v58, 4.0, v58
	v_mul_f32_e32 v59, 4.0, v59
	v_cvt_pk_fp8_f32 v171, v50, v51 op_sel:[0,0,1]
	v_cvt_pk_fp8_f32 v172, v52, v53 op_sel:[0,0,1]
	v_cvt_pk_fp8_f32 v173, v54, v55 op_sel:[0,0,1]
	v_cvt_pk_fp8_f32 v174, v56, v57 op_sel:[0,0,1]
	v_cvt_pk_fp8_f32 v175, v58, v59 op_sel:[0,0,1]
	global_store_dword v[92:93], v168, off
	global_store_dword v[92:93], v169, off offset:256
	global_store_dword v[92:93], v170, off offset:512
	global_store_dword v[92:93], v171, off offset:768
	global_store_dword v[92:93], v172, off offset:1024
	global_store_dword v[92:93], v173, off offset:1280
	global_store_dword v[92:93], v174, off offset:1536
	global_store_dword v[92:93], v175, off offset:1792
	global_load_dwordx4 v[44:47], v[38:39], off
	v_lshl_add_u64 v[48:49], s[54:55], 0, v[36:37]
	v_lshl_add_u64 v[36:37], v[36:37], 0, s[8:9]
	s_and_b64 vcc, s[14:15], exec
	v_lshl_add_u64 v[38:39], v[38:39], 0, s[0:1]
	s_waitcnt vmcnt(0)
	v_cvt_pk_bf16_f32 v44, v44, v45
	v_cvt_pk_bf16_f32 v45, v46, v47
	global_store_dwordx2 v[48:49], v[44:45], off
	s_cbranch_vccnz .LBB0_3245

.LBB0_3291:
	s_cmp_lt_u32 s3, 0x40001
	s_mov_b64 s[18:19], 0
	s_cselect_b64 s[20:21], -1, 0
	s_mov_b64 s[22:23], -1
	s_and_b64 vcc, exec, s[20:21]
	s_cbranch_vccnz .LBB0_3288
	s_branch .LBB0_3285
	s_nop 0
	s_nop 0
	s_nop 0
	s_nop 0
	s_nop 0
	s_nop 0
	s_nop 0
	s_nop 0
	s_nop 0
	s_nop 0
	s_nop 0
	s_nop 0
	s_nop 0
	s_nop 0
	s_nop 0
	s_nop 0
	s_nop 0
	s_nop 0
	s_nop 0
	s_nop 0
	s_nop 0
	s_nop 0
	s_nop 0
	s_nop 0
	s_nop 0
	s_nop 0
	s_nop 0
	s_nop 0
	s_nop 0
	s_nop 0
	s_nop 0
	s_nop 0
	s_nop 0
	s_nop 0
	s_nop 0
	s_nop 0
	s_nop 0
	s_nop 0
	s_nop 0
	s_nop 0
	s_nop 0
	s_nop 0
	s_nop 0
	s_nop 0
	s_nop 0
	s_nop 0
	s_nop 0
	s_nop 0
	s_nop 0
	s_nop 0
	s_nop 0
	s_nop 0
	s_nop 0
	s_nop 0
	s_nop 0
	s_nop 0
	s_nop 0
	s_nop 0
	s_nop 0
	s_nop 0
	s_nop 0
	s_nop 0

; DI unsigned pk2(float lo, float hi) { const f32x2 v = {lo, hi}; return __builtin_bit_cast(unsigned, __builtin_convertvector(v, bf16x2_t)); }
; DI float wave_sum(float v) { v += shx<1>(v); v += shx<2>(v); v += shx<4>(v); v += shx<8>(v); v += shx<16>(v); v += shx<32>(v); return v; }
; template <int MODE, bool SB  > DI void norm_phase(const Params& P, const Frame& F, int L, const void* src_, const float* gain, bool combine) {
;     ...
;     for (int row = r_lo + F.wave; row < r_hi; row += NWAVES) {
;         f32x4 v[8];
; #pragma unroll
;         for (int j = 0; j < 8; ++j) { if constexpr (SB) v[j] = (f32x4){bflo(vb[j].x), bfhi(vb[j].x), bflo(vb[j].y), bfhi(vb[j].y)}; else v[j] = vn[j]; }
;         { const int rnx = (row + NWAVES < r_hi) ? row + NWAVES : row;
; #pragma unroll
;           for (int j = 0; j < 8; ++j) { if constexpr (SB) vb[j] = *(const u32x2*)(srcb + (size_t)rnx * D + 4 * F.lane + 256 * j); else vn[j] = *(const f32x4*)(src + (size_t)rnx * D + 4 * F.lane + 256 * j); } }
;         if (MODE == 3 && combine) {
;             const int* SLOT = (const int*)(ws + WS_SLOT); const float* TOPW = (const float*)(ws + WS_TOPW); const bf16* Y = (const bf16*)(ws + WS_T + T_YPERM);
;             const int s1 = SLOT[row * 2], s2 = SLOT[row * 2 + 1]; const float w1 = TOPW[row * 2], w2 = TOPW[row * 2 + 1];
;             u32x2 ya[8], yb[8];
; #pragma unroll
;             for (int j = 0; j < 8; ++j) { ya[j] = *(const u32x2*)(Y + (size_t)s1 * D + 4 * F.lane + 256 * j); yb[j] = *(const u32x2*)(Y + (size_t)s2 * D + 4 * F.lane + 256 * j); }
; #pragma unroll
;             for (int j = 0; j < 8; ++j) { const f32x4 y1 = (f32x4){bflo(ya[j].x), bfhi(ya[j].x), bflo(ya[j].y), bfhi(ya[j].y)}, y2 = (f32x4){bflo(yb[j].x), bfhi(yb[j].x), bflo(yb[j].y), bfhi(yb[j].y)};
;                 v[j] = v[j] + w1 * y1 + w2 * y2;
;                 const u32x2 hb = {pk2(v[j][0], v[j][1]), pk2(v[j][2], v[j][3])}; *(u32x2*)(const_cast<bf16*>(srcb) + (size_t)row * D + 4 * F.lane + 256 * j) = hb;
;                 v[j] = (f32x4){bflo(hb.x), bfhi(hb.x), bflo(hb.y), bfhi(hb.y)}; }
;         }
;         float ss = 0.f;
; #pragma unroll
;         for (int j = 0; j < 8; ++j) ss += (v[j][0] * v[j][0] + v[j][1] * v[j][1]) + (v[j][2] * v[j][2] + v[j][3] * v[j][3]);
;         const float rstd = 1.0f / sqrtf(wave_sum(ss) * (1.0f / D) + EPS);
.LBB0_3407:
	s_add_i32 s2, s6, 8
	s_waitcnt vmcnt(3)
	v_lshlrev_b32_e32 v42, 16, v40
	v_and_b32_e32 v43, 0xffff0000, v40
	v_lshlrev_b32_e32 v40, 16, v62
	v_and_b32_e32 v67, 0xffff0000, v62
	v_lshlrev_b32_e32 v46, 16, v63
	v_and_b32_e32 v47, 0xffff0000, v63
	v_lshlrev_b32_e32 v38, 16, v36
	v_and_b32_e32 v39, 0xffff0000, v36
	v_lshlrev_b32_e32 v36, 16, v60
	v_and_b32_e32 v89, 0xffff0000, v60
	v_lshlrev_b32_e32 v44, 16, v61
	v_and_b32_e32 v45, 0xffff0000, v61
	s_waitcnt vmcnt(0)
	v_and_b32_e32 v61, 0xffff0000, v58
	v_and_b32_e32 v60, 0xffff0000, v54
	v_and_b32_e32 v63, 0xffff0000, v59
	v_and_b32_e32 v62, 0xffff0000, v55
	s_cmp_lt_i32 s2, s8
	v_lshlrev_b32_e32 v49, 16, v58
	v_lshlrev_b32_e32 v48, 16, v54
	v_lshlrev_b32_e32 v51, 16, v59
	v_lshlrev_b32_e32 v50, 16, v55
	v_lshlrev_b32_e32 v69, 16, v53
	v_lshlrev_b32_e32 v68, 16, v52
	v_and_b32_e32 v53, 0xffff0000, v53
	v_and_b32_e32 v52, 0xffff0000, v52
	v_pk_mul_f32 v[72:73], v[60:61], v[60:61]
	v_pk_mul_f32 v[74:75], v[62:63], v[62:63]
	s_cselect_b64 s[4:5], -1, 0
	v_lshlrev_b32_e32 v54, 16, v41
	v_pk_mul_f32 v[76:77], v[52:53], v[52:53]
	v_pk_fma_f32 v[72:73], v[48:49], v[48:49], v[72:73]
	v_pk_fma_f32 v[74:75], v[50:51], v[50:51], v[74:75]
	s_and_b64 s[4:5], s[4:5], exec
	v_and_b32_e32 v55, 0xffff0000, v41
	v_lshlrev_b32_e32 v71, 16, v57
	v_lshlrev_b32_e32 v70, 16, v56
	v_and_b32_e32 v57, 0xffff0000, v57
	v_and_b32_e32 v56, 0xffff0000, v56
	v_lshlrev_b32_e32 v58, 16, v37
	v_mul_f32_e32 v41, v42, v42
	v_mul_f32_e32 v79, v43, v43
	v_mul_f32_e32 v80, v54, v54
	v_mov_b32_e32 v78, v40
	v_mov_b32_e32 v92, v49
	v_mov_b32_e32 v93, v61
	v_mov_b32_e32 v96, v68
	v_mov_b32_e32 v97, v52
	v_mov_b32_e32 v52, v69
	v_pk_fma_f32 v[68:69], v[68:69], v[68:69], v[76:77]
	v_mov_b32_e32 v49, v60
	v_pk_add_f32 v[60:61], v[72:73], v[74:75]
	s_cselect_b32 s10, s2, s6
	v_and_b32_e32 v59, 0xffff0000, v37
	v_pk_mul_f32 v[84:85], v[56:57], v[56:57]
	v_mul_f32_e32 v37, v38, v38
	v_mul_f32_e32 v87, v39, v39
	v_mul_f32_e32 v88, v58, v58
	v_mov_b32_e32 v86, v36
	v_mov_b32_e32 v94, v51
	v_mov_b32_e32 v95, v63
	v_pk_fma_f32 v[76:77], v[54:55], v[54:55], v[80:81] op_sel_hi:[1,1,0]
	v_pk_add_f32 v[78:79], v[40:41], v[78:79]
	v_mov_b32_e32 v51, v62
	v_pk_add_f32 v[62:63], v[68:69], v[68:69] op_sel_hi:[0,1]
	v_pk_add_f32 v[60:61], v[60:61], v[60:61] op_sel_hi:[0,1]
	s_ashr_i32 s11, s10, 31
	v_mul_f32_e32 v82, v40, v40
	v_mov_b32_e32 v98, v70
	v_mov_b32_e32 v99, v56
	v_mov_b32_e32 v56, v71
	v_pk_fma_f32 v[70:71], v[70:71], v[70:71], v[84:85]
	v_pk_fma_f32 v[80:81], v[58:59], v[58:59], v[88:89] op_sel_hi:[1,1,0]
	v_pk_add_f32 v[84:85], v[36:37], v[86:87]
	v_mul_f32_e32 v76, v67, v67
	v_mov_b32_e32 v83, v79
	v_mul_f32_e32 v62, v46, v46
	s_mov_b32 s6, s2
	v_mul_f32_e32 v60, v47, v47
	s_lshl_b64 s[2:3], s[10:11], 12
	v_mul_f32_e32 v90, v36, v36
	v_pk_add_f32 v[68:69], v[70:71], v[70:71] op_sel_hi:[0,1]
	v_mul_f32_e32 v80, v89, v89
	v_mov_b32_e32 v91, v85
	v_pk_add_f32 v[70:71], v[82:83], v[76:77]
	v_pk_add_f32 v[60:61], v[62:63], v[60:61]
	v_lshl_add_u64 v[74:75], v[32:33], 0, s[2:3]
	v_pk_add_f32 v[72:73], v[90:91], v[80:81]
	v_pk_add_f32 v[70:71], v[70:71], v[60:61]
	global_load_dwordx2 v[76:77], v[74:75], off
	global_load_dwordx2 v[78:79], v[74:75], off offset:512
	global_load_dwordx2 v[80:81], v[74:75], off offset:1024
	global_load_dwordx2 v[82:83], v[74:75], off offset:1536
	global_load_dwordx2 v[62:63], v[74:75], off offset:2048
	global_load_dwordx2 v[84:85], v[74:75], off offset:2560
	global_load_dwordx2 v[86:87], v[74:75], off offset:3072
	global_load_dwordx2 v[60:61], v[74:75], off offset:3584
	v_pk_add_f32 v[70:71], v[70:71], v[70:71] op_sel_hi:[0,1]
	v_mul_f32_e32 v68, v44, v44
	v_mul_f32_e32 v70, v45, v45
	v_pk_add_f32 v[68:69], v[68:69], v[70:71]
	v_mov_b32_e32 v41, v67
	v_pk_add_f32 v[68:69], v[72:73], v[68:69]
	v_mov_b32_e32 v37, v89
	v_add_f32_e32 v67, v68, v69
	s_nop 1
	v_add_f32_dpp v67, v67, v67 quad_perm:[1,0,3,2] row_mask:0xf bank_mask:0xf bound_ctrl:1
	s_nop 1
	v_add_f32_dpp v67, v67, v67 quad_perm:[2,3,0,1] row_mask:0xf bank_mask:0xf bound_ctrl:1
	ds_swizzle_b32 v68, v67 offset:swizzle(SWAP,4)
	s_waitcnt lgkmcnt(0)
; DI float wave_sum(float v) { v += shx<1>(v); v += shx<2>(v); v += shx<4>(v); v += shx<8>(v); v += shx<16>(v); v += shx<32>(v); return v; }
; template <int MODE, bool SB  > DI void norm_phase(const Params& P, const Frame& F, int L, const void* src_, const float* gain, bool combine) {
;     ...
;         for (int j = 0; j < 8; ++j) ss += (v[j][0] * v[j][0] + v[j][1] * v[j][1]) + (v[j][2] * v[j][2] + v[j][3] * v[j][3]);
;         const float rstd = 1.0f / sqrtf(wave_sum(ss) * (1.0f / D) + EPS);
; #pragma unroll
;         for (int j = 0; j < 8; ++j) v[j] = v[j] * rstd * g[j];
;         if (MODE == 4) {
; #pragma unroll
;             for (int j = 0; j < 8; ++j) *(f32x4*)(P.out + (size_t)row * D + 4 * F.lane + 256 * j) = v[j];
	v_add_f32_e32 v67, v67, v68
	ds_swizzle_b32 v68, v67 offset:swizzle(SWAP,8)
	s_waitcnt lgkmcnt(0)
	v_add_f32_e32 v67, v67, v68
	v_mov_b32_e32 v68, v67
	s_waitcnt lgkmcnt(0)
	s_nop 1
	v_permlane16_swap_b32_e32 v67, v68
	v_add_f32_e32 v67, v67, v68
	v_mov_b32_e32 v68, v67
	s_waitcnt lgkmcnt(0)
	s_nop 1
	v_permlane32_swap_b32_e32 v67, v68
	v_add_f32_e32 v67, v67, v68
	v_fmamk_f32 v67, v67, 0x3a000000, v65
	v_mul_f32_e32 v68, 0x4f800000, v67
	v_cmp_gt_f32_e32 vcc, s7, v67
	s_nop 1
	v_cndmask_b32_e32 v67, v67, v68, vcc
	v_sqrt_f32_e32 v68, v67
	s_nop 0
	v_add_u32_e32 v69, -1, v68
	v_add_u32_e32 v70, 1, v68
	v_fma_f32 v71, -v69, v68, v67
	v_fma_f32 v72, -v70, v68, v67
	v_cmp_ge_f32_e64 s[2:3], 0, v71
	s_nop 1
	v_cndmask_b32_e64 v68, v68, v69, s[2:3]
	v_cmp_lt_f32_e64 s[2:3], 0, v72
	s_nop 1
	v_cndmask_b32_e64 v68, v68, v70, s[2:3]
	v_mul_f32_e32 v69, 0x37800000, v68
	v_cndmask_b32_e32 v68, v68, v69, vcc
	v_cmp_class_f32_e32 vcc, v67, v66
	s_nop 1
	v_cndmask_b32_e32 v67, v68, v67, vcc
	v_div_scale_f32 v68, s[2:3], v67, v67, 1.0
	v_rcp_f32_e32 v70, v68
	v_div_scale_f32 v69, vcc, 1.0, v67, 1.0
	v_fma_f32 v71, -v68, v70, 1.0
	v_fmac_f32_e32 v70, v71, v70
	v_mul_f32_e32 v71, v69, v70
	v_fma_f32 v72, -v68, v71, v69
	v_fmac_f32_e32 v71, v72, v70
	v_fma_f32 v68, -v68, v71, v69
	v_div_fmas_f32 v68, v68, v70, v71
	v_div_fixup_f32 v68, v68, v67, 1.0
	v_pk_mul_f32 v[70:71], v[92:93], v[68:69] op_sel_hi:[1,0]
	v_pk_mul_f32 v[72:73], v[94:95], v[68:69] op_sel_hi:[1,0]
	v_pk_mul_f32 v[48:49], v[48:49], v[68:69] op_sel_hi:[1,0]
	v_pk_mul_f32 v[50:51], v[50:51], v[68:69] op_sel_hi:[1,0]
	v_pk_mul_f32 v[52:53], v[68:69], v[52:53] op_sel_hi:[0,1]
	v_pk_mul_f32 v[54:55], v[54:55], v[68:69] op_sel_hi:[1,0]
	v_pk_mul_f32 v[90:91], v[40:41], v[68:69] op_sel_hi:[1,0]
	v_pk_mul_f32 v[92:93], v[46:47], v[68:69] op_sel_hi:[1,0]
	v_pk_mul_f32 v[94:95], v[68:69], v[98:99] op_sel_hi:[0,1]
	v_pk_mul_f32 v[56:57], v[68:69], v[56:57] op_sel_hi:[0,1]
	v_pk_mul_f32 v[74:75], v[68:69], v[96:97] op_sel_hi:[0,1]
	v_pk_mul_f32 v[88:89], v[42:43], v[68:69] op_sel_hi:[1,0]
	v_pk_mul_f32 v[96:97], v[38:39], v[68:69] op_sel_hi:[1,0]
	v_pk_mul_f32 v[98:99], v[58:59], v[68:69] op_sel_hi:[1,0]
	v_pk_mul_f32 v[100:101], v[36:37], v[68:69] op_sel_hi:[1,0]
	v_pk_mul_f32 v[102:103], v[44:45], v[68:69] op_sel_hi:[1,0]
	v_pk_mul_f32 v[38:39], v[2:3], v[72:73]
	v_pk_mul_f32 v[36:37], v[0:1], v[70:71]
	v_pk_mul_f32 v[42:43], v[6:7], v[50:51]
	v_pk_mul_f32 v[40:41], v[4:5], v[48:49]
	v_pk_mul_f32 v[46:47], v[10:11], v[52:53]
	v_pk_mul_f32 v[50:51], v[14:15], v[54:55]
	v_pk_mul_f32 v[54:55], v[18:19], v[92:93]
	v_pk_mul_f32 v[52:53], v[16:17], v[90:91]
	v_pk_mul_f32 v[58:59], v[22:23], v[56:57]
	v_pk_mul_f32 v[56:57], v[20:21], v[94:95]
	v_pk_mul_f32 v[44:45], v[8:9], v[74:75]
	v_pk_mul_f32 v[48:49], v[12:13], v[88:89]
	v_pk_mul_f32 v[70:71], v[26:27], v[98:99]
	v_pk_mul_f32 v[68:69], v[24:25], v[96:97]
	v_pk_mul_f32 v[74:75], v[30:31], v[102:103]
	v_pk_mul_f32 v[72:73], v[28:29], v[100:101]
	global_store_dwordx4 v[34:35], v[36:39], off offset:-4096
	global_store_dwordx4 v[34:35], v[40:43], off offset:-3072
	global_store_dwordx4 v[34:35], v[44:47], off offset:-2048
	global_store_dwordx4 v[34:35], v[48:51], off offset:-1024
	global_store_dwordx4 v[34:35], v[52:55], off
	global_store_dwordx4 v[34:35], v[56:59], off offset:1024
	global_store_dwordx4 v[34:35], v[68:71], off offset:2048
	global_store_dwordx4 v[34:35], v[72:75], off offset:3072
	v_lshl_add_u64 v[34:35], v[34:35], 0, s[0:1]
	s_waitcnt vmcnt(9)
	v_mov_b64_e32 v[36:37], v[86:87]
	v_mov_b64_e32 v[56:57], v[84:85]
	v_mov_b64_e32 v[40:41], v[82:83]
	v_mov_b64_e32 v[52:53], v[80:81]
	v_mov_b64_e32 v[54:55], v[78:79]
	v_mov_b64_e32 v[58:59], v[76:77]
	s_mov_b64 vcc, s[4:5]
	s_cbranch_vccnz .LBB0_3407
